# GEMM2 epilogue: all 32 residual loads of a lane issued up front; GEMM3 routing tail: result stores staged in LDS and written after the last dependent gather
# speedup vs baseline: 1.0025x; 1.0025x over previous
;     __device__ __forceinline__ void fused(f32x4 (&acc)[2][2][4][2], const Unit& u, int wr, int wc, int fr, int fq, PG8_LAS unsigned char* lds, int wid, int lane) const {
;     ...
;             for (int m = 0; m < 4; ++m) { const int r = ai * HALF + wr * 64 + m * 16 + fr; const size_t off = (size_t)(u.pm * BM + r) * ldc + col0;
; #pragma unroll
;                 for (int bj = 0; bj < 2; ++bj)
; #pragma unroll
;                     for (int n = 0; n < 2; ++n) { const u32x2v bw = __builtin_nontemporal_load((const u32x2v*)(base + off + bj * HALF + n * 16));
;                         const f32x4 bs = (f32x4){__uint_as_float(bw.x << 16), __uint_as_float(bw.x & 0xffff0000u), __uint_as_float(bw.y << 16), __uint_as_float(bw.y & 0xffff0000u)}; acc[ai][bj][m][n] = bs * alpha + acc[ai][bj][m][n]; }
;                 asm volatile("" : "+v"(acc[ai][0][m][0]), "+v"(acc[ai][0][m][1]), "+v"(acc[ai][1][m][0]), "+v"(acc[ai][1][m][1]));
;                 if (m == 3) asm volatile("" ::: "memory"); }
.LBB0_452:
	s_add_u32 s6, s10, 0x2000000
	s_addc_u32 s7, s11, 0
	v_bfe_u32 v167, v144, 4, 2
	s_lshl_b32 s29, s16, 8
	v_lshlrev_b32_e32 v128, 2, v167
	s_add_i32 s4, s29, s57
	s_lshl_b32 s28, s8, 8
	v_lshl_or_b32 v163, s17, 5, v128
	v_or_b32_e32 v130, s4, v145
	v_or_b32_e32 v128, s28, v163
	v_ashrrev_i32_e32 v131, 31, v130
	v_ashrrev_i32_e32 v129, 31, v128
	v_lshlrev_b64 v[132:133], 11, v[130:131]
	v_lshl_add_u64 v[134:135], s[6:7], 0, v[132:133]
	v_lshlrev_b64 v[132:133], 1, v[128:129]
	v_lshl_add_u64 v[134:135], v[134:135], 0, v[132:133]
	s_barrier
	global_load_dwordx2 v[170:171], v[134:135], off nt
	global_load_dwordx2 v[172:173], v[134:135], off offset:32 nt
	global_load_dwordx2 v[174:175], v[134:135], off offset:256 nt
	global_load_dwordx2 v[176:177], v[134:135], off offset:288 nt
	v_add_u32_e32 v234, 0x10, v130
	v_mov_b32_e32 v235, 0
	v_lshlrev_b64 v[234:235], 11, v[234:235]
	v_lshl_add_u64 v[234:235], s[6:7], 0, v[234:235]
	v_lshl_add_u64 v[234:235], v[234:235], 0, v[132:133]
	s_nop 1
	global_load_dwordx2 v[178:179], v[234:235], off nt
	global_load_dwordx2 v[180:181], v[234:235], off offset:32 nt
	global_load_dwordx2 v[182:183], v[234:235], off offset:256 nt
	global_load_dwordx2 v[184:185], v[234:235], off offset:288 nt
	v_add_u32_e32 v234, 0x20, v130
	v_mov_b32_e32 v235, 0
	v_lshlrev_b64 v[234:235], 11, v[234:235]
	v_lshl_add_u64 v[234:235], s[6:7], 0, v[234:235]
	v_lshl_add_u64 v[234:235], v[234:235], 0, v[132:133]
	s_nop 1
	global_load_dwordx2 v[186:187], v[234:235], off nt
	global_load_dwordx2 v[188:189], v[234:235], off offset:32 nt
	global_load_dwordx2 v[190:191], v[234:235], off offset:256 nt
	global_load_dwordx2 v[192:193], v[234:235], off offset:288 nt
	v_add_u32_e32 v234, 0x30, v130
	v_mov_b32_e32 v235, 0
	v_lshlrev_b64 v[234:235], 11, v[234:235]
	v_lshl_add_u64 v[234:235], s[6:7], 0, v[234:235]
	v_lshl_add_u64 v[234:235], v[234:235], 0, v[132:133]
	s_nop 1
	global_load_dwordx2 v[194:195], v[234:235], off nt
	global_load_dwordx2 v[196:197], v[234:235], off offset:32 nt
	global_load_dwordx2 v[198:199], v[234:235], off offset:256 nt
	global_load_dwordx2 v[200:201], v[234:235], off offset:288 nt
	v_add_u32_e32 v234, 0x80, v130
	v_mov_b32_e32 v235, 0
	v_lshlrev_b64 v[234:235], 11, v[234:235]
	v_lshl_add_u64 v[234:235], s[6:7], 0, v[234:235]
	v_lshl_add_u64 v[234:235], v[234:235], 0, v[132:133]
	s_nop 1
	global_load_dwordx2 v[202:203], v[234:235], off nt
	global_load_dwordx2 v[204:205], v[234:235], off offset:32 nt
	global_load_dwordx2 v[206:207], v[234:235], off offset:256 nt
	global_load_dwordx2 v[208:209], v[234:235], off offset:288 nt
	v_add_u32_e32 v234, 0x90, v130
	v_mov_b32_e32 v235, 0
	v_lshlrev_b64 v[234:235], 11, v[234:235]
	v_lshl_add_u64 v[234:235], s[6:7], 0, v[234:235]
	v_lshl_add_u64 v[234:235], v[234:235], 0, v[132:133]
	s_nop 1
	global_load_dwordx2 v[210:211], v[234:235], off nt
	global_load_dwordx2 v[212:213], v[234:235], off offset:32 nt
	global_load_dwordx2 v[214:215], v[234:235], off offset:256 nt
	global_load_dwordx2 v[216:217], v[234:235], off offset:288 nt
	v_add_u32_e32 v234, 0xa0, v130
	v_mov_b32_e32 v235, 0
	v_lshlrev_b64 v[234:235], 11, v[234:235]
	v_lshl_add_u64 v[234:235], s[6:7], 0, v[234:235]
	v_lshl_add_u64 v[234:235], v[234:235], 0, v[132:133]
	s_nop 1
	global_load_dwordx2 v[218:219], v[234:235], off nt
	global_load_dwordx2 v[220:221], v[234:235], off offset:32 nt
	global_load_dwordx2 v[222:223], v[234:235], off offset:256 nt
	global_load_dwordx2 v[224:225], v[234:235], off offset:288 nt
	v_add_u32_e32 v234, 0xb0, v130
	v_mov_b32_e32 v235, 0
	v_lshlrev_b64 v[234:235], 11, v[234:235]
	v_lshl_add_u64 v[234:235], s[6:7], 0, v[234:235]
	v_lshl_add_u64 v[234:235], v[234:235], 0, v[132:133]
	s_nop 1
	global_load_dwordx2 v[226:227], v[234:235], off nt
	global_load_dwordx2 v[228:229], v[234:235], off offset:32 nt
	global_load_dwordx2 v[230:231], v[234:235], off offset:256 nt
	global_load_dwordx2 v[232:233], v[234:235], off offset:288 nt
	s_nop 0
	v_or_b32_e32 v142, 16, v130
	v_ashrrev_i32_e32 v143, 31, v142
	v_lshlrev_b64 v[142:143], 11, v[142:143]
	s_mov_b32 s4, 0x3fb504f3
	v_lshl_add_u64 v[142:143], s[6:7], 0, v[142:143]
	v_lshl_add_u64 v[142:143], v[142:143], 0, v[132:133]
	v_xor_b32_e32 v131, 16, v165
	v_and_b32_e32 v168, 63, v144
	s_waitcnt vmcnt(28)
	v_mov_b32_e32 v136, v170
	v_mov_b32_e32 v137, v171
	v_mov_b32_e32 v138, v172
	v_mov_b32_e32 v139, v173
	v_mov_b32_e32 v140, v174
	v_mov_b32_e32 v141, v175
	v_mov_b32_e32 v134, v176
	v_mov_b32_e32 v135, v177
	v_lshlrev_b32_e32 v146, 16, v136
	v_and_b32_e32 v147, 0xffff0000, v136
	v_lshlrev_b32_e32 v136, 16, v137
	v_and_b32_e32 v137, 0xffff0000, v137
	v_lshlrev_b32_e32 v148, 16, v138
	v_and_b32_e32 v149, 0xffff0000, v138
	v_lshlrev_b32_e32 v138, 16, v139
	v_and_b32_e32 v139, 0xffff0000, v139
	v_lshlrev_b32_e32 v150, 16, v140
	v_and_b32_e32 v151, 0xffff0000, v140
	v_lshlrev_b32_e32 v140, 16, v141
	v_and_b32_e32 v141, 0xffff0000, v141
	v_lshlrev_b32_e32 v154, 16, v134
	v_and_b32_e32 v155, 0xffff0000, v134
	v_lshlrev_b32_e32 v134, 16, v135
	v_and_b32_e32 v135, 0xffff0000, v135
	v_pk_fma_f32 v[126:127], v[136:137], s[4:5], v[126:127] op_sel_hi:[1,0,1]
	v_pk_fma_f32 v[124:125], v[146:147], s[4:5], v[124:125] op_sel_hi:[1,0,1]
	v_pk_fma_f32 v[122:123], v[138:139], s[4:5], v[122:123] op_sel_hi:[1,0,1]
	v_pk_fma_f32 v[120:121], v[148:149], s[4:5], v[120:121] op_sel_hi:[1,0,1]
	v_pk_fma_f32 v[118:119], v[140:141], s[4:5], v[118:119] op_sel_hi:[1,0,1]
	v_pk_fma_f32 v[116:117], v[150:151], s[4:5], v[116:117] op_sel_hi:[1,0,1]
	v_pk_fma_f32 v[102:103], v[134:135], s[4:5], v[102:103] op_sel_hi:[1,0,1]
	v_pk_fma_f32 v[100:101], v[154:155], s[4:5], v[100:101] op_sel_hi:[1,0,1]
	s_nop 0
	v_or_b32_e32 v142, 32, v130
	v_ashrrev_i32_e32 v143, 31, v142
	v_lshlrev_b64 v[142:143], 11, v[142:143]
	v_lshl_add_u64 v[142:143], s[6:7], 0, v[142:143]
	v_lshl_add_u64 v[142:143], v[142:143], 0, v[132:133]
	s_waitcnt vmcnt(24)
;     __device__ __forceinline__ void fused(f32x4 (&acc)[2][2][4][2], const Unit& u, int wr, int wc, int fr, int fq, PG8_LAS unsigned char* lds, int wid, int lane) const {
;     ...
;             for (int m = 0; m < 4; ++m) { const int r = ai * HALF + wr * 64 + m * 16 + fr; const size_t off = (size_t)(u.pm * BM + r) * ldc + col0;
; #pragma unroll
;                 for (int bj = 0; bj < 2; ++bj)
; #pragma unroll
;                     for (int n = 0; n < 2; ++n) { const u32x2v bw = __builtin_nontemporal_load((const u32x2v*)(base + off + bj * HALF + n * 16));
;                         const f32x4 bs = (f32x4){__uint_as_float(bw.x << 16), __uint_as_float(bw.x & 0xffff0000u), __uint_as_float(bw.y << 16), __uint_as_float(bw.y & 0xffff0000u)}; acc[ai][bj][m][n] = bs * alpha + acc[ai][bj][m][n]; }
	v_mov_b32_e32 v134, v178
	v_mov_b32_e32 v135, v179
	v_mov_b32_e32 v136, v180
	v_mov_b32_e32 v137, v181
	v_mov_b32_e32 v138, v182
	v_mov_b32_e32 v139, v183
	v_mov_b32_e32 v140, v184
	v_mov_b32_e32 v141, v185
	v_lshlrev_b32_e32 v146, 16, v134
	v_and_b32_e32 v147, 0xffff0000, v134
	v_lshlrev_b32_e32 v134, 16, v135
	v_and_b32_e32 v135, 0xffff0000, v135
	v_lshlrev_b32_e32 v148, 16, v136
	v_and_b32_e32 v149, 0xffff0000, v136
	v_lshlrev_b32_e32 v136, 16, v137
	v_and_b32_e32 v137, 0xffff0000, v137
	v_lshlrev_b32_e32 v150, 16, v138
	v_and_b32_e32 v151, 0xffff0000, v138
	v_lshlrev_b32_e32 v138, 16, v139
	v_and_b32_e32 v139, 0xffff0000, v139
	v_lshlrev_b32_e32 v154, 16, v140
	v_and_b32_e32 v155, 0xffff0000, v140
	v_lshlrev_b32_e32 v140, 16, v141
	v_and_b32_e32 v141, 0xffff0000, v141
	v_pk_fma_f32 v[114:115], v[134:135], s[4:5], v[114:115] op_sel_hi:[1,0,1]
	v_pk_fma_f32 v[112:113], v[146:147], s[4:5], v[112:113] op_sel_hi:[1,0,1]
	v_pk_fma_f32 v[106:107], v[136:137], s[4:5], v[106:107] op_sel_hi:[1,0,1]
	v_pk_fma_f32 v[104:105], v[148:149], s[4:5], v[104:105] op_sel_hi:[1,0,1]
	v_pk_fma_f32 v[90:91], v[138:139], s[4:5], v[90:91] op_sel_hi:[1,0,1]
	v_pk_fma_f32 v[88:89], v[150:151], s[4:5], v[88:89] op_sel_hi:[1,0,1]
	v_pk_fma_f32 v[78:79], v[140:141], s[4:5], v[78:79] op_sel_hi:[1,0,1]
	v_pk_fma_f32 v[76:77], v[154:155], s[4:5], v[76:77] op_sel_hi:[1,0,1]
	s_nop 0
	v_or_b32_e32 v142, 48, v130
	v_ashrrev_i32_e32 v143, 31, v142
	v_lshlrev_b64 v[142:143], 11, v[142:143]
	v_lshl_add_u64 v[142:143], s[6:7], 0, v[142:143]
	v_lshl_add_u64 v[142:143], v[142:143], 0, v[132:133]
	s_waitcnt vmcnt(20)
	v_mov_b32_e32 v134, v186
	v_mov_b32_e32 v135, v187
	v_mov_b32_e32 v136, v188
	v_mov_b32_e32 v137, v189
	v_mov_b32_e32 v138, v190
	v_mov_b32_e32 v139, v191
	v_mov_b32_e32 v140, v192
	v_mov_b32_e32 v141, v193
	v_lshlrev_b32_e32 v146, 16, v134
	v_and_b32_e32 v147, 0xffff0000, v134
	v_lshlrev_b32_e32 v134, 16, v135
	v_and_b32_e32 v135, 0xffff0000, v135
	v_lshlrev_b32_e32 v148, 16, v136
	v_and_b32_e32 v149, 0xffff0000, v136
	v_lshlrev_b32_e32 v136, 16, v137
	v_and_b32_e32 v137, 0xffff0000, v137
	v_lshlrev_b32_e32 v150, 16, v138
	v_and_b32_e32 v151, 0xffff0000, v138
	v_lshlrev_b32_e32 v138, 16, v139
	v_and_b32_e32 v139, 0xffff0000, v139
	v_lshlrev_b32_e32 v154, 16, v140
	v_and_b32_e32 v155, 0xffff0000, v140
	v_lshlrev_b32_e32 v140, 16, v141
	v_and_b32_e32 v141, 0xffff0000, v141
	v_pk_fma_f32 v[110:111], v[134:135], s[4:5], v[110:111] op_sel_hi:[1,0,1]
	v_pk_fma_f32 v[108:109], v[146:147], s[4:5], v[108:109] op_sel_hi:[1,0,1]
	v_pk_fma_f32 v[94:95], v[136:137], s[4:5], v[94:95] op_sel_hi:[1,0,1]
	v_pk_fma_f32 v[92:93], v[148:149], s[4:5], v[92:93] op_sel_hi:[1,0,1]
	v_pk_fma_f32 v[82:83], v[138:139], s[4:5], v[82:83] op_sel_hi:[1,0,1]
	v_pk_fma_f32 v[80:81], v[150:151], s[4:5], v[80:81] op_sel_hi:[1,0,1]
	v_pk_fma_f32 v[70:71], v[140:141], s[4:5], v[70:71] op_sel_hi:[1,0,1]
	v_pk_fma_f32 v[68:69], v[154:155], s[4:5], v[68:69] op_sel_hi:[1,0,1]
	s_nop 0
	v_add_u32_e32 v142, 0x80, v130
	v_ashrrev_i32_e32 v143, 31, v142
	v_lshlrev_b64 v[142:143], 11, v[142:143]
	v_lshl_add_u64 v[142:143], s[6:7], 0, v[142:143]
	v_lshl_add_u64 v[142:143], v[142:143], 0, v[132:133]
	s_waitcnt vmcnt(16)
	v_mov_b32_e32 v134, v194
	v_mov_b32_e32 v135, v195
	v_mov_b32_e32 v136, v196
	v_mov_b32_e32 v137, v197
	v_mov_b32_e32 v138, v198
	v_mov_b32_e32 v139, v199
	v_mov_b32_e32 v140, v200
	v_mov_b32_e32 v141, v201
	v_lshlrev_b32_e32 v146, 16, v134
	v_and_b32_e32 v147, 0xffff0000, v134
	v_lshlrev_b32_e32 v134, 16, v135
	v_and_b32_e32 v135, 0xffff0000, v135
	v_lshlrev_b32_e32 v148, 16, v136
	v_and_b32_e32 v149, 0xffff0000, v136
	v_lshlrev_b32_e32 v136, 16, v137
	v_and_b32_e32 v137, 0xffff0000, v137
	v_lshlrev_b32_e32 v150, 16, v138
	v_and_b32_e32 v151, 0xffff0000, v138
	v_lshlrev_b32_e32 v138, 16, v139
	v_and_b32_e32 v139, 0xffff0000, v139
	v_lshlrev_b32_e32 v154, 16, v140
	v_and_b32_e32 v155, 0xffff0000, v140
	v_lshlrev_b32_e32 v140, 16, v141
	v_and_b32_e32 v141, 0xffff0000, v141
	v_pk_fma_f32 v[98:99], v[134:135], s[4:5], v[98:99] op_sel_hi:[1,0,1]
	v_pk_fma_f32 v[96:97], v[146:147], s[4:5], v[96:97] op_sel_hi:[1,0,1]
	v_pk_fma_f32 v[86:87], v[136:137], s[4:5], v[86:87] op_sel_hi:[1,0,1]
	v_pk_fma_f32 v[84:85], v[148:149], s[4:5], v[84:85] op_sel_hi:[1,0,1]
	v_pk_fma_f32 v[74:75], v[138:139], s[4:5], v[74:75] op_sel_hi:[1,0,1]
	v_pk_fma_f32 v[72:73], v[150:151], s[4:5], v[72:73] op_sel_hi:[1,0,1]
	v_pk_fma_f32 v[66:67], v[140:141], s[4:5], v[66:67] op_sel_hi:[1,0,1]
	v_pk_fma_f32 v[64:65], v[154:155], s[4:5], v[64:65] op_sel_hi:[1,0,1]
	s_nop 0
	v_add_u32_e32 v142, 0x90, v130
	v_ashrrev_i32_e32 v143, 31, v142
	v_lshlrev_b64 v[142:143], 11, v[142:143]
	v_lshl_add_u64 v[142:143], s[6:7], 0, v[142:143]
	v_lshl_add_u64 v[142:143], v[142:143], 0, v[132:133]
	s_waitcnt vmcnt(12)
	v_mov_b32_e32 v134, v202
	v_mov_b32_e32 v135, v203
	v_mov_b32_e32 v136, v204
	v_mov_b32_e32 v137, v205
	v_mov_b32_e32 v138, v206
	v_mov_b32_e32 v139, v207
	v_mov_b32_e32 v140, v208
	v_mov_b32_e32 v141, v209
	v_lshlrev_b32_e32 v146, 16, v134
	v_and_b32_e32 v147, 0xffff0000, v134
	v_lshlrev_b32_e32 v134, 16, v135
	v_and_b32_e32 v135, 0xffff0000, v135
	v_lshlrev_b32_e32 v148, 16, v136
	v_and_b32_e32 v149, 0xffff0000, v136
	v_lshlrev_b32_e32 v136, 16, v137
	v_and_b32_e32 v137, 0xffff0000, v137
	v_lshlrev_b32_e32 v150, 16, v138
	v_and_b32_e32 v151, 0xffff0000, v138
	v_lshlrev_b32_e32 v138, 16, v139
	v_and_b32_e32 v139, 0xffff0000, v139
	v_lshlrev_b32_e32 v154, 16, v140
	v_and_b32_e32 v155, 0xffff0000, v140
	v_lshlrev_b32_e32 v140, 16, v141
	v_and_b32_e32 v141, 0xffff0000, v141
	v_pk_fma_f32 v[62:63], v[134:135], s[4:5], v[62:63] op_sel_hi:[1,0,1]
	v_pk_fma_f32 v[60:61], v[146:147], s[4:5], v[60:61] op_sel_hi:[1,0,1]
	v_pk_fma_f32 v[54:55], v[136:137], s[4:5], v[54:55] op_sel_hi:[1,0,1]
	v_pk_fma_f32 v[52:53], v[148:149], s[4:5], v[52:53] op_sel_hi:[1,0,1]
	v_pk_fma_f32 v[46:47], v[138:139], s[4:5], v[46:47] op_sel_hi:[1,0,1]
	v_pk_fma_f32 v[44:45], v[150:151], s[4:5], v[44:45] op_sel_hi:[1,0,1]
	v_pk_fma_f32 v[38:39], v[140:141], s[4:5], v[38:39] op_sel_hi:[1,0,1]
	v_pk_fma_f32 v[36:37], v[154:155], s[4:5], v[36:37] op_sel_hi:[1,0,1]
	s_nop 0
	v_add_u32_e32 v142, 0xa0, v130
	v_ashrrev_i32_e32 v143, 31, v142
	v_lshlrev_b64 v[142:143], 11, v[142:143]
	v_lshl_add_u64 v[142:143], s[6:7], 0, v[142:143]
	v_lshl_add_u64 v[142:143], v[142:143], 0, v[132:133]
	s_waitcnt vmcnt(8)
;     __device__ __forceinline__ bool run(const f32x4 (&v)[2][2][4][2], const Unit& u, int wr, int wc, int fr, int fq, PG8_LAS unsigned char* lds, int wid, int lane) const {
;     ...
;                     for (int n = 0; n < 2; ++n) { const f32x4 x = v[ai][bj][m][n]; s += (x[0] + x[1]) + (x[2] + x[3]); }
;                 s += __shfl_xor(s, 16); s += __shfl_xor(s, 32);
;     __device__ __forceinline__ void fused(f32x4 (&acc)[2][2][4][2], const Unit& u, int wr, int wc, int fr, int fq, PG8_LAS unsigned char* lds, int wid, int lane) const {
;     ...
;             for (int m = 0; m < 4; ++m) { const int r = ai * HALF + wr * 64 + m * 16 + fr; const size_t off = (size_t)(u.pm * BM + r) * ldc + col0;
; #pragma unroll
;                 for (int bj = 0; bj < 2; ++bj)
; #pragma unroll
;                     for (int n = 0; n < 2; ++n) { const u32x2v bw = __builtin_nontemporal_load((const u32x2v*)(base + off + bj * HALF + n * 16));
;                         const f32x4 bs = (f32x4){__uint_as_float(bw.x << 16), __uint_as_float(bw.x & 0xffff0000u), __uint_as_float(bw.y << 16), __uint_as_float(bw.y & 0xffff0000u)}; acc[ai][bj][m][n] = bs * alpha + acc[ai][bj][m][n]; }
	v_mov_b32_e32 v134, v210
	v_mov_b32_e32 v135, v211
	v_mov_b32_e32 v136, v212
	v_mov_b32_e32 v137, v213
	v_mov_b32_e32 v138, v214
	v_mov_b32_e32 v139, v215
	v_mov_b32_e32 v140, v216
	v_mov_b32_e32 v141, v217
	v_lshlrev_b32_e32 v146, 16, v134
	v_and_b32_e32 v147, 0xffff0000, v134
	v_lshlrev_b32_e32 v134, 16, v135
	v_and_b32_e32 v135, 0xffff0000, v135
	v_lshlrev_b32_e32 v148, 16, v136
	v_and_b32_e32 v149, 0xffff0000, v136
	v_lshlrev_b32_e32 v136, 16, v137
	v_and_b32_e32 v137, 0xffff0000, v137
	v_lshlrev_b32_e32 v150, 16, v138
	v_and_b32_e32 v151, 0xffff0000, v138
	v_lshlrev_b32_e32 v138, 16, v139
	v_and_b32_e32 v139, 0xffff0000, v139
	v_lshlrev_b32_e32 v154, 16, v140
	v_and_b32_e32 v155, 0xffff0000, v140
	v_lshlrev_b32_e32 v140, 16, v141
	v_and_b32_e32 v141, 0xffff0000, v141
	v_pk_fma_f32 v[58:59], v[134:135], s[4:5], v[58:59] op_sel_hi:[1,0,1]
	v_pk_fma_f32 v[56:57], v[146:147], s[4:5], v[56:57] op_sel_hi:[1,0,1]
	v_pk_fma_f32 v[50:51], v[136:137], s[4:5], v[50:51] op_sel_hi:[1,0,1]
	v_pk_fma_f32 v[48:49], v[148:149], s[4:5], v[48:49] op_sel_hi:[1,0,1]
	v_pk_fma_f32 v[42:43], v[138:139], s[4:5], v[42:43] op_sel_hi:[1,0,1]
	v_pk_fma_f32 v[40:41], v[150:151], s[4:5], v[40:41] op_sel_hi:[1,0,1]
	v_pk_fma_f32 v[34:35], v[140:141], s[4:5], v[34:35] op_sel_hi:[1,0,1]
	v_pk_fma_f32 v[32:33], v[154:155], s[4:5], v[32:33] op_sel_hi:[1,0,1]
	v_mov_b32_e32 v146, v124
	v_and_b32_e32 v142, 64, v165
	v_add_u32_e32 v153, 64, v142
	v_add_u32_e32 v142, 0xb0, v130
	v_ashrrev_i32_e32 v143, 31, v142
	v_lshlrev_b64 v[142:143], 11, v[142:143]
	v_lshl_add_u64 v[142:143], s[6:7], 0, v[142:143]
	v_lshl_add_u64 v[132:133], v[142:143], 0, v[132:133]
	v_mov_b32_e32 v142, v125
	v_mov_b32_e32 v143, v126
	v_mov_b32_e32 v147, v127
	v_pk_add_f32 v[142:143], v[142:143], v[146:147]
	v_mov_b32_e32 v148, v121
	v_mov_b32_e32 v149, v122
	v_add_f32_e32 v130, v142, v143
	v_cmp_lt_i32_e32 vcc, v131, v153
	s_waitcnt vmcnt(4)
	v_mov_b32_e32 v134, v218
	v_mov_b32_e32 v135, v219
	v_mov_b32_e32 v136, v220
	v_mov_b32_e32 v137, v221
	v_mov_b32_e32 v138, v222
	v_mov_b32_e32 v139, v223
	v_mov_b32_e32 v140, v224
	v_mov_b32_e32 v141, v225
	v_lshlrev_b32_e32 v150, 16, v134
	v_and_b32_e32 v151, 0xffff0000, v134
	v_lshlrev_b32_e32 v134, 16, v135
	v_and_b32_e32 v135, 0xffff0000, v135
	v_lshlrev_b32_e32 v154, 16, v136
	v_and_b32_e32 v155, 0xffff0000, v136
	v_lshlrev_b32_e32 v136, 16, v137
	v_and_b32_e32 v137, 0xffff0000, v137
	v_lshlrev_b32_e32 v156, 16, v138
	v_and_b32_e32 v157, 0xffff0000, v138
	v_lshlrev_b32_e32 v138, 16, v139
	v_and_b32_e32 v139, 0xffff0000, v139
	v_lshlrev_b32_e32 v158, 16, v140
	v_and_b32_e32 v159, 0xffff0000, v140
	v_lshlrev_b32_e32 v140, 16, v141
	v_and_b32_e32 v141, 0xffff0000, v141
	v_pk_fma_f32 v[30:31], v[134:135], s[4:5], v[30:31] op_sel_hi:[1,0,1]
	v_pk_fma_f32 v[28:29], v[150:151], s[4:5], v[28:29] op_sel_hi:[1,0,1]
	v_pk_fma_f32 v[26:27], v[136:137], s[4:5], v[26:27] op_sel_hi:[1,0,1]
	v_pk_fma_f32 v[24:25], v[154:155], s[4:5], v[24:25] op_sel_hi:[1,0,1]
	v_pk_fma_f32 v[22:23], v[138:139], s[4:5], v[22:23] op_sel_hi:[1,0,1]
	v_pk_fma_f32 v[20:21], v[156:157], s[4:5], v[20:21] op_sel_hi:[1,0,1]
	v_pk_fma_f32 v[18:19], v[140:141], s[4:5], v[18:19] op_sel_hi:[1,0,1]
	v_pk_fma_f32 v[16:17], v[158:159], s[4:5], v[16:17] op_sel_hi:[1,0,1]
	v_mov_b32_e32 v134, v120
	v_mov_b32_e32 v135, v123
	v_pk_add_f32 v[132:133], v[148:149], v[134:135]
	v_add_f32_e32 v141, v116, v117
	v_pk_add_f32 v[132:133], v[132:133], v[132:133] op_sel_hi:[0,1]
	v_add_f32_e32 v151, v118, v119
	v_mov_b32_e32 v140, v100
	v_mov_b32_e32 v150, v101
	v_mov_b32_e32 v156, v103
	v_add_f32_e32 v157, 0, v130
	v_mov_b32_e32 v132, v102
	v_pk_add_f32 v[134:135], v[140:141], v[150:151]
	v_pk_add_f32 v[132:133], v[132:133], v[156:157]
	v_cndmask_b32_e32 v131, v165, v131, vcc
	v_pk_add_f32 v[132:133], v[134:135], v[132:133]
	v_lshlrev_b32_e32 v131, 2, v131
	v_add_f32_e32 v132, v132, v133
	ds_bpermute_b32 v133, v131, v132
	v_xor_b32_e32 v130, 32, v165
	v_cmp_lt_i32_e32 vcc, v130, v153
	s_waitcnt lgkmcnt(0)
;     __device__ __forceinline__ bool run(const f32x4 (&v)[2][2][4][2], const Unit& u, int wr, int wc, int fr, int fq, PG8_LAS unsigned char* lds, int wid, int lane) const {
;     ...
;                     for (int n = 0; n < 2; ++n) { const f32x4 x = v[ai][bj][m][n]; s += (x[0] + x[1]) + (x[2] + x[3]); }
;                 s += __shfl_xor(s, 16); s += __shfl_xor(s, 32);
;                 const float mw = s * (1.0f / 64.0f); float q = 0.f;
; #pragma unroll
;                 for (int bj = 0; bj < 2; ++bj)
; #pragma unroll
;                     for (int n = 0; n < 2; ++n) { const f32x4 d = v[ai][bj][m][n] - mw; q += (d[0] * d[0] + d[1] * d[1]) + (d[2] * d[2] + d[3] * d[3]); }
;                 q += __shfl_xor(q, 16); q += __shfl_xor(q, 32);
;                 if (fq == 0) P[(ai * HALF + wr * 64 + m * 16 + fr) * 4 + wc] = (f32x2v){mw, q};
;     __device__ __forceinline__ void fused(f32x4 (&acc)[2][2][4][2], const Unit& u, int wr, int wc, int fr, int fq, PG8_LAS unsigned char* lds, int wid, int lane) const {
;     ...
;             for (int m = 0; m < 4; ++m) { const int r = ai * HALF + wr * 64 + m * 16 + fr; const size_t off = (size_t)(u.pm * BM + r) * ldc + col0;
; #pragma unroll
;                 for (int bj = 0; bj < 2; ++bj)
; #pragma unroll
;                     for (int n = 0; n < 2; ++n) { const u32x2v bw = __builtin_nontemporal_load((const u32x2v*)(base + off + bj * HALF + n * 16));
;                         const f32x4 bs = (f32x4){__uint_as_float(bw.x << 16), __uint_as_float(bw.x & 0xffff0000u), __uint_as_float(bw.y << 16), __uint_as_float(bw.y & 0xffff0000u)}; acc[ai][bj][m][n] = bs * alpha + acc[ai][bj][m][n]; }
;                 asm volatile("" : "+v"(acc[ai][0][m][0]), "+v"(acc[ai][0][m][1]), "+v"(acc[ai][1][m][0]), "+v"(acc[ai][1][m][1]));
;                 if (m == 3) asm volatile("" ::: "memory"); }
	v_add_f32_e32 v132, v132, v133
	v_cndmask_b32_e32 v130, v165, v130, vcc
	v_lshlrev_b32_e32 v130, 2, v130
	ds_bpermute_b32 v133, v130, v132
	v_cmp_gt_u32_e32 vcc, 16, v168
	s_waitcnt lgkmcnt(0)
	v_add_f32_e32 v132, v132, v133
	v_fmamk_f32 v134, v132, 0xbc800000, v127
	v_fmamk_f32 v140, v132, 0xbc800000, v125
	v_fmamk_f32 v142, v132, 0xbc800000, v123
	v_fmamk_f32 v148, v132, 0xbc800000, v121
	v_fmamk_f32 v133, v132, 0xbc800000, v126
	v_fmamk_f32 v135, v132, 0xbc800000, v124
	v_fmamk_f32 v141, v132, 0xbc800000, v122
	v_fmamk_f32 v143, v132, 0xbc800000, v120
	v_fmamk_f32 v150, v132, 0xbc800000, v119
	v_fmamk_f32 v153, v132, 0xbc800000, v117
	v_mul_f32_e32 v140, v140, v140
	v_mul_f32_e32 v134, v134, v134
	v_mul_f32_e32 v148, v148, v148
	v_mul_f32_e32 v142, v142, v142
	v_fmamk_f32 v149, v132, 0xbc800000, v118
	v_fmamk_f32 v151, v132, 0xbc800000, v116
	v_fmamk_f32 v157, v132, 0xbc800000, v103
	v_fmamk_f32 v159, v132, 0xbc800000, v101
	v_mul_f32_e32 v153, v153, v153
	v_mul_f32_e32 v150, v150, v150
	v_fmac_f32_e32 v140, v135, v135
	v_fmac_f32_e32 v134, v133, v133
	v_fmac_f32_e32 v148, v143, v143
	v_fmac_f32_e32 v142, v141, v141
	v_fmamk_f32 v156, v132, 0xbc800000, v102
	v_fmamk_f32 v158, v132, 0xbc800000, v100
	v_mul_f32_e32 v159, v159, v159
	v_mul_f32_e32 v157, v157, v157
	v_fmac_f32_e32 v153, v151, v151
	v_fmac_f32_e32 v150, v149, v149
	v_add_f32_e32 v133, v140, v134
	v_add_f32_e32 v134, v148, v142
	v_fmac_f32_e32 v159, v158, v158
	v_fmac_f32_e32 v157, v156, v156
	v_add_f32_e32 v135, v153, v150
	v_add_f32_e32 v133, v133, v134
	v_add_f32_e32 v140, v159, v157
	v_add_f32_e32 v133, v135, v133
	v_add_f32_e32 v133, v140, v133
	ds_bpermute_b32 v134, v131, v133
	s_waitcnt lgkmcnt(0)
	v_add_f32_e32 v133, v133, v134
	ds_bpermute_b32 v134, v130, v133
	s_waitcnt vmcnt(0)
	v_mov_b32_e32 v136, v226
	v_mov_b32_e32 v137, v227
	v_mov_b32_e32 v138, v228
	v_mov_b32_e32 v139, v229
	v_mov_b32_e32 v154, v230
	v_mov_b32_e32 v155, v231
	v_mov_b32_e32 v146, v232
	v_mov_b32_e32 v147, v233
	v_lshlrev_b32_e32 v140, 16, v136
	v_and_b32_e32 v141, 0xffff0000, v136
	v_lshlrev_b32_e32 v136, 16, v137
	v_and_b32_e32 v137, 0xffff0000, v137
	v_lshlrev_b32_e32 v142, 16, v138
	v_and_b32_e32 v143, 0xffff0000, v138
	v_lshlrev_b32_e32 v138, 16, v139
	v_and_b32_e32 v139, 0xffff0000, v139
	v_lshlrev_b32_e32 v148, 16, v154
	v_and_b32_e32 v149, 0xffff0000, v154
	v_lshlrev_b32_e32 v150, 16, v155
	v_and_b32_e32 v151, 0xffff0000, v155
	v_lshlrev_b32_e32 v154, 16, v146
	v_and_b32_e32 v155, 0xffff0000, v146
	v_lshlrev_b32_e32 v146, 16, v147
	v_and_b32_e32 v147, 0xffff0000, v147
	v_pk_fma_f32 v[14:15], v[136:137], s[4:5], v[14:15] op_sel_hi:[1,0,1]
	v_pk_fma_f32 v[12:13], v[140:141], s[4:5], v[12:13] op_sel_hi:[1,0,1]
	v_pk_fma_f32 v[10:11], v[138:139], s[4:5], v[10:11] op_sel_hi:[1,0,1]
	v_pk_fma_f32 v[8:9], v[142:143], s[4:5], v[8:9] op_sel_hi:[1,0,1]
	v_pk_fma_f32 v[6:7], v[150:151], s[4:5], v[6:7] op_sel_hi:[1,0,1]
	v_pk_fma_f32 v[4:5], v[148:149], s[4:5], v[4:5] op_sel_hi:[1,0,1]
	v_pk_fma_f32 v[2:3], v[146:147], s[4:5], v[2:3] op_sel_hi:[1,0,1]
	v_pk_fma_f32 v[0:1], v[154:155], s[4:5], v[0:1] op_sel_hi:[1,0,1]
	s_lshl_b32 s4, s17, 3
	s_add_i32 s6, s4, 0
	s_and_saveexec_b64 s[4:5], vcc
	s_cbranch_execz .LBB0_454
	s_lshl_b32 s7, s9, 11
	s_add_i32 s7, s6, s7
	v_mul_f32_e32 v132, 0x3c800000, v132
	s_waitcnt lgkmcnt(0)
	v_add_f32_e32 v133, v133, v134
	v_lshl_add_u32 v134, v145, 5, s7
	ds_write_b64 v134, v[132:133]

; #define PG8_LAS __attribute__((address_space(3)))
;     __device__ __forceinline__ void fused(f32x4 (&acc)[2][2][4][2], const Unit& u, int wr, int wc, int fr, int fq, PG8_LAS unsigned char* lds, int wid, int lane) const {
;     ...
;         if (half == 0) {
;             PG8_LAS int* idxl = (PG8_LAS int*)(lds + 65536) + row * 32;
;             float v0[16], v1[16];
; #pragma unroll
;             for (int q = 0; q < 16; ++q) { const unsigned b0 = __float_as_uint(top0[q]), b1 = __float_as_uint(top1[q]);
;                 v0[q] = __uint_as_float(b0 & ~127u); v1[q] = __uint_as_float(b1 & ~127u); idxl[q] = (int)(b0 & 127u); idxl[16 + q] = (int)(b1 & 127u); }
;             float best[16];
;             { float cv[16]; cv[0] = __uint_as_float((__float_as_uint(v0[0] + v1[0]) & ~255u) | 0u); cv[1] = __uint_as_float((__float_as_uint(v0[0] + v1[1]) & ~255u) | 1u); cv[2] = __uint_as_float((__float_as_uint(v0[0] + v1[2]) & ~255u) | 2u); cv[3] = __uint_as_float((__float_as_uint(v0[0] + v1[3]) & ~255u) | 3u); cv[4] = __uint_as_float((__float_as_uint(v0[0] + v1[4]) & ~255u) | 4u); cv[5] = __uint_as_float((__float_as_uint(v0[0] + v1[5]) & ~255u) | 5u); cv[6] = __uint_as_float((__float_as_uint(v0[0] + v1[6]) & ~255u) | 6u); cv[7] = __uint_as_float((__float_as_uint(v0[0] + v1[7]) & ~255u) | 7u); cv[8] = __uint_as_float((__float_as_uint(v0[0] + v1[8]) & ~255u) | 8u); cv[9] = __uint_as_float((__float_as_uint(v0[0] + v1[9]) & ~255u) | 9u); cv[10] = __uint_as_float((__float_as_uint(v0[0] + v1[10]) & ~255u) | 10u); cv[11] = __uint_as_float((__float_as_uint(v0[0] + v1[11]) & ~255u) | 11u); cv[12] = __uint_as_float((__float_as_uint(v0[0] + v1[12]) & ~255u) | 12u); cv[13] = __uint_as_float((__float_as_uint(v0[0] + v1[13]) & ~255u) | 13u); cv[14] = __uint_as_float((__float_as_uint(v0[0] + v1[14]) & ~255u) | 14u); cv[15] = __uint_as_float((__float_as_uint(v0[0] + v1[15]) & ~255u) | 15u); sort16_desc(cv);
; #pragma unroll
;               for (int q = 0; q < 16; ++q) best[q] = cv[q]; }
.LBB0_588:
	s_waitcnt lgkmcnt(0)
	s_barrier
	s_and_b64 vcc, exec, s[4:5]
	s_cbranch_vccnz .LBB0_590
	v_lshl_add_u32 v16, v128, 7, 0
	v_add_u32_e32 v16, 0x10000, v16
	v_and_b32_e32 v17, 0xffffff80, v12
	v_and_b32_e32 v18, 0xffffff80, v13
	v_and_b32_e32 v21, 0x7f, v77
	v_and_b32_e32 v20, 0x7f, v76
	v_and_b32_e32 v13, 0x7f, v13
	v_and_b32_e32 v12, 0x7f, v12
	v_and_b32_e32 v26, 0xffffff80, v14
	v_and_b32_e32 v28, 0xffffff80, v15
	v_and_b32_e32 v23, 0x7f, v79
	v_and_b32_e32 v22, 0x7f, v78
	v_and_b32_e32 v15, 0x7f, v15
	v_and_b32_e32 v14, 0x7f, v14
	ds_write_b128 v16, v[20:23]
	ds_write_b128 v16, v[12:15] offset:64
	v_and_b32_e32 v21, 0xffffff80, v8
	v_and_b32_e32 v23, 0xffffff80, v9
	v_and_b32_e32 v13, 0x7f, v73
	v_and_b32_e32 v12, 0x7f, v72
	v_and_b32_e32 v9, 0x7f, v9
	v_and_b32_e32 v8, 0x7f, v8
	v_and_b32_e32 v30, 0xffffff80, v10
	v_and_b32_e32 v32, 0xffffff80, v11
	v_and_b32_e32 v15, 0x7f, v75
	v_and_b32_e32 v14, 0x7f, v74
	v_and_b32_e32 v11, 0x7f, v11
	v_and_b32_e32 v10, 0x7f, v10
	v_and_b32_e32 v19, 0xffffff80, v76
	ds_write_b128 v16, v[12:15] offset:16
	ds_write_b128 v16, v[8:11] offset:80
	v_and_b32_e32 v13, 0xffffff80, v4
	v_and_b32_e32 v15, 0xffffff80, v5
	v_and_b32_e32 v9, 0x7f, v69
	v_and_b32_e32 v8, 0x7f, v68
	v_and_b32_e32 v5, 0x7f, v5
	v_and_b32_e32 v4, 0x7f, v4
	v_and_b32_e32 v34, 0xffffff80, v6
	v_and_b32_e32 v36, 0xffffff80, v7
	v_and_b32_e32 v11, 0x7f, v71
	v_and_b32_e32 v10, 0x7f, v70
	v_and_b32_e32 v7, 0x7f, v7
	v_and_b32_e32 v6, 0x7f, v6
	ds_write_b128 v16, v[8:11] offset:32
	ds_write_b128 v16, v[4:7] offset:96
	v_and_b32_e32 v5, 0x7f, v65
	v_and_b32_e32 v4, 0x7f, v64
	v_and_b32_e32 v41, 0xffffff80, v2
	v_and_b32_e32 v42, 0xffffff80, v3
	v_and_b32_e32 v7, 0x7f, v67
	v_and_b32_e32 v6, 0x7f, v66
	v_and_b32_e32 v11, 0x7f, v3
	v_and_b32_e32 v10, 0x7f, v2
	v_add_f32_e32 v2, v19, v17
	s_movk_i32 s4, 0xff00
	v_add_f32_e32 v3, v19, v18
	v_and_b32_e32 v24, 0xffffff80, v77
	ds_write_b128 v16, v[4:7] offset:48
	v_and_b32_e32 v2, 0xffffff00, v2
	v_and_or_b32 v3, v3, s4, 1
	v_add_f32_e32 v4, v19, v26
	v_add_f32_e32 v5, v19, v28
	v_and_b32_e32 v40, 0xffffff80, v1
	v_and_b32_e32 v9, 0x7f, v1
	v_and_b32_e32 v8, 0x7f, v0
	v_and_or_b32 v4, v4, s4, 2
	v_and_or_b32 v5, v5, s4, 3
	v_add_f32_e32 v48, v24, v17
	v_add_f32_e32 v49, v24, v18
	ds_write_b128 v16, v[8:11] offset:112
	v_add_f32_e32 v6, v19, v21
	v_add_f32_e32 v7, v19, v23
	v_add_f32_e32 v11, v19, v15
	v_add_f32_e32 v15, v19, v36
	v_add_f32_e32 v36, v19, v40
	v_max_f32_e32 v40, v2, v3
	v_min_f32_e32 v2, v2, v3
	v_max_f32_e32 v3, v5, v5
	v_and_or_b32 v48, v48, s4, 16
	v_and_or_b32 v49, v49, s4, 17
	v_add_f32_e32 v50, v24, v26
	v_add_f32_e32 v51, v24, v28
	v_and_or_b32 v6, v6, s4, 4
	v_and_or_b32 v7, v7, s4, 5
	v_add_f32_e32 v8, v19, v30
	v_add_f32_e32 v9, v19, v32
	v_max_f32_e32 v5, v4, v3
	v_min_f32_e32 v3, v4, v3
	v_and_or_b32 v50, v50, s4, 18
	v_and_or_b32 v51, v51, s4, 19
	v_and_or_b32 v8, v8, s4, 6
	v_and_or_b32 v9, v9, s4, 7
	v_max_f32_e32 v4, v40, v5
	v_min_f32_e32 v5, v40, v5
	v_max_f32_e32 v40, v2, v3
	v_add_f32_e32 v52, v24, v21
	v_add_f32_e32 v23, v24, v23
	v_add_f32_e32 v30, v24, v30
	v_add_f32_e32 v24, v24, v32
	v_max_f32_e32 v58, v48, v49
	v_min_f32_e32 v48, v48, v49
	v_max_f32_e32 v49, v51, v51
	v_min_f32_e32 v2, v2, v3
	v_max_f32_e32 v3, v40, v5
	v_min_f32_e32 v5, v40, v5
	v_max_f32_e32 v40, v6, v7
	v_min_f32_e32 v6, v6, v7
	v_max_f32_e32 v7, v9, v9
	v_and_or_b32 v52, v52, s4, 20
	v_and_or_b32 v23, v23, s4, 21
	v_and_or_b32 v30, v30, s4, 22
	v_and_or_b32 v24, v24, s4, 23
	v_max_f32_e32 v51, v50, v49
	v_min_f32_e32 v49, v50, v49
	v_max_f32_e32 v9, v8, v7
	v_min_f32_e32 v7, v8, v7
	v_max_f32_e32 v50, v58, v51
	v_min_f32_e32 v51, v58, v51
	v_max_f32_e32 v58, v48, v49
	v_max_f32_e32 v8, v40, v9
	v_min_f32_e32 v9, v40, v9
	v_max_f32_e32 v40, v6, v7
	v_min_f32_e32 v48, v48, v49
	v_max_f32_e32 v49, v58, v51
	v_min_f32_e32 v51, v58, v51
	v_max_f32_e32 v58, v52, v23
	v_min_f32_e32 v23, v52, v23
	v_max_f32_e32 v52, v30, v24
	v_min_f32_e32 v24, v30, v24
	v_min_f32_e32 v6, v6, v7
	v_max_f32_e32 v7, v40, v9
	v_min_f32_e32 v9, v40, v9
	v_max_f32_e32 v30, v58, v52
	v_min_f32_e32 v52, v58, v52
	v_max_f32_e32 v58, v23, v24
	v_max_f32_e32 v40, v4, v8
	v_min_f32_e32 v4, v4, v8
	v_max_f32_e32 v8, v5, v9
	v_min_f32_e32 v23, v23, v24
	v_max_f32_e32 v24, v58, v52
	v_min_f32_e32 v52, v58, v52
	v_and_b32_e32 v25, 0xffffff80, v78
	v_add_f32_e32 v10, v19, v13
	v_min_f32_e32 v5, v5, v9
	v_max_f32_e32 v9, v8, v4
	v_min_f32_e32 v4, v8, v4
	v_max_f32_e32 v8, v3, v7
	v_min_f32_e32 v3, v3, v7
	v_max_f32_e32 v7, v2, v6
	v_max_f32_e32 v58, v50, v30
	v_min_f32_e32 v30, v50, v30
	v_max_f32_e32 v50, v51, v52
	v_and_or_b32 v10, v10, s4, 8
	v_and_or_b32 v11, v11, s4, 9
	v_add_f32_e32 v13, v19, v34
	v_min_f32_e32 v2, v2, v6
	v_max_f32_e32 v6, v7, v3
	v_min_f32_e32 v3, v7, v3
	v_add_f32_e32 v32, v25, v17
	v_add_f32_e32 v53, v25, v18
	v_min_f32_e32 v51, v51, v52
	v_max_f32_e32 v52, v50, v30
	v_min_f32_e32 v30, v50, v30
	v_max_f32_e32 v50, v49, v24
	v_min_f32_e32 v24, v49, v24
	v_max_f32_e32 v49, v48, v23
	v_and_or_b32 v13, v13, s4, 10
	v_and_or_b32 v15, v15, s4, 11
	v_max_f32_e32 v7, v8, v9
	v_min_f32_e32 v8, v8, v9
	v_max_f32_e32 v9, v6, v4
	v_min_f32_e32 v4, v6, v4
	v_max_f32_e32 v6, v3, v5
	v_min_f32_e32 v3, v3, v5
	v_max_f32_e32 v5, v11, v11
	v_and_or_b32 v32, v32, s4, 32
	v_and_or_b32 v53, v53, s4, 33
	v_add_f32_e32 v54, v25, v26
	v_add_f32_e32 v55, v25, v28
	v_min_f32_e32 v23, v48, v23
	v_max_f32_e32 v48, v49, v24
	v_min_f32_e32 v24, v49, v24
	v_and_b32_e32 v27, 0xffffff80, v79
	v_and_b32_e32 v38, 0xffffff80, v0
	v_max_f32_e32 v11, v10, v5
	v_min_f32_e32 v5, v10, v5
	v_max_f32_e32 v10, v15, v15
; __device__ __forceinline__ void sort16_desc(float (&v)[16]) {
;     CE(v[0], v[1]); CE(v[2], v[3]); CE(v[0], v[2]); CE(v[1], v[3]);
;     CE(v[1], v[2]); CE(v[4], v[5]); CE(v[6], v[7]); CE(v[4], v[6]);
;     CE(v[5], v[7]); CE(v[5], v[6]); CE(v[0], v[4]); CE(v[2], v[6]);
;     CE(v[2], v[4]); CE(v[1], v[5]); CE(v[3], v[7]); CE(v[3], v[5]);
;     CE(v[1], v[2]); CE(v[3], v[4]); CE(v[5], v[6]); CE(v[8], v[9]);
;     CE(v[10], v[11]); CE(v[8], v[10]); CE(v[9], v[11]); CE(v[9], v[10]);
;     CE(v[12], v[13]); CE(v[14], v[15]); CE(v[12], v[14]); CE(v[13], v[15]);
;     CE(v[13], v[14]); CE(v[8], v[12]); CE(v[10], v[14]); CE(v[10], v[12]);
;     CE(v[9], v[13]); CE(v[11], v[15]); CE(v[11], v[13]); CE(v[9], v[10]);
;     CE(v[11], v[12]); CE(v[13], v[14]); CE(v[0], v[8]); CE(v[4], v[12]);
;     CE(v[4], v[8]); CE(v[2], v[10]); CE(v[6], v[14]); CE(v[6], v[10]);
;     CE(v[2], v[4]); CE(v[6], v[8]); CE(v[10], v[12]); CE(v[1], v[9]);
;     CE(v[5], v[13]); CE(v[5], v[9]); CE(v[3], v[11]); CE(v[7], v[15]);
;     CE(v[7], v[11]); CE(v[3], v[5]); CE(v[7], v[9]); CE(v[11], v[13]);
;     CE(v[1], v[2]); CE(v[3], v[4]); CE(v[5], v[6]); CE(v[7], v[8]);
;     CE(v[9], v[10]); CE(v[11], v[12]); CE(v[13], v[14]);
; }
; __device__ __forceinline__ void merge_top16(float (&v)[16], const float (&nw)[16]) {
;     v[0] = fmaxf(v[0], nw[15]); v[1] = fmaxf(v[1], nw[14]); v[2] = fmaxf(v[2], nw[13]); v[3] = fmaxf(v[3], nw[12]); v[4] = fmaxf(v[4], nw[11]); v[5] = fmaxf(v[5], nw[10]); v[6] = fmaxf(v[6], nw[9]); v[7] = fmaxf(v[7], nw[8]); v[8] = fmaxf(v[8], nw[7]); v[9] = fmaxf(v[9], nw[6]); v[10] = fmaxf(v[10], nw[5]); v[11] = fmaxf(v[11], nw[4]); v[12] = fmaxf(v[12], nw[3]); v[13] = fmaxf(v[13], nw[2]); v[14] = fmaxf(v[14], nw[1]); v[15] = fmaxf(v[15], nw[0]);
;     CE(v[0], v[8]); CE(v[1], v[9]); CE(v[2], v[10]); CE(v[3], v[11]);
;     CE(v[4], v[12]); CE(v[5], v[13]); CE(v[6], v[14]); CE(v[7], v[15]);
;     CE(v[0], v[4]); CE(v[1], v[5]); CE(v[2], v[6]); CE(v[3], v[7]);
;     CE(v[8], v[12]); CE(v[9], v[13]); CE(v[10], v[14]); CE(v[11], v[15]);
;     CE(v[0], v[2]); CE(v[1], v[3]); CE(v[4], v[6]); CE(v[5], v[7]);
;     CE(v[8], v[10]); CE(v[9], v[11]); CE(v[12], v[14]); CE(v[13], v[15]);
;     CE(v[0], v[1]); CE(v[2], v[3]); CE(v[4], v[5]); CE(v[6], v[7]);
;     CE(v[8], v[9]); CE(v[10], v[11]); CE(v[12], v[13]); CE(v[14], v[15]);
; }
	v_and_or_b32 v54, v54, s4, 34
	v_and_or_b32 v55, v55, s4, 35
	v_max_f32_e32 v49, v50, v52
	v_min_f32_e32 v50, v50, v52
	v_max_f32_e32 v52, v48, v30
	v_min_f32_e32 v30, v48, v30
	v_max_f32_e32 v48, v24, v51
	v_min_f32_e32 v24, v24, v51
	v_max_f32_e32 v51, v53, v53
	v_add_f32_e32 v34, v19, v38
	v_max_f32_e32 v15, v13, v10
	v_min_f32_e32 v10, v13, v10
	v_add_f32_e32 v21, v25, v21
	v_add_f32_e32 v25, v27, v17
	v_max_f32_e32 v53, v32, v51
	v_min_f32_e32 v32, v32, v51
	v_max_f32_e32 v51, v55, v55
	v_and_or_b32 v34, v34, s4, 12
	v_and_or_b32 v36, v36, s4, 13
	v_add_f32_e32 v38, v19, v41
	v_add_f32_e32 v19, v19, v42
	v_max_f32_e32 v13, v11, v15
	v_min_f32_e32 v11, v11, v15
	v_max_f32_e32 v15, v5, v10
	v_and_or_b32 v21, v21, s4, 36
	v_and_or_b32 v25, v25, s4, 48
	v_add_f32_e32 v56, v27, v18
	v_add_f32_e32 v57, v27, v26
	v_max_f32_e32 v55, v54, v51
	v_min_f32_e32 v51, v54, v51
	v_and_or_b32 v38, v38, s4, 14
	v_and_or_b32 v19, v19, s4, 15
	v_min_f32_e32 v5, v5, v10
	v_max_f32_e32 v10, v15, v11
	v_min_f32_e32 v11, v15, v11
	v_max_f32_e32 v15, v36, v36
	v_and_or_b32 v56, v56, s4, 49
	v_and_or_b32 v57, v57, s4, 50
	v_max_f32_e32 v54, v53, v55
	v_min_f32_e32 v53, v53, v55
	v_max_f32_e32 v55, v32, v51
	v_max_f32_e32 v36, v34, v15
	v_min_f32_e32 v15, v34, v15
	v_max_f32_e32 v34, v38, v38
	v_min_f32_e32 v32, v32, v51
	v_max_f32_e32 v51, v55, v53
	v_min_f32_e32 v53, v55, v53
	v_max_f32_e32 v55, v21, v25
	v_min_f32_e32 v21, v21, v25
	v_max_f32_e32 v25, v57, v57
	v_max_f32_e32 v38, v34, v19
	v_min_f32_e32 v19, v34, v19
	v_max_f32_e32 v57, v56, v25
	v_min_f32_e32 v25, v56, v25
	v_max_f32_e32 v34, v36, v38
	v_min_f32_e32 v36, v36, v38
	v_max_f32_e32 v38, v15, v19
	v_max_f32_e32 v56, v55, v57
	v_min_f32_e32 v55, v55, v57
	v_max_f32_e32 v57, v21, v25
	v_min_f32_e32 v15, v15, v19
	v_max_f32_e32 v19, v38, v36
	v_min_f32_e32 v36, v38, v36
	v_min_f32_e32 v21, v21, v25
	v_max_f32_e32 v25, v57, v55
	v_min_f32_e32 v55, v57, v55
	v_max_f32_e32 v38, v13, v34
	v_min_f32_e32 v13, v13, v34
	v_max_f32_e32 v34, v11, v36
	v_max_f32_e32 v57, v54, v56
	v_min_f32_e32 v54, v54, v56
	v_max_f32_e32 v56, v53, v55
	v_min_f32_e32 v11, v11, v36
	v_max_f32_e32 v36, v34, v13
	v_min_f32_e32 v13, v34, v13
	v_max_f32_e32 v34, v10, v19
	v_min_f32_e32 v10, v10, v19
	v_max_f32_e32 v19, v5, v15
	v_min_f32_e32 v53, v53, v55
	v_max_f32_e32 v55, v56, v54
	v_min_f32_e32 v54, v56, v54
	v_max_f32_e32 v56, v51, v25
	v_min_f32_e32 v25, v51, v25
	v_max_f32_e32 v51, v32, v21
	v_min_f32_e32 v5, v5, v15
	v_max_f32_e32 v15, v19, v10
	v_min_f32_e32 v21, v32, v21
	v_max_f32_e32 v32, v51, v25
	v_min_f32_e32 v10, v19, v10
	v_max_f32_e32 v19, v34, v36
	v_min_f32_e32 v34, v34, v36
	v_max_f32_e32 v36, v15, v13
	v_min_f32_e32 v13, v15, v13
	v_min_f32_e32 v25, v51, v25
	v_max_f32_e32 v51, v56, v55
	v_min_f32_e32 v55, v56, v55
	v_max_f32_e32 v56, v32, v54
	v_min_f32_e32 v32, v32, v54
	v_max_f32_e32 v15, v10, v11
	v_min_f32_e32 v10, v10, v11
	v_min_f32_e32 v11, v40, v38
	v_max_f32_e32 v41, v4, v13
	v_max_f32_e32 v54, v25, v53
	v_min_f32_e32 v25, v25, v53
	v_min_f32_e32 v53, v58, v57
	v_max_f32_e32 v59, v30, v32
	v_min_f32_e32 v4, v4, v13
	v_max_f32_e32 v13, v41, v11
	v_min_f32_e32 v11, v41, v11
	v_max_f32_e32 v41, v8, v34
	v_min_f32_e32 v8, v8, v34
	v_max_f32_e32 v34, v3, v10
	v_min_f32_e32 v30, v30, v32
	v_max_f32_e32 v32, v59, v53
	v_min_f32_e32 v53, v59, v53
	v_max_f32_e32 v59, v50, v55
	v_min_f32_e32 v50, v50, v55
	v_max_f32_e32 v55, v24, v25
	v_min_f32_e32 v3, v3, v10
	v_max_f32_e32 v10, v34, v8
	v_min_f32_e32 v8, v34, v8
	v_min_f32_e32 v24, v24, v25
	v_max_f32_e32 v25, v55, v50
	v_min_f32_e32 v50, v55, v50
	v_max_f32_e32 v34, v41, v13
	v_min_f32_e32 v13, v41, v13
	v_max_f32_e32 v41, v10, v11
	v_min_f32_e32 v10, v10, v11
	v_max_f32_e32 v11, v8, v4
	v_min_f32_e32 v4, v8, v4
	v_max_f32_e32 v8, v7, v19
	v_min_f32_e32 v7, v7, v19
	v_max_f32_e32 v19, v6, v15
	v_max_f32_e32 v55, v59, v32
	v_min_f32_e32 v32, v59, v32
	v_max_f32_e32 v59, v25, v53
	v_min_f32_e32 v25, v25, v53
	v_max_f32_e32 v53, v50, v30
	v_min_f32_e32 v30, v50, v30
	v_max_f32_e32 v50, v49, v51
	v_min_f32_e32 v49, v49, v51
	v_max_f32_e32 v51, v48, v54
	v_min_f32_e32 v6, v6, v15
	v_max_f32_e32 v15, v19, v7
	v_min_f32_e32 v7, v19, v7
	v_max_f32_e32 v19, v9, v36
	v_min_f32_e32 v9, v9, v36
	v_max_f32_e32 v36, v2, v5
	v_min_f32_e32 v48, v48, v54
	v_max_f32_e32 v54, v51, v49
	v_min_f32_e32 v49, v51, v49
	v_max_f32_e32 v51, v52, v56
	v_min_f32_e32 v52, v52, v56
	v_max_f32_e32 v56, v23, v21
	v_min_f32_e32 v2, v2, v5
	v_max_f32_e32 v5, v36, v9
	v_min_f32_e32 v9, v36, v9
	v_max_f32_e32 v36, v19, v15
	v_min_f32_e32 v21, v23, v21
	v_max_f32_e32 v23, v56, v52
	v_min_f32_e32 v52, v56, v52
	v_and_b32_e32 v20, 0xffffff80, v72
	v_min_f32_e32 v15, v19, v15
	v_max_f32_e32 v19, v5, v7
	v_min_f32_e32 v5, v5, v7
	v_max_f32_e32 v7, v9, v6
	v_min_f32_e32 v6, v9, v6
	v_min_f32_e32 v9, v8, v34
	v_min_f32_e32 v42, v36, v13
	v_max_f32_e32 v56, v51, v54
	v_min_f32_e32 v51, v51, v54
	v_max_f32_e32 v54, v23, v49
	v_min_f32_e32 v23, v23, v49
	v_max_f32_e32 v49, v52, v48
	v_min_f32_e32 v48, v52, v48
	v_and_b32_e32 v39, 0xffffff80, v65
	v_min_f32_e32 v65, v48, v24
	v_max3_f32 v9, v9, v48, v24
	v_max3_f32 v24, v42, v49, v30
	v_add_f32_e32 v27, v27, v28
	v_add_f32_e32 v28, v20, v17
	v_add_f32_e32 v42, v20, v18
	v_add_f32_e32 v20, v20, v26
	v_and_b32_e32 v22, 0xffffff80, v73
	v_and_or_b32 v27, v27, s4, 51
	v_and_or_b32 v28, v28, s4, 64
	v_and_b32_e32 v42, 0xffffff00, v42
	v_and_b32_e32 v20, 0xffffff00, v20
	v_and_b32_e32 v29, 0xffffff80, v74
	v_and_b32_e32 v31, 0xffffff80, v75
	v_and_b32_e32 v33, 0xffffff80, v70
	v_and_b32_e32 v35, 0xffffff80, v71
	v_and_b32_e32 v37, 0xffffff80, v64
; __device__ __forceinline__ void sort16_desc(float (&v)[16]) {
;     CE(v[0], v[1]); CE(v[2], v[3]); CE(v[0], v[2]); CE(v[1], v[3]);
;     CE(v[1], v[2]); CE(v[4], v[5]); CE(v[6], v[7]); CE(v[4], v[6]);
;     CE(v[5], v[7]); CE(v[5], v[6]); CE(v[0], v[4]); CE(v[2], v[6]);
;     CE(v[2], v[4]); CE(v[1], v[5]); CE(v[3], v[7]); CE(v[3], v[5]);
;     CE(v[1], v[2]); CE(v[3], v[4]); CE(v[5], v[6]); CE(v[8], v[9]);
;     CE(v[10], v[11]); CE(v[8], v[10]); CE(v[9], v[11]); CE(v[9], v[10]);
;     CE(v[12], v[13]); CE(v[14], v[15]); CE(v[12], v[14]); CE(v[13], v[15]);
;     CE(v[13], v[14]); CE(v[8], v[12]); CE(v[10], v[14]); CE(v[10], v[12]);
;     CE(v[9], v[13]); CE(v[11], v[15]); CE(v[11], v[13]); CE(v[9], v[10]);
;     CE(v[11], v[12]); CE(v[13], v[14]); CE(v[0], v[8]); CE(v[4], v[12]);
;     CE(v[4], v[8]); CE(v[2], v[10]); CE(v[6], v[14]); CE(v[6], v[10]);
;     CE(v[2], v[4]); CE(v[6], v[8]); CE(v[10], v[12]); CE(v[1], v[9]);
;     CE(v[5], v[13]); CE(v[5], v[9]); CE(v[3], v[11]); CE(v[7], v[15]);
;     CE(v[7], v[11]); CE(v[3], v[5]); CE(v[7], v[9]); CE(v[11], v[13]);
;     CE(v[1], v[2]); CE(v[3], v[4]); CE(v[5], v[6]); CE(v[7], v[8]);
;     CE(v[9], v[10]); CE(v[11], v[12]); CE(v[13], v[14]);
; }
; __device__ __forceinline__ void merge_top16(float (&v)[16], const float (&nw)[16]) {
;     v[0] = fmaxf(v[0], nw[15]); v[1] = fmaxf(v[1], nw[14]); v[2] = fmaxf(v[2], nw[13]); v[3] = fmaxf(v[3], nw[12]); v[4] = fmaxf(v[4], nw[11]); v[5] = fmaxf(v[5], nw[10]); v[6] = fmaxf(v[6], nw[9]); v[7] = fmaxf(v[7], nw[8]); v[8] = fmaxf(v[8], nw[7]); v[9] = fmaxf(v[9], nw[6]); v[10] = fmaxf(v[10], nw[5]); v[11] = fmaxf(v[11], nw[4]); v[12] = fmaxf(v[12], nw[3]); v[13] = fmaxf(v[13], nw[2]); v[14] = fmaxf(v[14], nw[1]); v[15] = fmaxf(v[15], nw[0]);
;     CE(v[0], v[8]); CE(v[1], v[9]); CE(v[2], v[10]); CE(v[3], v[11]);
;     CE(v[4], v[12]); CE(v[5], v[13]); CE(v[6], v[14]); CE(v[7], v[15]);
;     CE(v[0], v[4]); CE(v[1], v[5]); CE(v[2], v[6]); CE(v[3], v[7]);
;     CE(v[8], v[12]); CE(v[9], v[13]); CE(v[10], v[14]); CE(v[11], v[15]);
;     CE(v[0], v[2]); CE(v[1], v[3]); CE(v[4], v[6]); CE(v[5], v[7]);
;     CE(v[8], v[10]); CE(v[9], v[11]); CE(v[12], v[14]); CE(v[13], v[15]);
;     CE(v[0], v[1]); CE(v[2], v[3]); CE(v[4], v[5]); CE(v[6], v[7]);
;     CE(v[8], v[9]); CE(v[10], v[11]); CE(v[12], v[13]); CE(v[14], v[15]);
; }
	v_min_f32_e32 v43, v15, v41
	v_min_f32_e32 v44, v19, v10
	v_min_f32_e32 v62, v54, v25
	v_or_b32_e32 v42, 0x41, v42
	v_or_b32_e32 v20, 0x42, v20
	v_add_f32_e32 v26, v22, v17
	v_add_f32_e32 v22, v22, v18
	v_min_f32_e32 v63, v23, v53
	v_max3_f32 v23, v43, v23, v53
	v_max3_f32 v10, v19, v10, v62
	v_max3_f32 v19, v44, v54, v25
	v_and_b32_e32 v26, 0xffffff00, v26
	v_and_b32_e32 v22, 0xffffff00, v22
	v_add_f32_e32 v43, v29, v17
	v_add_f32_e32 v29, v29, v18
	v_add_f32_e32 v44, v31, v17
	v_add_f32_e32 v18, v31, v18
	v_add_f32_e32 v31, v33, v17
	v_add_f32_e32 v33, v35, v17
	v_add_f32_e32 v35, v37, v17
	v_add_f32_e32 v37, v39, v17
	v_max_f32_e32 v39, v27, v28
	v_min_f32_e32 v27, v27, v28
	v_max_f32_e32 v28, v42, v42
	v_or_b32_e32 v26, 0x50, v26
	v_or_b32_e32 v22, 0x51, v22
	v_and_b32_e32 v43, 0xffffff00, v43
	v_and_b32_e32 v29, 0xffffff00, v29
	v_max_f32_e32 v42, v28, v20
	v_min_f32_e32 v20, v28, v20
	v_or_b32_e32 v43, 0x60, v43
	v_or_b32_e32 v29, 0x61, v29
	v_max_f32_e32 v28, v39, v42
	v_min_f32_e32 v39, v39, v42
	v_max_f32_e32 v42, v27, v20
	v_min_f32_e32 v20, v27, v20
	v_max_f32_e32 v27, v42, v39
	v_min_f32_e32 v39, v42, v39
	v_max_f32_e32 v42, v26, v22
	v_min_f32_e32 v22, v26, v22
	v_max_f32_e32 v26, v29, v29
	v_max_f32_e32 v29, v43, v43
	v_max_f32_e32 v43, v29, v26
	v_min_f32_e32 v26, v29, v26
	v_max_f32_e32 v29, v42, v43
	v_min_f32_e32 v42, v42, v43
	v_max_f32_e32 v43, v22, v26
	v_and_b32_e32 v12, 0xffffff80, v68
	v_and_b32_e32 v14, 0xffffff80, v69
	v_min_f32_e32 v22, v22, v26
	v_max_f32_e32 v26, v43, v42
	v_min_f32_e32 v42, v43, v42
	v_add_f32_e32 v12, v12, v17
	v_add_f32_e32 v14, v14, v17
	v_max_f32_e32 v43, v28, v29
	v_min_f32_e32 v28, v28, v29
	v_max_f32_e32 v29, v39, v42
	v_and_b32_e32 v44, 0xffffff00, v44
	v_and_b32_e32 v18, 0xffffff00, v18
	v_and_b32_e32 v12, 0xffffff00, v12
	v_and_b32_e32 v14, 0xffffff00, v14
	v_min_f32_e32 v39, v39, v42
	v_max_f32_e32 v42, v29, v28
	v_min_f32_e32 v28, v29, v28
	v_max_f32_e32 v29, v27, v26
	v_min_f32_e32 v26, v27, v26
	v_max_f32_e32 v27, v20, v22
	v_or_b32_e32 v44, 0x70, v44
	v_or_b32_e32 v18, 0x71, v18
	v_or_b32_e32 v12, 0x80, v12
	v_or_b32_e32 v14, 0x90, v14
	v_min_f32_e32 v20, v20, v22
	v_max_f32_e32 v22, v27, v26
	v_min_f32_e32 v26, v27, v26
	v_and_b32_e32 v31, 0xffffff00, v31
	v_and_b32_e32 v33, 0xffffff00, v33
	v_max_f32_e32 v27, v29, v42
	v_min_f32_e32 v29, v29, v42
	v_max_f32_e32 v42, v22, v28
	v_min_f32_e32 v22, v22, v28
	v_max_f32_e32 v28, v26, v39
	v_min_f32_e32 v26, v26, v39
	v_max_f32_e32 v39, v44, v44
	v_or_b32_e32 v31, 0xa0, v31
	v_or_b32_e32 v33, 0xb0, v33
	v_and_b32_e32 v35, 0xffffff00, v35
	v_and_b32_e32 v37, 0xffffff00, v37
	v_max_f32_e32 v44, v39, v18
	v_min_f32_e32 v18, v39, v18
	v_max_f32_e32 v39, v12, v14
	v_min_f32_e32 v12, v12, v14
	v_or_b32_e32 v35, 0xc0, v35
	v_or_b32_e32 v37, 0xd0, v37
	v_max_f32_e32 v14, v44, v39
	v_min_f32_e32 v39, v44, v39
	v_max_f32_e32 v44, v18, v12
	v_min_f32_e32 v12, v18, v12
	v_max_f32_e32 v18, v44, v39
	v_min_f32_e32 v39, v44, v39
	v_max_f32_e32 v44, v31, v33
	v_min_f32_e32 v31, v31, v33
	v_max_f32_e32 v33, v37, v37
	v_max_f32_e32 v37, v35, v33
	v_min_f32_e32 v33, v35, v33
	v_max_f32_e32 v35, v44, v37
	v_min_f32_e32 v37, v44, v37
	v_max_f32_e32 v44, v31, v33
	v_min_f32_e32 v31, v31, v33
	v_max_f32_e32 v33, v44, v37
	v_min_f32_e32 v37, v44, v37
	v_max_f32_e32 v44, v14, v35
	v_min_f32_e32 v14, v14, v35
	v_max_f32_e32 v35, v39, v37
	v_min_f32_e32 v37, v39, v37
	v_max_f32_e32 v39, v35, v14
	v_min_f32_e32 v14, v35, v14
	v_max_f32_e32 v35, v18, v33
	v_min_f32_e32 v18, v18, v33
	v_max_f32_e32 v33, v12, v31
	v_min_f32_e32 v12, v12, v31
	v_max_f32_e32 v31, v33, v18
	v_min_f32_e32 v45, v5, v11
	v_min_f32_e32 v61, v51, v59
	v_min_f32_e32 v18, v33, v18
	v_max_f32_e32 v33, v35, v39
	v_min_f32_e32 v35, v35, v39
	v_max_f32_e32 v39, v31, v14
	v_min_f32_e32 v14, v31, v14
	v_max3_f32 v5, v5, v11, v61
	v_max3_f32 v11, v45, v51, v59
	v_max_f32_e32 v31, v18, v37
	v_min_f32_e32 v18, v18, v37
	v_min_f32_e32 v37, v43, v44
	v_max_f32_e32 v45, v22, v14
	v_min_f32_e32 v14, v22, v14
	v_max_f32_e32 v22, v45, v37
	v_min_f32_e32 v37, v45, v37
	v_max_f32_e32 v45, v29, v35
	v_min_f32_e32 v29, v29, v35
	v_max_f32_e32 v35, v26, v18
	v_min_f32_e32 v46, v7, v4
	v_min_f32_e32 v47, v6, v3
	v_min_f32_e32 v52, v50, v55
	v_min_f32_e32 v60, v56, v32
	v_min_f32_e32 v64, v49, v30
	v_min_f32_e32 v18, v26, v18
	v_max_f32_e32 v26, v35, v29
	v_min_f32_e32 v29, v35, v29
	v_max3_f32 v21, v40, v38, v21
	v_max3_f32 v8, v8, v34, v65
	v_max3_f32 v13, v36, v13, v64
	v_max3_f32 v15, v15, v41, v63
	v_max3_f32 v4, v7, v4, v60
	v_max3_f32 v7, v46, v56, v32
	v_max3_f32 v3, v6, v3, v52
	v_max3_f32 v6, v47, v50, v55
	v_max3_f32 v2, v2, v58, v57
	v_max_f32_e32 v35, v45, v22
	v_min_f32_e32 v22, v45, v22
	v_max_f32_e32 v45, v26, v37
	v_min_f32_e32 v26, v26, v37
	v_max_f32_e32 v37, v29, v14
	v_min_f32_e32 v14, v29, v14
	v_max_f32_e32 v29, v27, v33
	v_min_f32_e32 v27, v27, v33
	v_max_f32_e32 v33, v28, v31
	v_max_f32_e32 v25, v21, v19
	v_min_f32_e32 v19, v21, v19
	v_max_f32_e32 v21, v8, v5
	v_min_f32_e32 v5, v8, v5
	v_max_f32_e32 v8, v9, v11
	v_min_f32_e32 v9, v9, v11
	v_max_f32_e32 v11, v13, v4
	v_min_f32_e32 v4, v13, v4
	v_max_f32_e32 v13, v24, v7
	v_min_f32_e32 v7, v24, v7
	v_max_f32_e32 v24, v15, v3
	v_min_f32_e32 v3, v15, v3
	v_max_f32_e32 v15, v23, v6
	v_min_f32_e32 v6, v23, v6
	v_max_f32_e32 v23, v10, v2
	v_min_f32_e32 v2, v10, v2
	v_min_f32_e32 v28, v28, v31
	v_max_f32_e32 v31, v33, v27
	v_min_f32_e32 v27, v33, v27
	v_max_f32_e32 v33, v42, v39
	v_min_f32_e32 v39, v42, v39
	v_max_f32_e32 v42, v20, v12
	v_max_f32_e32 v10, v25, v13
	v_min_f32_e32 v13, v25, v13
	v_max_f32_e32 v25, v21, v24
	v_min_f32_e32 v21, v21, v24
; #define CE(a, b) do { const float hi_ = fmaxf(a, b), lo_ = fminf(a, b); a = hi_; b = lo_; } while (0)
; __device__ __forceinline__ void merge_top16(float (&v)[16], const float (&nw)[16]) {
;     v[0] = fmaxf(v[0], nw[15]); v[1] = fmaxf(v[1], nw[14]); v[2] = fmaxf(v[2], nw[13]); v[3] = fmaxf(v[3], nw[12]); v[4] = fmaxf(v[4], nw[11]); v[5] = fmaxf(v[5], nw[10]); v[6] = fmaxf(v[6], nw[9]); v[7] = fmaxf(v[7], nw[8]); v[8] = fmaxf(v[8], nw[7]); v[9] = fmaxf(v[9], nw[6]); v[10] = fmaxf(v[10], nw[5]); v[11] = fmaxf(v[11], nw[4]); v[12] = fmaxf(v[12], nw[3]); v[13] = fmaxf(v[13], nw[2]); v[14] = fmaxf(v[14], nw[1]); v[15] = fmaxf(v[15], nw[0]);
;     CE(v[0], v[8]); CE(v[1], v[9]); CE(v[2], v[10]); CE(v[3], v[11]);
;     CE(v[4], v[12]); CE(v[5], v[13]); CE(v[6], v[14]); CE(v[7], v[15]);
;     CE(v[0], v[4]); CE(v[1], v[5]); CE(v[2], v[6]); CE(v[3], v[7]);
;     CE(v[8], v[12]); CE(v[9], v[13]); CE(v[10], v[14]); CE(v[11], v[15]);
;     CE(v[0], v[2]); CE(v[1], v[3]); CE(v[4], v[6]); CE(v[5], v[7]);
;     CE(v[8], v[10]); CE(v[9], v[11]); CE(v[12], v[14]); CE(v[13], v[15]);
;     CE(v[0], v[1]); CE(v[2], v[3]); CE(v[4], v[5]); CE(v[6], v[7]);
;     CE(v[8], v[9]); CE(v[10], v[11]); CE(v[12], v[13]); CE(v[14], v[15]);
; }
;     __device__ __forceinline__ void fused(f32x4 (&acc)[2][2][4][2], const Unit& u, int wr, int wc, int fr, int fq, PG8_LAS unsigned char* lds, int wid, int lane) const {
;     ...
;             { float cv[16]; cv[0] = __uint_as_float((__float_as_uint(v0[14] + v1[0]) & ~255u) | 224u); cv[1] = __uint_as_float((__float_as_uint(v0[15] + v1[0]) & ~255u) | 240u); cv[2] = -INFINITY; cv[3] = -INFINITY; cv[4] = -INFINITY; cv[5] = -INFINITY; cv[6] = -INFINITY; cv[7] = -INFINITY; cv[8] = -INFINITY; cv[9] = -INFINITY; cv[10] = -INFINITY; cv[11] = -INFINITY; cv[12] = -INFINITY; cv[13] = -INFINITY; cv[14] = -INFINITY; cv[15] = -INFINITY; sort16_desc(cv); merge_top16(best, cv); }
;             float sc[16], sum = 0.f;
; #pragma unroll
;             for (int q = 0; q < 16; ++q) { sc[q] = __uint_as_float(__float_as_uint(best[q]) & ~255u); }
;             const float smax = sc[0];
; #pragma unroll
;             for (int q = 0; q < 16; ++q) { sc[q] = __builtin_amdgcn_exp2f((sc[q] - smax) * 1.4426950408889634f); }
	v_max_f32_e32 v24, v8, v15
	v_min_f32_e32 v8, v8, v15
	v_max_f32_e32 v15, v11, v23
	v_min_f32_e32 v11, v11, v23
	v_max_f32_e32 v23, v19, v7
	v_min_f32_e32 v7, v19, v7
	v_max_f32_e32 v19, v5, v3
	v_min_f32_e32 v3, v5, v3
	v_max_f32_e32 v5, v9, v6
	v_min_f32_e32 v6, v9, v6
	v_max_f32_e32 v9, v4, v2
	v_min_f32_e32 v2, v4, v2
	v_min_f32_e32 v12, v20, v12
	v_max_f32_e32 v20, v42, v39
	v_min_f32_e32 v39, v42, v39
	v_and_b32_e32 v1, 0xffffff80, v66
	v_and_b32_e32 v0, 0xffffff80, v67
	v_max_f32_e32 v4, v10, v24
	v_min_f32_e32 v10, v10, v24
	v_max_f32_e32 v24, v25, v15
	v_min_f32_e32 v15, v25, v15
	v_max_f32_e32 v25, v13, v8
	v_min_f32_e32 v8, v13, v8
	v_max_f32_e32 v13, v21, v11
	v_min_f32_e32 v11, v21, v11
	v_max_f32_e32 v21, v23, v5
	v_min_f32_e32 v5, v23, v5
	v_max_f32_e32 v23, v19, v9
	v_min_f32_e32 v9, v19, v9
	v_max_f32_e32 v19, v7, v6
	v_min_f32_e32 v6, v7, v6
	v_max_f32_e32 v7, v3, v2
	v_min_f32_e32 v2, v3, v2
	v_max_f32_e32 v42, v33, v31
	v_min_f32_e32 v31, v33, v31
	v_max_f32_e32 v33, v20, v27
	v_min_f32_e32 v20, v20, v27
	v_max_f32_e32 v27, v39, v28
	v_min_f32_e32 v28, v39, v28
	v_min_f32_e32 v3, v4, v24
	v_min_f32_e32 v30, v10, v15
	v_min_f32_e32 v32, v25, v13
	v_min_f32_e32 v34, v8, v11
	v_min_f32_e32 v36, v21, v23
	v_min_f32_e32 v38, v5, v9
	v_min_f32_e32 v40, v19, v7
	v_min_f32_e32 v41, v6, v2
	v_max_f32_e32 v39, v29, v35
	v_min_f32_e32 v29, v29, v35
	v_max_f32_e32 v35, v42, v22
	v_min_f32_e32 v22, v42, v22
	v_max_f32_e32 v42, v31, v45
	v_min_f32_e32 v31, v31, v45
	v_max_f32_e32 v45, v33, v26
	v_min_f32_e32 v26, v33, v26
	v_max_f32_e32 v33, v20, v37
	v_min_f32_e32 v20, v20, v37
	v_max_f32_e32 v37, v27, v14
	v_min_f32_e32 v14, v27, v14
	v_max_f32_e32 v27, v28, v18
	v_min_f32_e32 v18, v28, v18
	v_add_f32_e32 v1, v1, v17
	v_add_f32_e32 v0, v0, v17
	v_max3_f32 v4, v4, v24, v12
	v_max_f32_e32 v3, v3, v18
	v_max3_f32 v10, v10, v15, v27
	v_max_f32_e32 v12, v30, v14
	v_max3_f32 v13, v25, v13, v37
	v_max_f32_e32 v14, v32, v20
	v_max3_f32 v8, v8, v11, v33
	v_max_f32_e32 v11, v34, v26
	v_max3_f32 v15, v21, v23, v45
	v_max_f32_e32 v18, v36, v31
	v_max3_f32 v5, v5, v9, v42
	v_max_f32_e32 v9, v38, v22
	v_max3_f32 v7, v19, v7, v35
	v_max_f32_e32 v19, v40, v29
	v_max3_f32 v2, v6, v2, v39
	v_max3_f32 v6, v41, v43, v44
	v_and_b32_e32 v1, 0xffffff00, v1
	v_and_b32_e32 v0, 0xffffff00, v0
	v_max_f32_e32 v20, v4, v15
	v_min_f32_e32 v4, v4, v15
	v_max_f32_e32 v15, v3, v18
	v_min_f32_e32 v3, v3, v18
	v_max_f32_e32 v18, v10, v5
	v_min_f32_e32 v5, v10, v5
	v_max_f32_e32 v10, v12, v9
	v_min_f32_e32 v9, v12, v9
	v_max_f32_e32 v12, v13, v7
	v_min_f32_e32 v7, v13, v7
	v_max_f32_e32 v13, v14, v19
	v_min_f32_e32 v14, v14, v19
	v_max_f32_e32 v19, v8, v2
	v_min_f32_e32 v2, v8, v2
	v_max_f32_e32 v8, v11, v6
	v_min_f32_e32 v6, v11, v6
	v_or_b32_e32 v1, 0xe0, v1
	v_or_b32_e32 v0, 0xf0, v0
	v_max_f32_e32 v11, v20, v12
	v_min_f32_e32 v12, v20, v12
	v_max_f32_e32 v20, v15, v13
	v_min_f32_e32 v13, v15, v13
	v_max_f32_e32 v15, v18, v19
	v_min_f32_e32 v18, v18, v19
	v_max_f32_e32 v19, v10, v8
	v_min_f32_e32 v8, v10, v8
	v_max_f32_e32 v10, v4, v7
	v_min_f32_e32 v4, v4, v7
	v_max_f32_e32 v7, v3, v14
	v_min_f32_e32 v3, v3, v14
	v_max_f32_e32 v14, v5, v2
	v_min_f32_e32 v2, v5, v2
	v_max_f32_e32 v5, v9, v6
	v_min_f32_e32 v6, v9, v6
	v_max_f32_e32 v9, v11, v15
	v_min_f32_e32 v11, v11, v15
	v_max_f32_e32 v15, v20, v19
	v_min_f32_e32 v19, v20, v19
	v_max_f32_e32 v20, v12, v18
	v_min_f32_e32 v12, v12, v18
	v_max_f32_e32 v18, v13, v8
	v_min_f32_e32 v8, v13, v8
	v_max_f32_e32 v13, v10, v14
	v_min_f32_e32 v10, v10, v14
	v_max_f32_e32 v14, v7, v5
	v_min_f32_e32 v5, v7, v5
	v_max_f32_e32 v7, v4, v2
	v_min_f32_e32 v2, v4, v2
	v_max_f32_e32 v4, v3, v6
	v_min_f32_e32 v3, v3, v6
	v_max_f32_e32 v17, v1, v0
	v_min_f32_e32 v0, v1, v0
	v_min_f32_e32 v6, v9, v15
	v_min_f32_e32 v21, v11, v19
	v_min_f32_e32 v22, v20, v18
	v_min_f32_e32 v23, v12, v8
	v_min_f32_e32 v24, v13, v14
	v_min_f32_e32 v25, v10, v5
	v_min_f32_e32 v26, v7, v4
	v_min_f32_e32 v27, v2, v3
	s_mov_b32 s4, 0xff800000
	v_max_f32_e32 v0, 0xff800000, v0
	v_max3_f32 v1, v9, v15, s4
	v_max_f32_e32 v6, 0xff800000, v6
	v_max3_f32 v9, v11, v19, s4
	v_max_f32_e32 v11, 0xff800000, v21
	v_max3_f32 v15, v20, v18, s4
	v_max_f32_e32 v18, 0xff800000, v22
	v_max3_f32 v8, v12, v8, s4
	v_max_f32_e32 v12, 0xff800000, v23
	v_max3_f32 v13, v13, v14, s4
	v_max_f32_e32 v14, 0xff800000, v24
	v_max3_f32 v5, v10, v5, s4
	v_max_f32_e32 v10, 0xff800000, v25
	v_max3_f32 v4, v7, v4, s4
	v_max_f32_e32 v7, 0xff800000, v26
	v_max3_f32 v0, v2, v3, v0
	v_max3_f32 v2, v27, v17, s4
	v_max_f32_e32 v3, v1, v13
	v_min_f32_e32 v1, v1, v13
	v_max_f32_e32 v13, v6, v14
	v_min_f32_e32 v6, v6, v14
	v_max_f32_e32 v14, v9, v5
	v_min_f32_e32 v5, v9, v5
	v_max_f32_e32 v9, v11, v10
	v_min_f32_e32 v10, v11, v10
	v_max_f32_e32 v11, v15, v4
	v_min_f32_e32 v4, v15, v4
	v_max_f32_e32 v15, v18, v7
	v_max_f32_e32 v17, v8, v0
	v_min_f32_e32 v0, v8, v0
	v_max_f32_e32 v8, v12, v2
	v_min_f32_e32 v2, v12, v2
	v_max_f32_e32 v12, v3, v11
	v_min_f32_e32 v3, v3, v11
	v_max_f32_e32 v11, v13, v15
	v_min_f32_e32 v13, v13, v15
	v_max_f32_e32 v15, v14, v17
	v_min_f32_e32 v14, v14, v17
	v_max_f32_e32 v17, v9, v8
	v_min_f32_e32 v8, v9, v8
	v_max_f32_e32 v9, v1, v4
	v_min_f32_e32 v24, v1, v4
	v_max_f32_e32 v27, v5, v0
	v_min_f32_e32 v28, v5, v0
	v_max_f32_e32 v29, v10, v2
	v_min_f32_e32 v30, v10, v2
	v_max_f32_e32 v0, v12, v15
	v_min_f32_e32 v1, v12, v15
	v_max_f32_e32 v2, v11, v17
	v_min_f32_e32 v4, v11, v17
	v_min_f32_e32 v7, v18, v7
	v_max_f32_e32 v33, v0, v2
	v_min_f32_e32 v34, v0, v2
	v_min_f32_e32 v36, v1, v4
	v_max_f32_e32 v25, v6, v7
	v_min_f32_e32 v26, v6, v7
	v_max_f32_e32 v35, v1, v4
	v_lshrrev_b32_e32 v0, 2, v33
	v_lshrrev_b32_e32 v2, 2, v34
	v_lshrrev_b32_e32 v6, 2, v36
	v_max_f32_e32 v17, v3, v14
	v_min_f32_e32 v31, v3, v14
	v_and_b32_e32 v0, 60, v0
	v_and_b32_e32 v1, 15, v33
	v_and_b32_e32 v2, 60, v2
	v_and_b32_e32 v3, 15, v34
	v_lshrrev_b32_e32 v4, 2, v35
	v_and_b32_e32 v5, 15, v35
	v_and_b32_e32 v6, 60, v6
	v_and_b32_e32 v7, 15, v36
	s_waitcnt lgkmcnt(0)
; #define RT_PK(q_) (ex[q_] | (int)((__float_as_uint(usc[ex[q_]]) >> 23) << 14))
;     __device__ __forceinline__ void fused(f32x4 (&acc)[2][2][4][2], const Unit& u, int wr, int wc, int fr, int fq, PG8_LAS unsigned char* lds, int wid, int lane) const {
;     ...
;             float sc[16], sum = 0.f;
; #pragma unroll
;             for (int q = 0; q < 16; ++q) { sc[q] = __uint_as_float(__float_as_uint(best[q]) & ~255u); }
;             const float smax = sc[0];
; #pragma unroll
;             for (int q = 0; q < 16; ++q) { sc[q] = __builtin_amdgcn_exp2f((sc[q] - smax) * 1.4426950408889634f); }
; #pragma unroll
;             for (int q = 0; q < 16; ++q) sum += sc[q];
;             const float rs = 1.0f / sum;
;             asm volatile("s_waitcnt lgkmcnt(0)" ::: "memory");
;             int ex[16];
; #pragma unroll
;             for (int q = 0; q < 16; ++q) { const unsigned cid = __float_as_uint(best[q]) & 255u; ex[q] = idxl[cid >> 4] * 128 + idxl[16 + (cid & 15u)]; }
;             const size_t o = ((size_t)u.pn * 16384 + (size_t)(u.pm * BM + row)) * 16;
;             typedef int i32x4 __attribute__((ext_vector_type(4)));
; #pragma unroll
;             for (int i = 0; i < 4; ++i) {
;     ...
;                 *(i32x4*)(eidx + o + 4 * i) = (i32x4){RT_PK(4 * i), RT_PK(4 * i + 1), RT_PK(4 * i + 2), RT_PK(4 * i + 3)};
;                 *(f32x4*)(egate + o + 4 * i) = (f32x4){sc[4 * i] * rs * vsc[ex[4 * i]], sc[4 * i + 1] * rs * vsc[ex[4 * i + 1]], sc[4 * i + 2] * rs * vsc[ex[4 * i + 2]], sc[4 * i + 3] * rs * vsc[ex[4 * i + 3]]};
	v_add_u32_e32 v0, v16, v0
	v_lshl_add_u32 v1, v1, 2, v16
	v_add_u32_e32 v2, v16, v2
	v_lshl_add_u32 v3, v3, 2, v16
	v_and_b32_e32 v4, 60, v4
	v_lshl_add_u32 v5, v5, 2, v16
	v_add_u32_e32 v6, v16, v6
	v_lshl_add_u32 v7, v7, 2, v16
	v_add_u32_e32 v4, v16, v4
	ds_read_b32 v0, v0
	ds_read_b32 v1, v1 offset:64
	ds_read_b32 v2, v2
	ds_read_b32 v3, v3 offset:64
	ds_read_b32 v10, v4
	ds_read_b32 v5, v5 offset:64
	ds_read_b32 v6, v6
	ds_read_b32 v7, v7 offset:64
	s_waitcnt lgkmcnt(0)
	v_lshl_add_u32 v0, v0, 7, v1
	v_ashrrev_i32_e32 v1, 31, v0
	v_lshl_add_u32 v4, v2, 7, v3
	v_lshlrev_b64 v[14:15], 2, v[0:1]
	v_lshl_add_u32 v10, v10, 7, v5
	v_lshl_add_u32 v12, v6, 7, v7
	v_lshl_add_u64 v[2:3], s[8:9], 0, v[14:15]
	v_ashrrev_i32_e32 v5, 31, v4
	v_max_f32_e32 v32, v13, v8
	v_min_f32_e32 v8, v13, v8
	global_load_dword v1, v[2:3], off
	v_lshlrev_b64 v[18:19], 2, v[4:5]
	v_ashrrev_i32_e32 v11, 31, v10
	v_ashrrev_i32_e32 v13, 31, v12
	v_lshl_add_u64 v[2:3], s[8:9], 0, v[18:19]
	v_lshlrev_b64 v[20:21], 2, v[10:11]
	v_lshlrev_b64 v[22:23], 2, v[12:13]
	v_lshl_add_u64 v[6:7], s[8:9], 0, v[20:21]
	global_load_dword v5, v[2:3], off
	global_load_dword v11, v[6:7], off
	v_lshl_add_u64 v[2:3], s[8:9], 0, v[22:23]
	global_load_dword v13, v[2:3], off
	v_min_f32_e32 v2, v9, v27
	v_min_f32_e32 v6, v25, v29
	v_max_f32_e32 v43, v2, v6
	v_min_f32_e32 v44, v2, v6
	v_and_b32_e32 v2, 0xffffff00, v34
	v_and_b32_e32 v51, 0xffffff00, v33
	v_max_f32_e32 v37, v9, v27
	v_max_f32_e32 v3, v25, v29
	v_sub_f32_e32 v2, v2, v51
	v_min_f32_e32 v9, v24, v28
	v_min_f32_e32 v25, v26, v30
	v_max_f32_e32 v41, v37, v3
	v_min_f32_e32 v42, v37, v3
	v_and_b32_e32 v3, 0xffffff00, v35
	v_mul_f32_e32 v2, 0x3fb8aa3b, v2
	v_max_f32_e32 v47, v9, v25
	v_min_f32_e32 v48, v9, v25
	v_exp_f32_e32 v25, v2
	v_sub_f32_e32 v2, v3, v51
	v_and_b32_e32 v6, 0xffffff00, v36
	v_mul_f32_e32 v2, 0x3fb8aa3b, v2
	v_max_f32_e32 v7, v24, v28
	v_max_f32_e32 v24, v26, v30
	v_max_f32_e32 v38, v17, v32
	v_exp_f32_e32 v26, v2
	v_sub_f32_e32 v2, v6, v51
	v_max_f32_e32 v45, v7, v24
	v_min_f32_e32 v46, v7, v24
	v_and_b32_e32 v7, 0xffffff00, v38
	v_mul_f32_e32 v2, 0x3fb8aa3b, v2
	v_min_f32_e32 v17, v17, v32
	v_exp_f32_e32 v27, v2
	v_sub_f32_e32 v2, v7, v51
	v_max_f32_e32 v39, v31, v8
	v_min_f32_e32 v40, v31, v8
	v_and_b32_e32 v8, 0xffffff00, v17
	v_mul_f32_e32 v2, 0x3fb8aa3b, v2
	v_exp_f32_e32 v28, v2
	v_sub_f32_e32 v2, v8, v51
	v_and_b32_e32 v9, 0xffffff00, v39
	v_mul_f32_e32 v2, 0x3fb8aa3b, v2
	v_exp_f32_e32 v29, v2
	v_sub_f32_e32 v2, v9, v51
	v_and_b32_e32 v31, 0xffffff00, v40
	v_mul_f32_e32 v2, 0x3fb8aa3b, v2
	v_exp_f32_e32 v30, v2
	v_sub_f32_e32 v2, v31, v51
	v_and_b32_e32 v32, 0xffffff00, v41
	v_mul_f32_e32 v2, 0x3fb8aa3b, v2
	v_exp_f32_e32 v31, v2
	v_sub_f32_e32 v2, v32, v51
	v_and_b32_e32 v34, 0xffffff00, v42
	v_mul_f32_e32 v2, 0x3fb8aa3b, v2
	v_exp_f32_e32 v6, v2
	v_sub_f32_e32 v2, v34, v51
	v_and_b32_e32 v35, 0xffffff00, v43
	v_mul_f32_e32 v2, 0x3fb8aa3b, v2
	v_exp_f32_e32 v7, v2
	v_sub_f32_e32 v2, v35, v51
	v_mul_f32_e32 v2, 0x3fb8aa3b, v2
	v_exp_f32_e32 v8, v2
	v_lshl_or_b32 v2, s18, 8, v128
	v_ashrrev_i32_e32 v3, 31, v2
	s_lshl_b64 s[4:5], s[16:17], 18
	v_lshl_add_u64 v[32:33], v[2:3], 4, s[4:5]
	s_mov_b32 s4, 0x7fc000
	v_sub_f32_e32 v24, v51, v51
	v_mul_f32_e32 v24, 0x3fb8aa3b, v24
	v_exp_f32_e32 v24, v24
	s_waitcnt vmcnt(0)
	v_lshrrev_b32_e32 v1, 9, v1
	v_and_or_b32 v2, v1, s4, v0
	v_and_b32_e32 v36, 0xffffff00, v44
	v_and_b32_e32 v37, 0xffffff00, v45
	v_and_b32_e32 v49, 0xffffff00, v46
	v_and_b32_e32 v50, 0xffffff00, v47
	v_and_b32_e32 v52, 0xffffff00, v48
	v_lshrrev_b32_e32 v0, 9, v5
	v_and_or_b32 v3, v0, s4, v4
	v_lshrrev_b32_e32 v0, 9, v11
	v_and_or_b32 v4, v0, s4, v10
	v_lshrrev_b32_e32 v0, 9, v13
	v_and_or_b32 v5, v0, s4, v12
	v_lshlrev_b64 v[12:13], 2, v[32:33]
	v_lshl_add_u64 v[0:1], s[12:13], 0, v[12:13]
	v_mov_b32_e32 v152, v0
	v_mov_b32_e32 v153, v1
	v_lshlrev_b32_e32 v154, 7, v128
	ds_write_b128 v154, v[2:5]
	v_lshl_add_u64 v[10:11], s[6:7], 0, v[20:21]
	v_lshrrev_b32_e32 v32, 2, v40
	v_lshl_add_u64 v[2:3], s[6:7], 0, v[14:15]
	v_lshl_add_u64 v[4:5], s[6:7], 0, v[18:19]
	v_lshl_add_u64 v[14:15], s[6:7], 0, v[22:23]
	global_load_dword v18, v[2:3], off
	global_load_dword v19, v[4:5], off
	global_load_dword v20, v[10:11], off
	global_load_dword v21, v[14:15], off
	v_add_f32_e32 v10, 0, v24
	v_add_f32_e32 v10, v25, v10
	v_add_f32_e32 v10, v26, v10
	v_add_f32_e32 v10, v27, v10
	v_sub_f32_e32 v2, v36, v51
	v_add_f32_e32 v10, v28, v10
	v_mul_f32_e32 v2, 0x3fb8aa3b, v2
	v_add_f32_e32 v10, v29, v10
	v_exp_f32_e32 v9, v2
	v_sub_f32_e32 v2, v37, v51
	v_add_f32_e32 v10, v30, v10
	v_mul_f32_e32 v2, 0x3fb8aa3b, v2
	v_sub_f32_e32 v3, v49, v51
	v_add_f32_e32 v10, v31, v10
	v_exp_f32_e32 v2, v2
	v_mul_f32_e32 v3, 0x3fb8aa3b, v3
	v_sub_f32_e32 v4, v50, v51
	v_add_f32_e32 v10, v6, v10
	v_exp_f32_e32 v3, v3
	v_mul_f32_e32 v4, 0x3fb8aa3b, v4
	v_sub_f32_e32 v5, v52, v51
	v_add_f32_e32 v10, v7, v10
	v_exp_f32_e32 v4, v4
	v_mul_f32_e32 v5, 0x3fb8aa3b, v5
	v_add_f32_e32 v10, v8, v10
	v_exp_f32_e32 v5, v5
	v_add_f32_e32 v10, v9, v10
	v_add_f32_e32 v10, v2, v10
	v_lshrrev_b32_e32 v11, 2, v38
	v_lshrrev_b32_e32 v15, 2, v17
	v_add_f32_e32 v10, v3, v10
	v_and_b32_e32 v11, 60, v11
	v_and_b32_e32 v14, 15, v38
	v_and_b32_e32 v15, 60, v15
	v_and_b32_e32 v17, 15, v17
	v_lshrrev_b32_e32 v22, 2, v39
	v_and_b32_e32 v23, 15, v39
	v_and_b32_e32 v33, 15, v40
	v_add_f32_e32 v10, v4, v10
	v_add_u32_e32 v11, v16, v11
	v_lshl_add_u32 v14, v14, 2, v16
	v_add_u32_e32 v15, v16, v15
	v_lshl_add_u32 v17, v17, 2, v16
	v_and_b32_e32 v22, 60, v22
	v_lshl_add_u32 v23, v23, 2, v16
	v_and_b32_e32 v32, 60, v32
	v_lshl_add_u32 v33, v33, 2, v16
	v_add_f32_e32 v10, v5, v10
	v_add_u32_e32 v22, v16, v22
	v_add_u32_e32 v32, v16, v32
	ds_read_b32 v11, v11
	ds_read_b32 v14, v14 offset:64
	ds_read_b32 v15, v15
	ds_read_b32 v17, v17 offset:64
	ds_read_b32 v34, v22
	ds_read_b32 v23, v23 offset:64
	ds_read_b32 v35, v32
	ds_read_b32 v33, v33 offset:64
	s_waitcnt lgkmcnt(6)
; #define RT_PK(q_) (ex[q_] | (int)((__float_as_uint(usc[ex[q_]]) >> 23) << 14))
;     __device__ __forceinline__ void fused(f32x4 (&acc)[2][2][4][2], const Unit& u, int wr, int wc, int fr, int fq, PG8_LAS unsigned char* lds, int wid, int lane) const {
;     ...
;             for (int q = 0; q < 16; ++q) { sc[q] = __builtin_amdgcn_exp2f((sc[q] - smax) * 1.4426950408889634f); }
; #pragma unroll
;             for (int q = 0; q < 16; ++q) sum += sc[q];
;             const float rs = 1.0f / sum;
;             asm volatile("s_waitcnt lgkmcnt(0)" ::: "memory");
;             int ex[16];
; #pragma unroll
;             for (int q = 0; q < 16; ++q) { const unsigned cid = __float_as_uint(best[q]) & 255u; ex[q] = idxl[cid >> 4] * 128 + idxl[16 + (cid & 15u)]; }
;             const size_t o = ((size_t)u.pn * 16384 + (size_t)(u.pm * BM + row)) * 16;
;             typedef int i32x4 __attribute__((ext_vector_type(4)));
; #pragma unroll
;             for (int i = 0; i < 4; ++i) {
;     ...
;                 *(i32x4*)(eidx + o + 4 * i) = (i32x4){RT_PK(4 * i), RT_PK(4 * i + 1), RT_PK(4 * i + 2), RT_PK(4 * i + 3)};
;                 *(f32x4*)(egate + o + 4 * i) = (f32x4){sc[4 * i] * rs * vsc[ex[4 * i]], sc[4 * i + 1] * rs * vsc[ex[4 * i + 1]], sc[4 * i + 2] * rs * vsc[ex[4 * i + 2]], sc[4 * i + 3] * rs * vsc[ex[4 * i + 3]]};
	v_lshl_add_u32 v14, v11, 7, v14
	v_div_scale_f32 v11, s[16:17], v10, v10, 1.0
	v_rcp_f32_e32 v36, v11
	s_waitcnt lgkmcnt(4)
	v_lshl_add_u32 v22, v15, 7, v17
	s_waitcnt lgkmcnt(2)
	v_lshl_add_u32 v32, v34, 7, v23
	s_waitcnt lgkmcnt(0)
	v_lshl_add_u32 v34, v35, 7, v33
	v_fma_f32 v15, -v11, v36, 1.0
	v_fmac_f32_e32 v36, v15, v36
	v_div_scale_f32 v15, vcc, 1.0, v10, 1.0
	v_mul_f32_e32 v17, v15, v36
	v_fma_f32 v23, -v11, v17, v15
	v_fmac_f32_e32 v17, v23, v36
	v_fma_f32 v11, -v11, v17, v15
	v_div_fmas_f32 v11, v11, v36, v17
	v_div_fixup_f32 v10, v11, v10, 1.0
	v_pk_mul_f32 v[24:25], v[24:25], v[10:11] op_sel_hi:[1,0]
	v_pk_mul_f32 v[26:27], v[26:27], v[10:11] op_sel_hi:[1,0]
	v_ashrrev_i32_e32 v15, 31, v14
	v_ashrrev_i32_e32 v33, 31, v32
	v_lshl_add_u64 v[12:13], s[10:11], 0, v[12:13]
	v_ashrrev_i32_e32 v23, 31, v22
	v_lshlrev_b64 v[36:37], 2, v[32:33]
	v_lshl_add_u64 v[38:39], s[8:9], 0, v[36:37]
	v_ashrrev_i32_e32 v35, 31, v34
	s_waitcnt vmcnt(2)
	v_pk_mul_f32 v[18:19], v[24:25], v[18:19]
	v_lshlrev_b64 v[24:25], 2, v[14:15]
	s_waitcnt vmcnt(0)
	v_pk_mul_f32 v[20:21], v[26:27], v[20:21]
	ds_write_b128 v154, v[18:21] offset:64
	v_lshlrev_b64 v[26:27], 2, v[22:23]
	s_nop 0
	v_lshl_add_u64 v[18:19], s[8:9], 0, v[24:25]
	v_lshl_add_u64 v[20:21], s[8:9], 0, v[26:27]
	global_load_dword v11, v[18:19], off
	global_load_dword v15, v[20:21], off
	global_load_dword v17, v[38:39], off
	v_lshlrev_b64 v[38:39], 2, v[34:35]
	v_lshl_add_u64 v[18:19], s[8:9], 0, v[38:39]
	global_load_dword v21, v[18:19], off
	s_waitcnt vmcnt(3)
	v_lshrrev_b32_e32 v11, 9, v11
	v_and_or_b32 v18, v11, s4, v14
	s_waitcnt vmcnt(2)
	v_lshrrev_b32_e32 v11, 9, v15
	v_and_or_b32 v19, v11, s4, v22
	s_waitcnt vmcnt(1)
	v_lshrrev_b32_e32 v11, 9, v17
	v_and_or_b32 v20, v11, s4, v32
	s_waitcnt vmcnt(0)
	v_lshrrev_b32_e32 v11, 9, v21
	v_and_or_b32 v21, v11, s4, v34
	ds_write_b128 v154, v[18:21] offset:16
	v_lshl_add_u64 v[14:15], s[6:7], 0, v[24:25]
	v_lshl_add_u64 v[22:23], s[6:7], 0, v[38:39]
	v_lshl_add_u64 v[18:19], s[6:7], 0, v[26:27]
	v_lshl_add_u64 v[20:21], s[6:7], 0, v[36:37]
	global_load_dword v24, v[14:15], off
	global_load_dword v26, v[20:21], off
	global_load_dword v27, v[22:23], off
	global_load_dword v25, v[18:19], off
	v_lshrrev_b32_e32 v11, 2, v41
	v_lshrrev_b32_e32 v15, 2, v42
	v_lshrrev_b32_e32 v18, 2, v43
	v_lshrrev_b32_e32 v20, 2, v44
	v_and_b32_e32 v11, 60, v11
	v_and_b32_e32 v14, 15, v41
	v_and_b32_e32 v15, 60, v15
	v_and_b32_e32 v17, 15, v42
	v_and_b32_e32 v18, 60, v18
	v_and_b32_e32 v19, 15, v43
	v_and_b32_e32 v20, 60, v20
	v_and_b32_e32 v21, 15, v44
	v_add_u32_e32 v11, v16, v11
	v_lshl_add_u32 v14, v14, 2, v16
	v_add_u32_e32 v15, v16, v15
	v_lshl_add_u32 v17, v17, 2, v16
	v_add_u32_e32 v18, v16, v18
	v_lshl_add_u32 v19, v19, 2, v16
	v_add_u32_e32 v20, v16, v20
	v_lshl_add_u32 v21, v21, 2, v16
	ds_read_b32 v11, v11
	ds_read_b32 v14, v14 offset:64
	ds_read_b32 v15, v15
	ds_read_b32 v17, v17 offset:64
	ds_read_b32 v18, v18
	ds_read_b32 v19, v19 offset:64
	ds_read_b32 v20, v20
	ds_read_b32 v21, v21 offset:64
	s_waitcnt lgkmcnt(6)
	v_lshl_add_u32 v14, v11, 7, v14
	s_waitcnt lgkmcnt(4)
	v_lshl_add_u32 v22, v15, 7, v17
	s_waitcnt lgkmcnt(2)
	v_lshl_add_u32 v32, v18, 7, v19
	v_pk_mul_f32 v[18:19], v[28:29], v[10:11] op_sel_hi:[1,0]
	s_waitcnt lgkmcnt(0)
	v_lshl_add_u32 v34, v20, 7, v21
	v_pk_mul_f32 v[20:21], v[30:31], v[10:11] op_sel_hi:[1,0]
	v_ashrrev_i32_e32 v15, 31, v14
	v_ashrrev_i32_e32 v33, 31, v32
	v_ashrrev_i32_e32 v23, 31, v22
	v_lshlrev_b64 v[28:29], 2, v[32:33]
	v_lshl_add_u64 v[30:31], s[8:9], 0, v[28:29]
	v_ashrrev_i32_e32 v35, 31, v34
	s_waitcnt vmcnt(1)
	v_pk_mul_f32 v[20:21], v[20:21], v[26:27]
	s_waitcnt vmcnt(0)
	v_pk_mul_f32 v[18:19], v[18:19], v[24:25]
	v_lshlrev_b64 v[24:25], 2, v[14:15]
	ds_write_b128 v154, v[18:21] offset:80
	v_lshlrev_b64 v[26:27], 2, v[22:23]
	s_nop 0
	v_lshl_add_u64 v[18:19], s[8:9], 0, v[24:25]
	v_lshl_add_u64 v[20:21], s[8:9], 0, v[26:27]
	global_load_dword v11, v[18:19], off
	global_load_dword v15, v[20:21], off
	global_load_dword v17, v[30:31], off
	v_lshlrev_b64 v[30:31], 2, v[34:35]
	v_lshl_add_u64 v[18:19], s[8:9], 0, v[30:31]
	global_load_dword v21, v[18:19], off
	s_waitcnt vmcnt(3)
	v_lshrrev_b32_e32 v11, 9, v11
	v_and_or_b32 v18, v11, s4, v14
	s_waitcnt vmcnt(2)
; #define RT_PK(q_) (ex[q_] | (int)((__float_as_uint(usc[ex[q_]]) >> 23) << 14))
;     __device__ __forceinline__ void fused(f32x4 (&acc)[2][2][4][2], const Unit& u, int wr, int wc, int fr, int fq, PG8_LAS unsigned char* lds, int wid, int lane) const {
;     ...
;             for (int q = 0; q < 16; ++q) { const unsigned cid = __float_as_uint(best[q]) & 255u; ex[q] = idxl[cid >> 4] * 128 + idxl[16 + (cid & 15u)]; }
;             const size_t o = ((size_t)u.pn * 16384 + (size_t)(u.pm * BM + row)) * 16;
;             typedef int i32x4 __attribute__((ext_vector_type(4)));
; #pragma unroll
;             for (int i = 0; i < 4; ++i) {
;     ...
;                 *(i32x4*)(eidx + o + 4 * i) = (i32x4){RT_PK(4 * i), RT_PK(4 * i + 1), RT_PK(4 * i + 2), RT_PK(4 * i + 3)};
;                 *(f32x4*)(egate + o + 4 * i) = (f32x4){sc[4 * i] * rs * vsc[ex[4 * i]], sc[4 * i + 1] * rs * vsc[ex[4 * i + 1]], sc[4 * i + 2] * rs * vsc[ex[4 * i + 2]], sc[4 * i + 3] * rs * vsc[ex[4 * i + 3]]};
;             }
	v_lshrrev_b32_e32 v11, 9, v15
	v_and_or_b32 v19, v11, s4, v22
	s_waitcnt vmcnt(1)
	v_lshrrev_b32_e32 v11, 9, v17
	v_and_or_b32 v20, v11, s4, v32
	s_waitcnt vmcnt(0)
	v_lshrrev_b32_e32 v11, 9, v21
	v_and_or_b32 v21, v11, s4, v34
	ds_write_b128 v154, v[18:21] offset:32
	v_lshl_add_u64 v[14:15], s[6:7], 0, v[24:25]
	v_lshl_add_u64 v[22:23], s[6:7], 0, v[30:31]
	v_lshl_add_u64 v[18:19], s[6:7], 0, v[26:27]
	v_lshl_add_u64 v[20:21], s[6:7], 0, v[28:29]
	global_load_dword v24, v[14:15], off
	global_load_dword v26, v[20:21], off
	global_load_dword v27, v[22:23], off
	global_load_dword v25, v[18:19], off
	v_lshrrev_b32_e32 v11, 2, v45
	v_lshrrev_b32_e32 v15, 2, v46
	v_lshrrev_b32_e32 v18, 2, v47
	v_lshrrev_b32_e32 v20, 2, v48
	v_and_b32_e32 v11, 60, v11
	v_and_b32_e32 v14, 15, v45
	v_and_b32_e32 v15, 60, v15
	v_and_b32_e32 v17, 15, v46
	v_and_b32_e32 v18, 60, v18
	v_and_b32_e32 v19, 15, v47
	v_and_b32_e32 v20, 60, v20
	v_add_u32_e32 v11, v16, v11
	v_lshl_add_u32 v14, v14, 2, v16
	v_add_u32_e32 v15, v16, v15
	v_lshl_add_u32 v17, v17, 2, v16
	v_add_u32_e32 v18, v16, v18
	v_lshl_add_u32 v19, v19, 2, v16
	v_add_u32_e32 v20, v16, v20
	v_and_b32_e32 v21, 15, v48
	v_lshl_add_u32 v16, v21, 2, v16
	ds_read_b32 v11, v11
	ds_read_b32 v14, v14 offset:64
	ds_read_b32 v15, v15
	ds_read_b32 v17, v17 offset:64
	ds_read_b32 v18, v18
	ds_read_b32 v19, v19 offset:64
	ds_read_b32 v20, v20
	ds_read_b32 v21, v16 offset:64
	s_waitcnt lgkmcnt(6)
	v_lshl_add_u32 v14, v11, 7, v14
	s_waitcnt lgkmcnt(4)
	v_lshl_add_u32 v16, v15, 7, v17
	s_waitcnt lgkmcnt(2)
	v_lshl_add_u32 v18, v18, 7, v19
	v_pk_mul_f32 v[6:7], v[6:7], v[10:11] op_sel_hi:[1,0]
	v_pk_mul_f32 v[8:9], v[8:9], v[10:11] op_sel_hi:[1,0]
	v_ashrrev_i32_e32 v15, 31, v14
	v_ashrrev_i32_e32 v19, 31, v18
	s_waitcnt lgkmcnt(0)
	v_lshl_add_u32 v20, v20, 7, v21
	v_lshlrev_b64 v[22:23], 2, v[14:15]
	v_ashrrev_i32_e32 v17, 31, v16
	v_ashrrev_i32_e32 v21, 31, v20
	s_waitcnt vmcnt(1)
	v_pk_mul_f32 v[8:9], v[8:9], v[26:27]
	s_waitcnt vmcnt(0)
	v_pk_mul_f32 v[6:7], v[6:7], v[24:25]
	v_lshlrev_b64 v[26:27], 2, v[18:19]
	ds_write_b128 v154, v[6:9] offset:96
	v_lshlrev_b64 v[24:25], 2, v[16:17]
	v_lshl_add_u64 v[28:29], s[8:9], 0, v[26:27]
	v_lshl_add_u64 v[6:7], s[8:9], 0, v[22:23]
	v_lshl_add_u64 v[8:9], s[8:9], 0, v[24:25]
	global_load_dword v11, v[6:7], off
	global_load_dword v15, v[8:9], off
	global_load_dword v17, v[28:29], off
	v_lshlrev_b64 v[28:29], 2, v[20:21]
	v_lshl_add_u64 v[6:7], s[8:9], 0, v[28:29]
	global_load_dword v9, v[6:7], off
	s_waitcnt vmcnt(3)
	v_lshrrev_b32_e32 v6, 9, v11
	s_waitcnt vmcnt(2)
	v_lshrrev_b32_e32 v7, 9, v15
	s_waitcnt vmcnt(1)
	v_lshrrev_b32_e32 v8, 9, v17
	v_and_or_b32 v6, v6, s4, v14
	v_and_or_b32 v7, v7, s4, v16
	s_waitcnt vmcnt(0)
	v_lshrrev_b32_e32 v9, 9, v9
	v_and_or_b32 v8, v8, s4, v18
	v_and_or_b32 v9, v9, s4, v20
	ds_write_b128 v154, v[6:9] offset:48
	v_lshl_add_u64 v[0:1], s[6:7], 0, v[22:23]
	v_lshl_add_u64 v[14:15], s[6:7], 0, v[28:29]
	v_lshl_add_u64 v[6:7], s[6:7], 0, v[24:25]
	v_lshl_add_u64 v[8:9], s[6:7], 0, v[26:27]
	global_load_dword v16, v[0:1], off
	global_load_dword v18, v[8:9], off
	global_load_dword v19, v[14:15], off
	global_load_dword v17, v[6:7], off
	v_pk_mul_f32 v[0:1], v[2:3], v[10:11] op_sel_hi:[1,0]
	v_pk_mul_f32 v[2:3], v[4:5], v[10:11] op_sel_hi:[1,0]
	s_waitcnt vmcnt(0)
	v_pk_mul_f32 v[0:1], v[0:1], v[16:17]
	v_pk_mul_f32 v[2:3], v[2:3], v[18:19]
	ds_write_b128 v154, v[0:3] offset:112
	s_waitcnt lgkmcnt(0)
	ds_read_b128 v[156:159], v154
	ds_read_b128 v[160:163], v154 offset:16
	ds_read_b128 v[164:167], v154 offset:32
	ds_read_b128 v[168:171], v154 offset:48
	ds_read_b128 v[172:175], v154 offset:64
	ds_read_b128 v[176:179], v154 offset:80
	ds_read_b128 v[180:183], v154 offset:96
	ds_read_b128 v[184:187], v154 offset:112
	s_waitcnt lgkmcnt(0)
	global_store_dwordx4 v[152:153], v[156:159], off
	global_store_dwordx4 v[152:153], v[160:163], off offset:16
	global_store_dwordx4 v[152:153], v[164:167], off offset:32
	global_store_dwordx4 v[152:153], v[168:171], off offset:48
	global_store_dwordx4 v[12:13], v[172:175], off
	global_store_dwordx4 v[12:13], v[176:179], off offset:16
	global_store_dwordx4 v[12:13], v[180:183], off offset:32
	global_store_dwordx4 v[12:13], v[184:187], off offset:48

; #define PG8_LAS __attribute__((address_space(3)))
;     __device__ __forceinline__ void fused(f32x4 (&acc)[2][2][4][2], const Unit& u, int wr, int wc, int fr, int fq, PG8_LAS unsigned char* lds, int wid, int lane) const {
;     ...
;         if (half == 0) {
;             PG8_LAS int* idxl = (PG8_LAS int*)(lds + 65536) + row * 32;
;             float v0[16], v1[16];
; #pragma unroll
;             for (int q = 0; q < 16; ++q) { const unsigned b0 = __float_as_uint(top0[q]), b1 = __float_as_uint(top1[q]);
;                 v0[q] = __uint_as_float(b0 & ~127u); v1[q] = __uint_as_float(b1 & ~127u); idxl[q] = (int)(b0 & 127u); idxl[16 + q] = (int)(b1 & 127u); }
;             float best[16];
;             { float cv[16]; cv[0] = __uint_as_float((__float_as_uint(v0[0] + v1[0]) & ~255u) | 0u); cv[1] = __uint_as_float((__float_as_uint(v0[0] + v1[1]) & ~255u) | 1u); cv[2] = __uint_as_float((__float_as_uint(v0[0] + v1[2]) & ~255u) | 2u); cv[3] = __uint_as_float((__float_as_uint(v0[0] + v1[3]) & ~255u) | 3u); cv[4] = __uint_as_float((__float_as_uint(v0[0] + v1[4]) & ~255u) | 4u); cv[5] = __uint_as_float((__float_as_uint(v0[0] + v1[5]) & ~255u) | 5u); cv[6] = __uint_as_float((__float_as_uint(v0[0] + v1[6]) & ~255u) | 6u); cv[7] = __uint_as_float((__float_as_uint(v0[0] + v1[7]) & ~255u) | 7u); cv[8] = __uint_as_float((__float_as_uint(v0[0] + v1[8]) & ~255u) | 8u); cv[9] = __uint_as_float((__float_as_uint(v0[0] + v1[9]) & ~255u) | 9u); cv[10] = __uint_as_float((__float_as_uint(v0[0] + v1[10]) & ~255u) | 10u); cv[11] = __uint_as_float((__float_as_uint(v0[0] + v1[11]) & ~255u) | 11u); cv[12] = __uint_as_float((__float_as_uint(v0[0] + v1[12]) & ~255u) | 12u); cv[13] = __uint_as_float((__float_as_uint(v0[0] + v1[13]) & ~255u) | 13u); cv[14] = __uint_as_float((__float_as_uint(v0[0] + v1[14]) & ~255u) | 14u); cv[15] = __uint_as_float((__float_as_uint(v0[0] + v1[15]) & ~255u) | 15u); sort16_desc(cv);
; #pragma unroll
;               for (int q = 0; q < 16; ++q) best[q] = cv[q]; }
.LBB0_606:
	s_waitcnt lgkmcnt(0)
	s_barrier
	s_and_b64 vcc, exec, s[4:5]
	s_cbranch_vccnz .LBB0_608
	v_lshl_add_u32 v16, v128, 7, 0
	v_add_u32_e32 v16, 0x10000, v16
	v_and_b32_e32 v17, 0xffffff80, v12
	v_and_b32_e32 v18, 0xffffff80, v13
	v_and_b32_e32 v21, 0x7f, v77
	v_and_b32_e32 v20, 0x7f, v76
	v_and_b32_e32 v13, 0x7f, v13
	v_and_b32_e32 v12, 0x7f, v12
	v_and_b32_e32 v26, 0xffffff80, v14
	v_and_b32_e32 v28, 0xffffff80, v15
	v_and_b32_e32 v23, 0x7f, v79
	v_and_b32_e32 v22, 0x7f, v78
	v_and_b32_e32 v15, 0x7f, v15
	v_and_b32_e32 v14, 0x7f, v14
	ds_write_b128 v16, v[20:23]
	ds_write_b128 v16, v[12:15] offset:64
	v_and_b32_e32 v21, 0xffffff80, v8
	v_and_b32_e32 v23, 0xffffff80, v9
	v_and_b32_e32 v13, 0x7f, v73
	v_and_b32_e32 v12, 0x7f, v72
	v_and_b32_e32 v9, 0x7f, v9
	v_and_b32_e32 v8, 0x7f, v8
	v_and_b32_e32 v30, 0xffffff80, v10
	v_and_b32_e32 v32, 0xffffff80, v11
	v_and_b32_e32 v15, 0x7f, v75
	v_and_b32_e32 v14, 0x7f, v74
	v_and_b32_e32 v11, 0x7f, v11
	v_and_b32_e32 v10, 0x7f, v10
	v_and_b32_e32 v19, 0xffffff80, v76
	ds_write_b128 v16, v[12:15] offset:16
	ds_write_b128 v16, v[8:11] offset:80
	v_and_b32_e32 v13, 0xffffff80, v4
	v_and_b32_e32 v15, 0xffffff80, v5
	v_and_b32_e32 v9, 0x7f, v69
	v_and_b32_e32 v8, 0x7f, v68
	v_and_b32_e32 v5, 0x7f, v5
	v_and_b32_e32 v4, 0x7f, v4
	v_and_b32_e32 v34, 0xffffff80, v6
	v_and_b32_e32 v36, 0xffffff80, v7
	v_and_b32_e32 v11, 0x7f, v71
	v_and_b32_e32 v10, 0x7f, v70
	v_and_b32_e32 v7, 0x7f, v7
	v_and_b32_e32 v6, 0x7f, v6
	ds_write_b128 v16, v[8:11] offset:32
	ds_write_b128 v16, v[4:7] offset:96
	v_and_b32_e32 v5, 0x7f, v65
	v_and_b32_e32 v4, 0x7f, v64
	v_and_b32_e32 v41, 0xffffff80, v2
	v_and_b32_e32 v42, 0xffffff80, v3
	v_and_b32_e32 v7, 0x7f, v67
	v_and_b32_e32 v6, 0x7f, v66
	v_and_b32_e32 v11, 0x7f, v3
	v_and_b32_e32 v10, 0x7f, v2
	v_add_f32_e32 v2, v19, v17
	s_movk_i32 s3, 0xff00
	v_add_f32_e32 v3, v19, v18
	v_and_b32_e32 v24, 0xffffff80, v77
	ds_write_b128 v16, v[4:7] offset:48
	v_and_b32_e32 v2, 0xffffff00, v2
	v_and_or_b32 v3, v3, s3, 1
	v_add_f32_e32 v4, v19, v26
	v_add_f32_e32 v5, v19, v28
	v_and_b32_e32 v40, 0xffffff80, v1
	v_and_b32_e32 v9, 0x7f, v1
	v_and_b32_e32 v8, 0x7f, v0
	v_and_or_b32 v4, v4, s3, 2
	v_and_or_b32 v5, v5, s3, 3
	v_add_f32_e32 v48, v24, v17
	v_add_f32_e32 v49, v24, v18
	ds_write_b128 v16, v[8:11] offset:112
	v_add_f32_e32 v6, v19, v21
	v_add_f32_e32 v7, v19, v23
	v_add_f32_e32 v11, v19, v15
	v_add_f32_e32 v15, v19, v36
	v_add_f32_e32 v36, v19, v40
	v_max_f32_e32 v40, v2, v3
	v_min_f32_e32 v2, v2, v3
	v_max_f32_e32 v3, v5, v5
	v_and_or_b32 v48, v48, s3, 16
	v_and_or_b32 v49, v49, s3, 17
	v_add_f32_e32 v50, v24, v26
	v_add_f32_e32 v51, v24, v28
	v_and_or_b32 v6, v6, s3, 4
	v_and_or_b32 v7, v7, s3, 5
	v_add_f32_e32 v8, v19, v30
	v_add_f32_e32 v9, v19, v32
	v_max_f32_e32 v5, v4, v3
	v_min_f32_e32 v3, v4, v3
	v_and_or_b32 v50, v50, s3, 18
	v_and_or_b32 v51, v51, s3, 19
	v_and_or_b32 v8, v8, s3, 6
	v_and_or_b32 v9, v9, s3, 7
	v_max_f32_e32 v4, v40, v5
	v_min_f32_e32 v5, v40, v5
	v_max_f32_e32 v40, v2, v3
	v_add_f32_e32 v52, v24, v21
	v_add_f32_e32 v23, v24, v23
	v_add_f32_e32 v30, v24, v30
	v_add_f32_e32 v24, v24, v32
	v_max_f32_e32 v58, v48, v49
	v_min_f32_e32 v48, v48, v49
	v_max_f32_e32 v49, v51, v51
	v_min_f32_e32 v2, v2, v3
	v_max_f32_e32 v3, v40, v5
	v_min_f32_e32 v5, v40, v5
	v_max_f32_e32 v40, v6, v7
	v_min_f32_e32 v6, v6, v7
	v_max_f32_e32 v7, v9, v9
	v_and_or_b32 v52, v52, s3, 20
	v_and_or_b32 v23, v23, s3, 21
	v_and_or_b32 v30, v30, s3, 22
	v_and_or_b32 v24, v24, s3, 23
	v_max_f32_e32 v51, v50, v49
	v_min_f32_e32 v49, v50, v49
	v_max_f32_e32 v9, v8, v7
	v_min_f32_e32 v7, v8, v7
	v_max_f32_e32 v50, v58, v51
	v_min_f32_e32 v51, v58, v51
	v_max_f32_e32 v58, v48, v49
	v_max_f32_e32 v8, v40, v9
	v_min_f32_e32 v9, v40, v9
	v_max_f32_e32 v40, v6, v7
	v_min_f32_e32 v48, v48, v49
	v_max_f32_e32 v49, v58, v51
	v_min_f32_e32 v51, v58, v51
	v_max_f32_e32 v58, v52, v23
	v_min_f32_e32 v23, v52, v23
	v_max_f32_e32 v52, v30, v24
	v_min_f32_e32 v24, v30, v24
	v_min_f32_e32 v6, v6, v7
	v_max_f32_e32 v7, v40, v9
	v_min_f32_e32 v9, v40, v9
	v_max_f32_e32 v30, v58, v52
	v_min_f32_e32 v52, v58, v52
	v_max_f32_e32 v58, v23, v24
	v_max_f32_e32 v40, v4, v8
	v_min_f32_e32 v4, v4, v8
	v_max_f32_e32 v8, v5, v9
	v_min_f32_e32 v23, v23, v24
	v_max_f32_e32 v24, v58, v52
	v_min_f32_e32 v52, v58, v52
	v_and_b32_e32 v25, 0xffffff80, v78
	v_add_f32_e32 v10, v19, v13
	v_min_f32_e32 v5, v5, v9
	v_max_f32_e32 v9, v8, v4
	v_min_f32_e32 v4, v8, v4
	v_max_f32_e32 v8, v3, v7
	v_min_f32_e32 v3, v3, v7
	v_max_f32_e32 v7, v2, v6
	v_max_f32_e32 v58, v50, v30
	v_min_f32_e32 v30, v50, v30
	v_max_f32_e32 v50, v51, v52
	v_and_or_b32 v10, v10, s3, 8
	v_and_or_b32 v11, v11, s3, 9
	v_add_f32_e32 v13, v19, v34
	v_min_f32_e32 v2, v2, v6
	v_max_f32_e32 v6, v7, v3
	v_min_f32_e32 v3, v7, v3
	v_add_f32_e32 v32, v25, v17
	v_add_f32_e32 v53, v25, v18
	v_min_f32_e32 v51, v51, v52
	v_max_f32_e32 v52, v50, v30
	v_min_f32_e32 v30, v50, v30
	v_max_f32_e32 v50, v49, v24
	v_min_f32_e32 v24, v49, v24
	v_max_f32_e32 v49, v48, v23
	v_and_or_b32 v13, v13, s3, 10
	v_and_or_b32 v15, v15, s3, 11
	v_max_f32_e32 v7, v8, v9
	v_min_f32_e32 v8, v8, v9
	v_max_f32_e32 v9, v6, v4
	v_min_f32_e32 v4, v6, v4
	v_max_f32_e32 v6, v3, v5
	v_min_f32_e32 v3, v3, v5
	v_max_f32_e32 v5, v11, v11
	v_and_or_b32 v32, v32, s3, 32
	v_and_or_b32 v53, v53, s3, 33
	v_add_f32_e32 v54, v25, v26
	v_add_f32_e32 v55, v25, v28
	v_min_f32_e32 v23, v48, v23
	v_max_f32_e32 v48, v49, v24
	v_min_f32_e32 v24, v49, v24
	v_and_b32_e32 v27, 0xffffff80, v79
	v_and_b32_e32 v38, 0xffffff80, v0
	v_max_f32_e32 v11, v10, v5
	v_min_f32_e32 v5, v10, v5
	v_max_f32_e32 v10, v15, v15
; __device__ __forceinline__ void sort16_desc(float (&v)[16]) {
;     CE(v[0], v[1]); CE(v[2], v[3]); CE(v[0], v[2]); CE(v[1], v[3]);
;     CE(v[1], v[2]); CE(v[4], v[5]); CE(v[6], v[7]); CE(v[4], v[6]);
;     CE(v[5], v[7]); CE(v[5], v[6]); CE(v[0], v[4]); CE(v[2], v[6]);
;     CE(v[2], v[4]); CE(v[1], v[5]); CE(v[3], v[7]); CE(v[3], v[5]);
;     CE(v[1], v[2]); CE(v[3], v[4]); CE(v[5], v[6]); CE(v[8], v[9]);
;     CE(v[10], v[11]); CE(v[8], v[10]); CE(v[9], v[11]); CE(v[9], v[10]);
;     CE(v[12], v[13]); CE(v[14], v[15]); CE(v[12], v[14]); CE(v[13], v[15]);
;     CE(v[13], v[14]); CE(v[8], v[12]); CE(v[10], v[14]); CE(v[10], v[12]);
;     CE(v[9], v[13]); CE(v[11], v[15]); CE(v[11], v[13]); CE(v[9], v[10]);
;     CE(v[11], v[12]); CE(v[13], v[14]); CE(v[0], v[8]); CE(v[4], v[12]);
;     CE(v[4], v[8]); CE(v[2], v[10]); CE(v[6], v[14]); CE(v[6], v[10]);
;     CE(v[2], v[4]); CE(v[6], v[8]); CE(v[10], v[12]); CE(v[1], v[9]);
;     CE(v[5], v[13]); CE(v[5], v[9]); CE(v[3], v[11]); CE(v[7], v[15]);
;     CE(v[7], v[11]); CE(v[3], v[5]); CE(v[7], v[9]); CE(v[11], v[13]);
;     CE(v[1], v[2]); CE(v[3], v[4]); CE(v[5], v[6]); CE(v[7], v[8]);
;     CE(v[9], v[10]); CE(v[11], v[12]); CE(v[13], v[14]);
; }
; __device__ __forceinline__ void merge_top16(float (&v)[16], const float (&nw)[16]) {
;     v[0] = fmaxf(v[0], nw[15]); v[1] = fmaxf(v[1], nw[14]); v[2] = fmaxf(v[2], nw[13]); v[3] = fmaxf(v[3], nw[12]); v[4] = fmaxf(v[4], nw[11]); v[5] = fmaxf(v[5], nw[10]); v[6] = fmaxf(v[6], nw[9]); v[7] = fmaxf(v[7], nw[8]); v[8] = fmaxf(v[8], nw[7]); v[9] = fmaxf(v[9], nw[6]); v[10] = fmaxf(v[10], nw[5]); v[11] = fmaxf(v[11], nw[4]); v[12] = fmaxf(v[12], nw[3]); v[13] = fmaxf(v[13], nw[2]); v[14] = fmaxf(v[14], nw[1]); v[15] = fmaxf(v[15], nw[0]);
;     CE(v[0], v[8]); CE(v[1], v[9]); CE(v[2], v[10]); CE(v[3], v[11]);
;     CE(v[4], v[12]); CE(v[5], v[13]); CE(v[6], v[14]); CE(v[7], v[15]);
;     CE(v[0], v[4]); CE(v[1], v[5]); CE(v[2], v[6]); CE(v[3], v[7]);
;     CE(v[8], v[12]); CE(v[9], v[13]); CE(v[10], v[14]); CE(v[11], v[15]);
;     CE(v[0], v[2]); CE(v[1], v[3]); CE(v[4], v[6]); CE(v[5], v[7]);
;     CE(v[8], v[10]); CE(v[9], v[11]); CE(v[12], v[14]); CE(v[13], v[15]);
;     CE(v[0], v[1]); CE(v[2], v[3]); CE(v[4], v[5]); CE(v[6], v[7]);
;     CE(v[8], v[9]); CE(v[10], v[11]); CE(v[12], v[13]); CE(v[14], v[15]);
; }
	v_and_or_b32 v54, v54, s3, 34
	v_and_or_b32 v55, v55, s3, 35
	v_max_f32_e32 v49, v50, v52
	v_min_f32_e32 v50, v50, v52
	v_max_f32_e32 v52, v48, v30
	v_min_f32_e32 v30, v48, v30
	v_max_f32_e32 v48, v24, v51
	v_min_f32_e32 v24, v24, v51
	v_max_f32_e32 v51, v53, v53
	v_add_f32_e32 v34, v19, v38
	v_max_f32_e32 v15, v13, v10
	v_min_f32_e32 v10, v13, v10
	v_add_f32_e32 v21, v25, v21
	v_add_f32_e32 v25, v27, v17
	v_max_f32_e32 v53, v32, v51
	v_min_f32_e32 v32, v32, v51
	v_max_f32_e32 v51, v55, v55
	v_and_or_b32 v34, v34, s3, 12
	v_and_or_b32 v36, v36, s3, 13
	v_add_f32_e32 v38, v19, v41
	v_add_f32_e32 v19, v19, v42
	v_max_f32_e32 v13, v11, v15
	v_min_f32_e32 v11, v11, v15
	v_max_f32_e32 v15, v5, v10
	v_and_or_b32 v21, v21, s3, 36
	v_and_or_b32 v25, v25, s3, 48
	v_add_f32_e32 v56, v27, v18
	v_add_f32_e32 v57, v27, v26
	v_max_f32_e32 v55, v54, v51
	v_min_f32_e32 v51, v54, v51
	v_and_or_b32 v38, v38, s3, 14
	v_and_or_b32 v19, v19, s3, 15
	v_min_f32_e32 v5, v5, v10
	v_max_f32_e32 v10, v15, v11
	v_min_f32_e32 v11, v15, v11
	v_max_f32_e32 v15, v36, v36
	v_and_or_b32 v56, v56, s3, 49
	v_and_or_b32 v57, v57, s3, 50
	v_max_f32_e32 v54, v53, v55
	v_min_f32_e32 v53, v53, v55
	v_max_f32_e32 v55, v32, v51
	v_max_f32_e32 v36, v34, v15
	v_min_f32_e32 v15, v34, v15
	v_max_f32_e32 v34, v38, v38
	v_min_f32_e32 v32, v32, v51
	v_max_f32_e32 v51, v55, v53
	v_min_f32_e32 v53, v55, v53
	v_max_f32_e32 v55, v21, v25
	v_min_f32_e32 v21, v21, v25
	v_max_f32_e32 v25, v57, v57
	v_max_f32_e32 v38, v34, v19
	v_min_f32_e32 v19, v34, v19
	v_max_f32_e32 v57, v56, v25
	v_min_f32_e32 v25, v56, v25
	v_max_f32_e32 v34, v36, v38
	v_min_f32_e32 v36, v36, v38
	v_max_f32_e32 v38, v15, v19
	v_max_f32_e32 v56, v55, v57
	v_min_f32_e32 v55, v55, v57
	v_max_f32_e32 v57, v21, v25
	v_min_f32_e32 v15, v15, v19
	v_max_f32_e32 v19, v38, v36
	v_min_f32_e32 v36, v38, v36
	v_min_f32_e32 v21, v21, v25
	v_max_f32_e32 v25, v57, v55
	v_min_f32_e32 v55, v57, v55
	v_max_f32_e32 v38, v13, v34
	v_min_f32_e32 v13, v13, v34
	v_max_f32_e32 v34, v11, v36
	v_max_f32_e32 v57, v54, v56
	v_min_f32_e32 v54, v54, v56
	v_max_f32_e32 v56, v53, v55
	v_min_f32_e32 v11, v11, v36
	v_max_f32_e32 v36, v34, v13
	v_min_f32_e32 v13, v34, v13
	v_max_f32_e32 v34, v10, v19
	v_min_f32_e32 v10, v10, v19
	v_max_f32_e32 v19, v5, v15
	v_min_f32_e32 v53, v53, v55
	v_max_f32_e32 v55, v56, v54
	v_min_f32_e32 v54, v56, v54
	v_max_f32_e32 v56, v51, v25
	v_min_f32_e32 v25, v51, v25
	v_max_f32_e32 v51, v32, v21
	v_min_f32_e32 v5, v5, v15
	v_max_f32_e32 v15, v19, v10
	v_min_f32_e32 v21, v32, v21
	v_max_f32_e32 v32, v51, v25
	v_min_f32_e32 v10, v19, v10
	v_max_f32_e32 v19, v34, v36
	v_min_f32_e32 v34, v34, v36
	v_max_f32_e32 v36, v15, v13
	v_min_f32_e32 v13, v15, v13
	v_min_f32_e32 v25, v51, v25
	v_max_f32_e32 v51, v56, v55
	v_min_f32_e32 v55, v56, v55
	v_max_f32_e32 v56, v32, v54
	v_min_f32_e32 v32, v32, v54
	v_max_f32_e32 v15, v10, v11
	v_min_f32_e32 v10, v10, v11
	v_min_f32_e32 v11, v40, v38
	v_max_f32_e32 v41, v4, v13
	v_max_f32_e32 v54, v25, v53
	v_min_f32_e32 v25, v25, v53
	v_min_f32_e32 v53, v58, v57
	v_max_f32_e32 v59, v30, v32
	v_min_f32_e32 v4, v4, v13
	v_max_f32_e32 v13, v41, v11
	v_min_f32_e32 v11, v41, v11
	v_max_f32_e32 v41, v8, v34
	v_min_f32_e32 v8, v8, v34
	v_max_f32_e32 v34, v3, v10
	v_min_f32_e32 v30, v30, v32
	v_max_f32_e32 v32, v59, v53
	v_min_f32_e32 v53, v59, v53
	v_max_f32_e32 v59, v50, v55
	v_min_f32_e32 v50, v50, v55
	v_max_f32_e32 v55, v24, v25
	v_min_f32_e32 v3, v3, v10
	v_max_f32_e32 v10, v34, v8
	v_min_f32_e32 v8, v34, v8
	v_min_f32_e32 v24, v24, v25
	v_max_f32_e32 v25, v55, v50
	v_min_f32_e32 v50, v55, v50
	v_max_f32_e32 v34, v41, v13
	v_min_f32_e32 v13, v41, v13
	v_max_f32_e32 v41, v10, v11
	v_min_f32_e32 v10, v10, v11
	v_max_f32_e32 v11, v8, v4
	v_min_f32_e32 v4, v8, v4
	v_max_f32_e32 v8, v7, v19
	v_min_f32_e32 v7, v7, v19
	v_max_f32_e32 v19, v6, v15
	v_max_f32_e32 v55, v59, v32
	v_min_f32_e32 v32, v59, v32
	v_max_f32_e32 v59, v25, v53
	v_min_f32_e32 v25, v25, v53
	v_max_f32_e32 v53, v50, v30
	v_min_f32_e32 v30, v50, v30
	v_max_f32_e32 v50, v49, v51
	v_min_f32_e32 v49, v49, v51
	v_max_f32_e32 v51, v48, v54
	v_min_f32_e32 v6, v6, v15
	v_max_f32_e32 v15, v19, v7
	v_min_f32_e32 v7, v19, v7
	v_max_f32_e32 v19, v9, v36
	v_min_f32_e32 v9, v9, v36
	v_max_f32_e32 v36, v2, v5
	v_min_f32_e32 v48, v48, v54
	v_max_f32_e32 v54, v51, v49
	v_min_f32_e32 v49, v51, v49
	v_max_f32_e32 v51, v52, v56
	v_min_f32_e32 v52, v52, v56
	v_max_f32_e32 v56, v23, v21
	v_min_f32_e32 v2, v2, v5
	v_max_f32_e32 v5, v36, v9
	v_min_f32_e32 v9, v36, v9
	v_max_f32_e32 v36, v19, v15
	v_min_f32_e32 v21, v23, v21
	v_max_f32_e32 v23, v56, v52
	v_min_f32_e32 v52, v56, v52
	v_and_b32_e32 v20, 0xffffff80, v72
	v_min_f32_e32 v15, v19, v15
	v_max_f32_e32 v19, v5, v7
	v_min_f32_e32 v5, v5, v7
	v_max_f32_e32 v7, v9, v6
	v_min_f32_e32 v6, v9, v6
	v_min_f32_e32 v9, v8, v34
	v_min_f32_e32 v42, v36, v13
	v_max_f32_e32 v56, v51, v54
	v_min_f32_e32 v51, v51, v54
	v_max_f32_e32 v54, v23, v49
	v_min_f32_e32 v23, v23, v49
	v_max_f32_e32 v49, v52, v48
	v_min_f32_e32 v48, v52, v48
	v_and_b32_e32 v39, 0xffffff80, v65
	v_min_f32_e32 v65, v48, v24
	v_max3_f32 v9, v9, v48, v24
	v_max3_f32 v24, v42, v49, v30
	v_add_f32_e32 v27, v27, v28
	v_add_f32_e32 v28, v20, v17
	v_add_f32_e32 v42, v20, v18
	v_add_f32_e32 v20, v20, v26
	v_and_b32_e32 v22, 0xffffff80, v73
	v_and_or_b32 v27, v27, s3, 51
	v_and_or_b32 v28, v28, s3, 64
	v_and_b32_e32 v42, 0xffffff00, v42
	v_and_b32_e32 v20, 0xffffff00, v20
	v_and_b32_e32 v29, 0xffffff80, v74
	v_and_b32_e32 v31, 0xffffff80, v75
	v_and_b32_e32 v33, 0xffffff80, v70
	v_and_b32_e32 v35, 0xffffff80, v71
	v_and_b32_e32 v37, 0xffffff80, v64
; __device__ __forceinline__ void sort16_desc(float (&v)[16]) {
;     CE(v[0], v[1]); CE(v[2], v[3]); CE(v[0], v[2]); CE(v[1], v[3]);
;     CE(v[1], v[2]); CE(v[4], v[5]); CE(v[6], v[7]); CE(v[4], v[6]);
;     CE(v[5], v[7]); CE(v[5], v[6]); CE(v[0], v[4]); CE(v[2], v[6]);
;     CE(v[2], v[4]); CE(v[1], v[5]); CE(v[3], v[7]); CE(v[3], v[5]);
;     CE(v[1], v[2]); CE(v[3], v[4]); CE(v[5], v[6]); CE(v[8], v[9]);
;     CE(v[10], v[11]); CE(v[8], v[10]); CE(v[9], v[11]); CE(v[9], v[10]);
;     CE(v[12], v[13]); CE(v[14], v[15]); CE(v[12], v[14]); CE(v[13], v[15]);
;     CE(v[13], v[14]); CE(v[8], v[12]); CE(v[10], v[14]); CE(v[10], v[12]);
;     CE(v[9], v[13]); CE(v[11], v[15]); CE(v[11], v[13]); CE(v[9], v[10]);
;     CE(v[11], v[12]); CE(v[13], v[14]); CE(v[0], v[8]); CE(v[4], v[12]);
;     CE(v[4], v[8]); CE(v[2], v[10]); CE(v[6], v[14]); CE(v[6], v[10]);
;     CE(v[2], v[4]); CE(v[6], v[8]); CE(v[10], v[12]); CE(v[1], v[9]);
;     CE(v[5], v[13]); CE(v[5], v[9]); CE(v[3], v[11]); CE(v[7], v[15]);
;     CE(v[7], v[11]); CE(v[3], v[5]); CE(v[7], v[9]); CE(v[11], v[13]);
;     CE(v[1], v[2]); CE(v[3], v[4]); CE(v[5], v[6]); CE(v[7], v[8]);
;     CE(v[9], v[10]); CE(v[11], v[12]); CE(v[13], v[14]);
; }
; __device__ __forceinline__ void merge_top16(float (&v)[16], const float (&nw)[16]) {
;     v[0] = fmaxf(v[0], nw[15]); v[1] = fmaxf(v[1], nw[14]); v[2] = fmaxf(v[2], nw[13]); v[3] = fmaxf(v[3], nw[12]); v[4] = fmaxf(v[4], nw[11]); v[5] = fmaxf(v[5], nw[10]); v[6] = fmaxf(v[6], nw[9]); v[7] = fmaxf(v[7], nw[8]); v[8] = fmaxf(v[8], nw[7]); v[9] = fmaxf(v[9], nw[6]); v[10] = fmaxf(v[10], nw[5]); v[11] = fmaxf(v[11], nw[4]); v[12] = fmaxf(v[12], nw[3]); v[13] = fmaxf(v[13], nw[2]); v[14] = fmaxf(v[14], nw[1]); v[15] = fmaxf(v[15], nw[0]);
;     CE(v[0], v[8]); CE(v[1], v[9]); CE(v[2], v[10]); CE(v[3], v[11]);
;     CE(v[4], v[12]); CE(v[5], v[13]); CE(v[6], v[14]); CE(v[7], v[15]);
;     CE(v[0], v[4]); CE(v[1], v[5]); CE(v[2], v[6]); CE(v[3], v[7]);
;     CE(v[8], v[12]); CE(v[9], v[13]); CE(v[10], v[14]); CE(v[11], v[15]);
;     CE(v[0], v[2]); CE(v[1], v[3]); CE(v[4], v[6]); CE(v[5], v[7]);
;     CE(v[8], v[10]); CE(v[9], v[11]); CE(v[12], v[14]); CE(v[13], v[15]);
;     CE(v[0], v[1]); CE(v[2], v[3]); CE(v[4], v[5]); CE(v[6], v[7]);
;     CE(v[8], v[9]); CE(v[10], v[11]); CE(v[12], v[13]); CE(v[14], v[15]);
; }
	v_min_f32_e32 v43, v15, v41
	v_min_f32_e32 v44, v19, v10
	v_min_f32_e32 v62, v54, v25
	v_or_b32_e32 v42, 0x41, v42
	v_or_b32_e32 v20, 0x42, v20
	v_add_f32_e32 v26, v22, v17
	v_add_f32_e32 v22, v22, v18
	v_min_f32_e32 v63, v23, v53
	v_max3_f32 v23, v43, v23, v53
	v_max3_f32 v10, v19, v10, v62
	v_max3_f32 v19, v44, v54, v25
	v_and_b32_e32 v26, 0xffffff00, v26
	v_and_b32_e32 v22, 0xffffff00, v22
	v_add_f32_e32 v43, v29, v17
	v_add_f32_e32 v29, v29, v18
	v_add_f32_e32 v44, v31, v17
	v_add_f32_e32 v18, v31, v18
	v_add_f32_e32 v31, v33, v17
	v_add_f32_e32 v33, v35, v17
	v_add_f32_e32 v35, v37, v17
	v_add_f32_e32 v37, v39, v17
	v_max_f32_e32 v39, v27, v28
	v_min_f32_e32 v27, v27, v28
	v_max_f32_e32 v28, v42, v42
	v_or_b32_e32 v26, 0x50, v26
	v_or_b32_e32 v22, 0x51, v22
	v_and_b32_e32 v43, 0xffffff00, v43
	v_and_b32_e32 v29, 0xffffff00, v29
	v_max_f32_e32 v42, v28, v20
	v_min_f32_e32 v20, v28, v20
	v_or_b32_e32 v43, 0x60, v43
	v_or_b32_e32 v29, 0x61, v29
	v_max_f32_e32 v28, v39, v42
	v_min_f32_e32 v39, v39, v42
	v_max_f32_e32 v42, v27, v20
	v_min_f32_e32 v20, v27, v20
	v_max_f32_e32 v27, v42, v39
	v_min_f32_e32 v39, v42, v39
	v_max_f32_e32 v42, v26, v22
	v_min_f32_e32 v22, v26, v22
	v_max_f32_e32 v26, v29, v29
	v_max_f32_e32 v29, v43, v43
	v_max_f32_e32 v43, v29, v26
	v_min_f32_e32 v26, v29, v26
	v_max_f32_e32 v29, v42, v43
	v_min_f32_e32 v42, v42, v43
	v_max_f32_e32 v43, v22, v26
	v_and_b32_e32 v12, 0xffffff80, v68
	v_and_b32_e32 v14, 0xffffff80, v69
	v_min_f32_e32 v22, v22, v26
	v_max_f32_e32 v26, v43, v42
	v_min_f32_e32 v42, v43, v42
	v_add_f32_e32 v12, v12, v17
	v_add_f32_e32 v14, v14, v17
	v_max_f32_e32 v43, v28, v29
	v_min_f32_e32 v28, v28, v29
	v_max_f32_e32 v29, v39, v42
	v_and_b32_e32 v44, 0xffffff00, v44
	v_and_b32_e32 v18, 0xffffff00, v18
	v_and_b32_e32 v12, 0xffffff00, v12
	v_and_b32_e32 v14, 0xffffff00, v14
	v_min_f32_e32 v39, v39, v42
	v_max_f32_e32 v42, v29, v28
	v_min_f32_e32 v28, v29, v28
	v_max_f32_e32 v29, v27, v26
	v_min_f32_e32 v26, v27, v26
	v_max_f32_e32 v27, v20, v22
	v_or_b32_e32 v44, 0x70, v44
	v_or_b32_e32 v18, 0x71, v18
	v_or_b32_e32 v12, 0x80, v12
	v_or_b32_e32 v14, 0x90, v14
	v_min_f32_e32 v20, v20, v22
	v_max_f32_e32 v22, v27, v26
	v_min_f32_e32 v26, v27, v26
	v_and_b32_e32 v31, 0xffffff00, v31
	v_and_b32_e32 v33, 0xffffff00, v33
	v_max_f32_e32 v27, v29, v42
	v_min_f32_e32 v29, v29, v42
	v_max_f32_e32 v42, v22, v28
	v_min_f32_e32 v22, v22, v28
	v_max_f32_e32 v28, v26, v39
	v_min_f32_e32 v26, v26, v39
	v_max_f32_e32 v39, v44, v44
	v_or_b32_e32 v31, 0xa0, v31
	v_or_b32_e32 v33, 0xb0, v33
	v_and_b32_e32 v35, 0xffffff00, v35
	v_and_b32_e32 v37, 0xffffff00, v37
	v_max_f32_e32 v44, v39, v18
	v_min_f32_e32 v18, v39, v18
	v_max_f32_e32 v39, v12, v14
	v_min_f32_e32 v12, v12, v14
	v_or_b32_e32 v35, 0xc0, v35
	v_or_b32_e32 v37, 0xd0, v37
	v_max_f32_e32 v14, v44, v39
	v_min_f32_e32 v39, v44, v39
	v_max_f32_e32 v44, v18, v12
	v_min_f32_e32 v12, v18, v12
	v_max_f32_e32 v18, v44, v39
	v_min_f32_e32 v39, v44, v39
	v_max_f32_e32 v44, v31, v33
	v_min_f32_e32 v31, v31, v33
	v_max_f32_e32 v33, v37, v37
	v_max_f32_e32 v37, v35, v33
	v_min_f32_e32 v33, v35, v33
	v_max_f32_e32 v35, v44, v37
	v_min_f32_e32 v37, v44, v37
	v_max_f32_e32 v44, v31, v33
	v_min_f32_e32 v31, v31, v33
	v_max_f32_e32 v33, v44, v37
	v_min_f32_e32 v37, v44, v37
	v_max_f32_e32 v44, v14, v35
	v_min_f32_e32 v14, v14, v35
	v_max_f32_e32 v35, v39, v37
	v_min_f32_e32 v37, v39, v37
	v_max_f32_e32 v39, v35, v14
	v_min_f32_e32 v14, v35, v14
	v_max_f32_e32 v35, v18, v33
	v_min_f32_e32 v18, v18, v33
	v_max_f32_e32 v33, v12, v31
	v_min_f32_e32 v12, v12, v31
	v_max_f32_e32 v31, v33, v18
	v_min_f32_e32 v45, v5, v11
	v_min_f32_e32 v61, v51, v59
	v_min_f32_e32 v18, v33, v18
	v_max_f32_e32 v33, v35, v39
	v_min_f32_e32 v35, v35, v39
	v_max_f32_e32 v39, v31, v14
	v_min_f32_e32 v14, v31, v14
	v_max3_f32 v5, v5, v11, v61
	v_max3_f32 v11, v45, v51, v59
	v_max_f32_e32 v31, v18, v37
	v_min_f32_e32 v18, v18, v37
	v_min_f32_e32 v37, v43, v44
	v_max_f32_e32 v45, v22, v14
	v_min_f32_e32 v14, v22, v14
	v_max_f32_e32 v22, v45, v37
	v_min_f32_e32 v37, v45, v37
	v_max_f32_e32 v45, v29, v35
	v_min_f32_e32 v29, v29, v35
	v_max_f32_e32 v35, v26, v18
	v_min_f32_e32 v46, v7, v4
	v_min_f32_e32 v47, v6, v3
	v_min_f32_e32 v52, v50, v55
	v_min_f32_e32 v60, v56, v32
	v_min_f32_e32 v64, v49, v30
	v_min_f32_e32 v18, v26, v18
	v_max_f32_e32 v26, v35, v29
	v_min_f32_e32 v29, v35, v29
	v_max3_f32 v21, v40, v38, v21
	v_max3_f32 v8, v8, v34, v65
	v_max3_f32 v13, v36, v13, v64
	v_max3_f32 v15, v15, v41, v63
	v_max3_f32 v4, v7, v4, v60
	v_max3_f32 v7, v46, v56, v32
	v_max3_f32 v3, v6, v3, v52
	v_max3_f32 v6, v47, v50, v55
	v_max3_f32 v2, v2, v58, v57
	v_max_f32_e32 v35, v45, v22
	v_min_f32_e32 v22, v45, v22
	v_max_f32_e32 v45, v26, v37
	v_min_f32_e32 v26, v26, v37
	v_max_f32_e32 v37, v29, v14
	v_min_f32_e32 v14, v29, v14
	v_max_f32_e32 v29, v27, v33
	v_min_f32_e32 v27, v27, v33
	v_max_f32_e32 v33, v28, v31
	v_max_f32_e32 v25, v21, v19
	v_min_f32_e32 v19, v21, v19
	v_max_f32_e32 v21, v8, v5
	v_min_f32_e32 v5, v8, v5
	v_max_f32_e32 v8, v9, v11
	v_min_f32_e32 v9, v9, v11
	v_max_f32_e32 v11, v13, v4
	v_min_f32_e32 v4, v13, v4
	v_max_f32_e32 v13, v24, v7
	v_min_f32_e32 v7, v24, v7
	v_max_f32_e32 v24, v15, v3
	v_min_f32_e32 v3, v15, v3
	v_max_f32_e32 v15, v23, v6
	v_min_f32_e32 v6, v23, v6
	v_max_f32_e32 v23, v10, v2
	v_min_f32_e32 v2, v10, v2
	v_min_f32_e32 v28, v28, v31
	v_max_f32_e32 v31, v33, v27
	v_min_f32_e32 v27, v33, v27
	v_max_f32_e32 v33, v42, v39
	v_min_f32_e32 v39, v42, v39
	v_max_f32_e32 v42, v20, v12
	v_max_f32_e32 v10, v25, v13
	v_min_f32_e32 v13, v25, v13
	v_max_f32_e32 v25, v21, v24
	v_min_f32_e32 v21, v21, v24
; #define CE(a, b) do { const float hi_ = fmaxf(a, b), lo_ = fminf(a, b); a = hi_; b = lo_; } while (0)
; __device__ __forceinline__ void merge_top16(float (&v)[16], const float (&nw)[16]) {
;     v[0] = fmaxf(v[0], nw[15]); v[1] = fmaxf(v[1], nw[14]); v[2] = fmaxf(v[2], nw[13]); v[3] = fmaxf(v[3], nw[12]); v[4] = fmaxf(v[4], nw[11]); v[5] = fmaxf(v[5], nw[10]); v[6] = fmaxf(v[6], nw[9]); v[7] = fmaxf(v[7], nw[8]); v[8] = fmaxf(v[8], nw[7]); v[9] = fmaxf(v[9], nw[6]); v[10] = fmaxf(v[10], nw[5]); v[11] = fmaxf(v[11], nw[4]); v[12] = fmaxf(v[12], nw[3]); v[13] = fmaxf(v[13], nw[2]); v[14] = fmaxf(v[14], nw[1]); v[15] = fmaxf(v[15], nw[0]);
;     CE(v[0], v[8]); CE(v[1], v[9]); CE(v[2], v[10]); CE(v[3], v[11]);
;     CE(v[4], v[12]); CE(v[5], v[13]); CE(v[6], v[14]); CE(v[7], v[15]);
;     CE(v[0], v[4]); CE(v[1], v[5]); CE(v[2], v[6]); CE(v[3], v[7]);
;     CE(v[8], v[12]); CE(v[9], v[13]); CE(v[10], v[14]); CE(v[11], v[15]);
;     CE(v[0], v[2]); CE(v[1], v[3]); CE(v[4], v[6]); CE(v[5], v[7]);
;     CE(v[8], v[10]); CE(v[9], v[11]); CE(v[12], v[14]); CE(v[13], v[15]);
;     CE(v[0], v[1]); CE(v[2], v[3]); CE(v[4], v[5]); CE(v[6], v[7]);
;     CE(v[8], v[9]); CE(v[10], v[11]); CE(v[12], v[13]); CE(v[14], v[15]);
; }
;     __device__ __forceinline__ void fused(f32x4 (&acc)[2][2][4][2], const Unit& u, int wr, int wc, int fr, int fq, PG8_LAS unsigned char* lds, int wid, int lane) const {
;     ...
;             { float cv[16]; cv[0] = __uint_as_float((__float_as_uint(v0[14] + v1[0]) & ~255u) | 224u); cv[1] = __uint_as_float((__float_as_uint(v0[15] + v1[0]) & ~255u) | 240u); cv[2] = -INFINITY; cv[3] = -INFINITY; cv[4] = -INFINITY; cv[5] = -INFINITY; cv[6] = -INFINITY; cv[7] = -INFINITY; cv[8] = -INFINITY; cv[9] = -INFINITY; cv[10] = -INFINITY; cv[11] = -INFINITY; cv[12] = -INFINITY; cv[13] = -INFINITY; cv[14] = -INFINITY; cv[15] = -INFINITY; sort16_desc(cv); merge_top16(best, cv); }
;             float sc[16], sum = 0.f;
; #pragma unroll
;             for (int q = 0; q < 16; ++q) { sc[q] = __uint_as_float(__float_as_uint(best[q]) & ~255u); }
;             const float smax = sc[0];
; #pragma unroll
;             for (int q = 0; q < 16; ++q) { sc[q] = __builtin_amdgcn_exp2f((sc[q] - smax) * 1.4426950408889634f); }
	v_max_f32_e32 v24, v8, v15
	v_min_f32_e32 v8, v8, v15
	v_max_f32_e32 v15, v11, v23
	v_min_f32_e32 v11, v11, v23
	v_max_f32_e32 v23, v19, v7
	v_min_f32_e32 v7, v19, v7
	v_max_f32_e32 v19, v5, v3
	v_min_f32_e32 v3, v5, v3
	v_max_f32_e32 v5, v9, v6
	v_min_f32_e32 v6, v9, v6
	v_max_f32_e32 v9, v4, v2
	v_min_f32_e32 v2, v4, v2
	v_min_f32_e32 v12, v20, v12
	v_max_f32_e32 v20, v42, v39
	v_min_f32_e32 v39, v42, v39
	v_and_b32_e32 v1, 0xffffff80, v66
	v_and_b32_e32 v0, 0xffffff80, v67
	v_max_f32_e32 v4, v10, v24
	v_min_f32_e32 v10, v10, v24
	v_max_f32_e32 v24, v25, v15
	v_min_f32_e32 v15, v25, v15
	v_max_f32_e32 v25, v13, v8
	v_min_f32_e32 v8, v13, v8
	v_max_f32_e32 v13, v21, v11
	v_min_f32_e32 v11, v21, v11
	v_max_f32_e32 v21, v23, v5
	v_min_f32_e32 v5, v23, v5
	v_max_f32_e32 v23, v19, v9
	v_min_f32_e32 v9, v19, v9
	v_max_f32_e32 v19, v7, v6
	v_min_f32_e32 v6, v7, v6
	v_max_f32_e32 v7, v3, v2
	v_min_f32_e32 v2, v3, v2
	v_max_f32_e32 v42, v33, v31
	v_min_f32_e32 v31, v33, v31
	v_max_f32_e32 v33, v20, v27
	v_min_f32_e32 v20, v20, v27
	v_max_f32_e32 v27, v39, v28
	v_min_f32_e32 v28, v39, v28
	v_min_f32_e32 v3, v4, v24
	v_min_f32_e32 v30, v10, v15
	v_min_f32_e32 v32, v25, v13
	v_min_f32_e32 v34, v8, v11
	v_min_f32_e32 v36, v21, v23
	v_min_f32_e32 v38, v5, v9
	v_min_f32_e32 v40, v19, v7
	v_min_f32_e32 v41, v6, v2
	v_max_f32_e32 v39, v29, v35
	v_min_f32_e32 v29, v29, v35
	v_max_f32_e32 v35, v42, v22
	v_min_f32_e32 v22, v42, v22
	v_max_f32_e32 v42, v31, v45
	v_min_f32_e32 v31, v31, v45
	v_max_f32_e32 v45, v33, v26
	v_min_f32_e32 v26, v33, v26
	v_max_f32_e32 v33, v20, v37
	v_min_f32_e32 v20, v20, v37
	v_max_f32_e32 v37, v27, v14
	v_min_f32_e32 v14, v27, v14
	v_max_f32_e32 v27, v28, v18
	v_min_f32_e32 v18, v28, v18
	v_add_f32_e32 v1, v1, v17
	v_add_f32_e32 v0, v0, v17
	v_max3_f32 v4, v4, v24, v12
	v_max_f32_e32 v3, v3, v18
	v_max3_f32 v10, v10, v15, v27
	v_max_f32_e32 v12, v30, v14
	v_max3_f32 v13, v25, v13, v37
	v_max_f32_e32 v14, v32, v20
	v_max3_f32 v8, v8, v11, v33
	v_max_f32_e32 v11, v34, v26
	v_max3_f32 v15, v21, v23, v45
	v_max_f32_e32 v18, v36, v31
	v_max3_f32 v5, v5, v9, v42
	v_max_f32_e32 v9, v38, v22
	v_max3_f32 v7, v19, v7, v35
	v_max_f32_e32 v19, v40, v29
	v_max3_f32 v2, v6, v2, v39
	v_max3_f32 v6, v41, v43, v44
	v_and_b32_e32 v1, 0xffffff00, v1
	v_and_b32_e32 v0, 0xffffff00, v0
	v_max_f32_e32 v20, v4, v15
	v_min_f32_e32 v4, v4, v15
	v_max_f32_e32 v15, v3, v18
	v_min_f32_e32 v3, v3, v18
	v_max_f32_e32 v18, v10, v5
	v_min_f32_e32 v5, v10, v5
	v_max_f32_e32 v10, v12, v9
	v_min_f32_e32 v9, v12, v9
	v_max_f32_e32 v12, v13, v7
	v_min_f32_e32 v7, v13, v7
	v_max_f32_e32 v13, v14, v19
	v_min_f32_e32 v14, v14, v19
	v_max_f32_e32 v19, v8, v2
	v_min_f32_e32 v2, v8, v2
	v_max_f32_e32 v8, v11, v6
	v_min_f32_e32 v6, v11, v6
	v_or_b32_e32 v1, 0xe0, v1
	v_or_b32_e32 v0, 0xf0, v0
	v_max_f32_e32 v11, v20, v12
	v_min_f32_e32 v12, v20, v12
	v_max_f32_e32 v20, v15, v13
	v_min_f32_e32 v13, v15, v13
	v_max_f32_e32 v15, v18, v19
	v_min_f32_e32 v18, v18, v19
	v_max_f32_e32 v19, v10, v8
	v_min_f32_e32 v8, v10, v8
	v_max_f32_e32 v10, v4, v7
	v_min_f32_e32 v4, v4, v7
	v_max_f32_e32 v7, v3, v14
	v_min_f32_e32 v3, v3, v14
	v_max_f32_e32 v14, v5, v2
	v_min_f32_e32 v2, v5, v2
	v_max_f32_e32 v5, v9, v6
	v_min_f32_e32 v6, v9, v6
	v_max_f32_e32 v9, v11, v15
	v_min_f32_e32 v11, v11, v15
	v_max_f32_e32 v15, v20, v19
	v_min_f32_e32 v19, v20, v19
	v_max_f32_e32 v20, v12, v18
	v_min_f32_e32 v12, v12, v18
	v_max_f32_e32 v18, v13, v8
	v_min_f32_e32 v8, v13, v8
	v_max_f32_e32 v13, v10, v14
	v_min_f32_e32 v10, v10, v14
	v_max_f32_e32 v14, v7, v5
	v_min_f32_e32 v5, v7, v5
	v_max_f32_e32 v7, v4, v2
	v_min_f32_e32 v2, v4, v2
	v_max_f32_e32 v4, v3, v6
	v_min_f32_e32 v3, v3, v6
	v_max_f32_e32 v17, v1, v0
	v_min_f32_e32 v0, v1, v0
	v_min_f32_e32 v6, v9, v15
	v_min_f32_e32 v21, v11, v19
	v_min_f32_e32 v22, v20, v18
	v_min_f32_e32 v23, v12, v8
	v_min_f32_e32 v24, v13, v14
	v_min_f32_e32 v25, v10, v5
	v_min_f32_e32 v26, v7, v4
	v_min_f32_e32 v27, v2, v3
	s_mov_b32 s3, 0xff800000
	v_max_f32_e32 v0, 0xff800000, v0
	v_max3_f32 v1, v9, v15, s3
	v_max_f32_e32 v6, 0xff800000, v6
	v_max3_f32 v9, v11, v19, s3
	v_max_f32_e32 v11, 0xff800000, v21
	v_max3_f32 v15, v20, v18, s3
	v_max_f32_e32 v18, 0xff800000, v22
	v_max3_f32 v8, v12, v8, s3
	v_max_f32_e32 v12, 0xff800000, v23
	v_max3_f32 v13, v13, v14, s3
	v_max_f32_e32 v14, 0xff800000, v24
	v_max3_f32 v5, v10, v5, s3
	v_max_f32_e32 v10, 0xff800000, v25
	v_max3_f32 v4, v7, v4, s3
	v_max_f32_e32 v7, 0xff800000, v26
	v_max3_f32 v0, v2, v3, v0
	v_max3_f32 v2, v27, v17, s3
	v_max_f32_e32 v3, v1, v13
	v_min_f32_e32 v1, v1, v13
	v_max_f32_e32 v13, v6, v14
	v_min_f32_e32 v6, v6, v14
	v_max_f32_e32 v14, v9, v5
	v_min_f32_e32 v5, v9, v5
	v_max_f32_e32 v9, v11, v10
	v_min_f32_e32 v10, v11, v10
	v_max_f32_e32 v11, v15, v4
	v_min_f32_e32 v4, v15, v4
	v_max_f32_e32 v15, v18, v7
	v_max_f32_e32 v17, v8, v0
	v_min_f32_e32 v0, v8, v0
	v_max_f32_e32 v8, v12, v2
	v_min_f32_e32 v2, v12, v2
	v_max_f32_e32 v12, v3, v11
	v_min_f32_e32 v3, v3, v11
	v_max_f32_e32 v11, v13, v15
	v_min_f32_e32 v13, v13, v15
	v_max_f32_e32 v15, v14, v17
	v_min_f32_e32 v14, v14, v17
	v_max_f32_e32 v17, v9, v8
	v_min_f32_e32 v8, v9, v8
	v_max_f32_e32 v9, v1, v4
	v_min_f32_e32 v24, v1, v4
	v_max_f32_e32 v27, v5, v0
	v_min_f32_e32 v28, v5, v0
	v_max_f32_e32 v29, v10, v2
	v_min_f32_e32 v30, v10, v2
	v_max_f32_e32 v0, v12, v15
	v_min_f32_e32 v1, v12, v15
	v_max_f32_e32 v2, v11, v17
	v_min_f32_e32 v4, v11, v17
	v_min_f32_e32 v7, v18, v7
	v_max_f32_e32 v33, v0, v2
	v_min_f32_e32 v34, v0, v2
	v_min_f32_e32 v36, v1, v4
	v_max_f32_e32 v25, v6, v7
	v_min_f32_e32 v26, v6, v7
	v_max_f32_e32 v35, v1, v4
	v_lshrrev_b32_e32 v0, 2, v33
	v_lshrrev_b32_e32 v2, 2, v34
	v_lshrrev_b32_e32 v6, 2, v36
	v_max_f32_e32 v17, v3, v14
	v_min_f32_e32 v31, v3, v14
	v_and_b32_e32 v0, 60, v0
	v_and_b32_e32 v1, 15, v33
	v_and_b32_e32 v2, 60, v2
	v_and_b32_e32 v3, 15, v34
	v_lshrrev_b32_e32 v4, 2, v35
	v_and_b32_e32 v5, 15, v35
	v_and_b32_e32 v6, 60, v6
	v_and_b32_e32 v7, 15, v36
	s_waitcnt lgkmcnt(0)
; #define RT_PK(q_) (ex[q_] | (int)((__float_as_uint(usc[ex[q_]]) >> 23) << 14))
;     __device__ __forceinline__ void fused(f32x4 (&acc)[2][2][4][2], const Unit& u, int wr, int wc, int fr, int fq, PG8_LAS unsigned char* lds, int wid, int lane) const {
;     ...
;             float sc[16], sum = 0.f;
; #pragma unroll
;             for (int q = 0; q < 16; ++q) { sc[q] = __uint_as_float(__float_as_uint(best[q]) & ~255u); }
;             const float smax = sc[0];
; #pragma unroll
;             for (int q = 0; q < 16; ++q) { sc[q] = __builtin_amdgcn_exp2f((sc[q] - smax) * 1.4426950408889634f); }
; #pragma unroll
;             for (int q = 0; q < 16; ++q) sum += sc[q];
;             const float rs = 1.0f / sum;
;             asm volatile("s_waitcnt lgkmcnt(0)" ::: "memory");
;             int ex[16];
; #pragma unroll
;             for (int q = 0; q < 16; ++q) { const unsigned cid = __float_as_uint(best[q]) & 255u; ex[q] = idxl[cid >> 4] * 128 + idxl[16 + (cid & 15u)]; }
;             const size_t o = ((size_t)u.pn * 16384 + (size_t)(u.pm * BM + row)) * 16;
;             typedef int i32x4 __attribute__((ext_vector_type(4)));
; #pragma unroll
;             for (int i = 0; i < 4; ++i) {
;     ...
;                 *(i32x4*)(eidx + o + 4 * i) = (i32x4){RT_PK(4 * i), RT_PK(4 * i + 1), RT_PK(4 * i + 2), RT_PK(4 * i + 3)};
;                 *(f32x4*)(egate + o + 4 * i) = (f32x4){sc[4 * i] * rs * vsc[ex[4 * i]], sc[4 * i + 1] * rs * vsc[ex[4 * i + 1]], sc[4 * i + 2] * rs * vsc[ex[4 * i + 2]], sc[4 * i + 3] * rs * vsc[ex[4 * i + 3]]};
	v_add_u32_e32 v0, v16, v0
	v_lshl_add_u32 v1, v1, 2, v16
	v_add_u32_e32 v2, v16, v2
	v_lshl_add_u32 v3, v3, 2, v16
	v_and_b32_e32 v4, 60, v4
	v_lshl_add_u32 v5, v5, 2, v16
	v_add_u32_e32 v6, v16, v6
	v_lshl_add_u32 v7, v7, 2, v16
	v_add_u32_e32 v4, v16, v4
	ds_read_b32 v0, v0
	ds_read_b32 v1, v1 offset:64
	ds_read_b32 v2, v2
	ds_read_b32 v3, v3 offset:64
	ds_read_b32 v10, v4
	ds_read_b32 v5, v5 offset:64
	ds_read_b32 v6, v6
	ds_read_b32 v7, v7 offset:64
	s_waitcnt lgkmcnt(0)
	v_lshl_add_u32 v0, v0, 7, v1
	v_ashrrev_i32_e32 v1, 31, v0
	v_lshl_add_u32 v4, v2, 7, v3
	v_lshlrev_b64 v[14:15], 2, v[0:1]
	v_lshl_add_u32 v10, v10, 7, v5
	v_lshl_add_u32 v12, v6, 7, v7
	v_lshl_add_u64 v[2:3], s[8:9], 0, v[14:15]
	v_ashrrev_i32_e32 v5, 31, v4
	v_max_f32_e32 v32, v13, v8
	v_min_f32_e32 v8, v13, v8
	global_load_dword v1, v[2:3], off
	v_lshlrev_b64 v[18:19], 2, v[4:5]
	v_ashrrev_i32_e32 v11, 31, v10
	v_ashrrev_i32_e32 v13, 31, v12
	v_lshl_add_u64 v[2:3], s[8:9], 0, v[18:19]
	v_lshlrev_b64 v[20:21], 2, v[10:11]
	v_lshlrev_b64 v[22:23], 2, v[12:13]
	v_lshl_add_u64 v[6:7], s[8:9], 0, v[20:21]
	global_load_dword v5, v[2:3], off
	global_load_dword v11, v[6:7], off
	v_lshl_add_u64 v[2:3], s[8:9], 0, v[22:23]
	global_load_dword v13, v[2:3], off
	v_min_f32_e32 v2, v9, v27
	v_min_f32_e32 v6, v25, v29
	v_max_f32_e32 v43, v2, v6
	v_min_f32_e32 v44, v2, v6
	v_and_b32_e32 v2, 0xffffff00, v34
	v_and_b32_e32 v51, 0xffffff00, v33
	v_max_f32_e32 v37, v9, v27
	v_max_f32_e32 v3, v25, v29
	v_sub_f32_e32 v2, v2, v51
	v_min_f32_e32 v9, v24, v28
	v_min_f32_e32 v25, v26, v30
	v_max_f32_e32 v41, v37, v3
	v_min_f32_e32 v42, v37, v3
	v_and_b32_e32 v3, 0xffffff00, v35
	v_mul_f32_e32 v2, 0x3fb8aa3b, v2
	v_max_f32_e32 v47, v9, v25
	v_min_f32_e32 v48, v9, v25
	v_exp_f32_e32 v25, v2
	v_sub_f32_e32 v2, v3, v51
	v_and_b32_e32 v6, 0xffffff00, v36
	v_mul_f32_e32 v2, 0x3fb8aa3b, v2
	v_max_f32_e32 v7, v24, v28
	v_max_f32_e32 v24, v26, v30
	v_max_f32_e32 v38, v17, v32
	v_exp_f32_e32 v26, v2
	v_sub_f32_e32 v2, v6, v51
	v_max_f32_e32 v45, v7, v24
	v_min_f32_e32 v46, v7, v24
	v_and_b32_e32 v7, 0xffffff00, v38
	v_mul_f32_e32 v2, 0x3fb8aa3b, v2
	v_min_f32_e32 v17, v17, v32
	v_exp_f32_e32 v27, v2
	v_sub_f32_e32 v2, v7, v51
	v_max_f32_e32 v39, v31, v8
	v_min_f32_e32 v40, v31, v8
	v_and_b32_e32 v8, 0xffffff00, v17
	v_mul_f32_e32 v2, 0x3fb8aa3b, v2
	v_exp_f32_e32 v28, v2
	v_sub_f32_e32 v2, v8, v51
	v_and_b32_e32 v9, 0xffffff00, v39
	v_mul_f32_e32 v2, 0x3fb8aa3b, v2
	v_exp_f32_e32 v29, v2
	v_sub_f32_e32 v2, v9, v51
	v_and_b32_e32 v31, 0xffffff00, v40
	v_mul_f32_e32 v2, 0x3fb8aa3b, v2
	v_exp_f32_e32 v30, v2
	v_sub_f32_e32 v2, v31, v51
	v_and_b32_e32 v32, 0xffffff00, v41
	v_mul_f32_e32 v2, 0x3fb8aa3b, v2
	v_exp_f32_e32 v31, v2
	v_sub_f32_e32 v2, v32, v51
	v_and_b32_e32 v34, 0xffffff00, v42
	v_mul_f32_e32 v2, 0x3fb8aa3b, v2
	v_exp_f32_e32 v6, v2
	v_sub_f32_e32 v2, v34, v51
	v_and_b32_e32 v35, 0xffffff00, v43
	v_mul_f32_e32 v2, 0x3fb8aa3b, v2
	v_exp_f32_e32 v7, v2
	v_sub_f32_e32 v2, v35, v51
	v_mul_f32_e32 v2, 0x3fb8aa3b, v2
	v_exp_f32_e32 v8, v2
	v_lshl_or_b32 v2, s18, 8, v128
	v_ashrrev_i32_e32 v3, 31, v2
	s_lshl_b64 s[4:5], s[16:17], 18
	s_mov_b32 s3, 0x7fc000
	v_lshl_add_u64 v[32:33], v[2:3], 4, s[4:5]
	v_sub_f32_e32 v24, v51, v51
	v_mul_f32_e32 v24, 0x3fb8aa3b, v24
	v_exp_f32_e32 v24, v24
	s_waitcnt vmcnt(0)
	v_lshrrev_b32_e32 v1, 9, v1
	v_and_or_b32 v2, v1, s3, v0
	v_and_b32_e32 v36, 0xffffff00, v44
	v_and_b32_e32 v37, 0xffffff00, v45
	v_and_b32_e32 v49, 0xffffff00, v46
	v_and_b32_e32 v50, 0xffffff00, v47
	v_and_b32_e32 v52, 0xffffff00, v48
	v_lshrrev_b32_e32 v0, 9, v5
	v_and_or_b32 v3, v0, s3, v4
	v_lshrrev_b32_e32 v0, 9, v11
	v_and_or_b32 v4, v0, s3, v10
	v_lshrrev_b32_e32 v0, 9, v13
	v_and_or_b32 v5, v0, s3, v12
	v_lshlrev_b64 v[12:13], 2, v[32:33]
	v_lshl_add_u64 v[0:1], s[12:13], 0, v[12:13]
	v_mov_b32_e32 v152, v0
	v_mov_b32_e32 v153, v1
	v_lshlrev_b32_e32 v154, 7, v128
	ds_write_b128 v154, v[2:5]
	v_lshl_add_u64 v[10:11], s[6:7], 0, v[20:21]
	v_lshrrev_b32_e32 v32, 2, v40
	v_lshl_add_u64 v[2:3], s[6:7], 0, v[14:15]
	v_lshl_add_u64 v[4:5], s[6:7], 0, v[18:19]
	v_lshl_add_u64 v[14:15], s[6:7], 0, v[22:23]
	global_load_dword v18, v[2:3], off
	global_load_dword v19, v[4:5], off
	global_load_dword v20, v[10:11], off
	global_load_dword v21, v[14:15], off
	v_add_f32_e32 v10, 0, v24
	v_add_f32_e32 v10, v25, v10
	v_add_f32_e32 v10, v26, v10
	v_add_f32_e32 v10, v27, v10
	v_sub_f32_e32 v2, v36, v51
	v_add_f32_e32 v10, v28, v10
	v_mul_f32_e32 v2, 0x3fb8aa3b, v2
	v_add_f32_e32 v10, v29, v10
	v_exp_f32_e32 v9, v2
	v_sub_f32_e32 v2, v37, v51
	v_add_f32_e32 v10, v30, v10
	v_mul_f32_e32 v2, 0x3fb8aa3b, v2
	v_sub_f32_e32 v3, v49, v51
	v_add_f32_e32 v10, v31, v10
	v_exp_f32_e32 v2, v2
	v_mul_f32_e32 v3, 0x3fb8aa3b, v3
	v_sub_f32_e32 v4, v50, v51
	v_add_f32_e32 v10, v6, v10
	v_exp_f32_e32 v3, v3
	v_mul_f32_e32 v4, 0x3fb8aa3b, v4
	v_sub_f32_e32 v5, v52, v51
	v_add_f32_e32 v10, v7, v10
	v_exp_f32_e32 v4, v4
	v_mul_f32_e32 v5, 0x3fb8aa3b, v5
	v_add_f32_e32 v10, v8, v10
	v_exp_f32_e32 v5, v5
	v_add_f32_e32 v10, v9, v10
	v_add_f32_e32 v10, v2, v10
	v_lshrrev_b32_e32 v11, 2, v38
	v_lshrrev_b32_e32 v15, 2, v17
	v_add_f32_e32 v10, v3, v10
	v_and_b32_e32 v11, 60, v11
	v_and_b32_e32 v14, 15, v38
	v_and_b32_e32 v15, 60, v15
	v_and_b32_e32 v17, 15, v17
	v_lshrrev_b32_e32 v22, 2, v39
	v_and_b32_e32 v23, 15, v39
	v_and_b32_e32 v33, 15, v40
	v_add_f32_e32 v10, v4, v10
	v_add_u32_e32 v11, v16, v11
	v_lshl_add_u32 v14, v14, 2, v16
	v_add_u32_e32 v15, v16, v15
	v_lshl_add_u32 v17, v17, 2, v16
	v_and_b32_e32 v22, 60, v22
	v_lshl_add_u32 v23, v23, 2, v16
	v_and_b32_e32 v32, 60, v32
	v_lshl_add_u32 v33, v33, 2, v16
	v_add_f32_e32 v10, v5, v10
	v_add_u32_e32 v22, v16, v22
	v_add_u32_e32 v32, v16, v32
	ds_read_b32 v11, v11
	ds_read_b32 v14, v14 offset:64
	ds_read_b32 v15, v15
	ds_read_b32 v17, v17 offset:64
	ds_read_b32 v34, v22
	ds_read_b32 v23, v23 offset:64
	ds_read_b32 v35, v32
	ds_read_b32 v33, v33 offset:64
	s_waitcnt lgkmcnt(6)
; #define RT_PK(q_) (ex[q_] | (int)((__float_as_uint(usc[ex[q_]]) >> 23) << 14))
;     __device__ __forceinline__ void fused(f32x4 (&acc)[2][2][4][2], const Unit& u, int wr, int wc, int fr, int fq, PG8_LAS unsigned char* lds, int wid, int lane) const {
;     ...
;             for (int q = 0; q < 16; ++q) { sc[q] = __builtin_amdgcn_exp2f((sc[q] - smax) * 1.4426950408889634f); }
; #pragma unroll
;             for (int q = 0; q < 16; ++q) sum += sc[q];
;             const float rs = 1.0f / sum;
;             asm volatile("s_waitcnt lgkmcnt(0)" ::: "memory");
;             int ex[16];
; #pragma unroll
;             for (int q = 0; q < 16; ++q) { const unsigned cid = __float_as_uint(best[q]) & 255u; ex[q] = idxl[cid >> 4] * 128 + idxl[16 + (cid & 15u)]; }
;             const size_t o = ((size_t)u.pn * 16384 + (size_t)(u.pm * BM + row)) * 16;
;             typedef int i32x4 __attribute__((ext_vector_type(4)));
; #pragma unroll
;             for (int i = 0; i < 4; ++i) {
;     ...
;                 *(i32x4*)(eidx + o + 4 * i) = (i32x4){RT_PK(4 * i), RT_PK(4 * i + 1), RT_PK(4 * i + 2), RT_PK(4 * i + 3)};
;                 *(f32x4*)(egate + o + 4 * i) = (f32x4){sc[4 * i] * rs * vsc[ex[4 * i]], sc[4 * i + 1] * rs * vsc[ex[4 * i + 1]], sc[4 * i + 2] * rs * vsc[ex[4 * i + 2]], sc[4 * i + 3] * rs * vsc[ex[4 * i + 3]]};
	v_lshl_add_u32 v14, v11, 7, v14
	v_div_scale_f32 v11, s[4:5], v10, v10, 1.0
	v_rcp_f32_e32 v36, v11
	s_waitcnt lgkmcnt(4)
	v_lshl_add_u32 v22, v15, 7, v17
	s_waitcnt lgkmcnt(2)
	v_lshl_add_u32 v32, v34, 7, v23
	s_waitcnt lgkmcnt(0)
	v_lshl_add_u32 v34, v35, 7, v33
	v_fma_f32 v15, -v11, v36, 1.0
	v_fmac_f32_e32 v36, v15, v36
	v_div_scale_f32 v15, vcc, 1.0, v10, 1.0
	v_mul_f32_e32 v17, v15, v36
	v_fma_f32 v23, -v11, v17, v15
	v_fmac_f32_e32 v17, v23, v36
	v_fma_f32 v11, -v11, v17, v15
	v_div_fmas_f32 v11, v11, v36, v17
	v_div_fixup_f32 v10, v11, v10, 1.0
	v_pk_mul_f32 v[24:25], v[24:25], v[10:11] op_sel_hi:[1,0]
	v_pk_mul_f32 v[26:27], v[26:27], v[10:11] op_sel_hi:[1,0]
	v_ashrrev_i32_e32 v15, 31, v14
	v_ashrrev_i32_e32 v33, 31, v32
	v_lshl_add_u64 v[12:13], s[10:11], 0, v[12:13]
	v_ashrrev_i32_e32 v23, 31, v22
	v_lshlrev_b64 v[36:37], 2, v[32:33]
	v_lshl_add_u64 v[38:39], s[8:9], 0, v[36:37]
	v_ashrrev_i32_e32 v35, 31, v34
	s_waitcnt vmcnt(2)
	v_pk_mul_f32 v[18:19], v[24:25], v[18:19]
	v_lshlrev_b64 v[24:25], 2, v[14:15]
	s_waitcnt vmcnt(0)
	v_pk_mul_f32 v[20:21], v[26:27], v[20:21]
	ds_write_b128 v154, v[18:21] offset:64
	v_lshlrev_b64 v[26:27], 2, v[22:23]
	s_nop 0
	v_lshl_add_u64 v[18:19], s[8:9], 0, v[24:25]
	v_lshl_add_u64 v[20:21], s[8:9], 0, v[26:27]
	global_load_dword v11, v[18:19], off
	global_load_dword v15, v[20:21], off
	global_load_dword v17, v[38:39], off
	v_lshlrev_b64 v[38:39], 2, v[34:35]
	v_lshl_add_u64 v[18:19], s[8:9], 0, v[38:39]
	global_load_dword v21, v[18:19], off
	s_waitcnt vmcnt(3)
	v_lshrrev_b32_e32 v11, 9, v11
	v_and_or_b32 v18, v11, s3, v14
	s_waitcnt vmcnt(2)
	v_lshrrev_b32_e32 v11, 9, v15
	v_and_or_b32 v19, v11, s3, v22
	s_waitcnt vmcnt(1)
	v_lshrrev_b32_e32 v11, 9, v17
	v_and_or_b32 v20, v11, s3, v32
	s_waitcnt vmcnt(0)
	v_lshrrev_b32_e32 v11, 9, v21
	v_and_or_b32 v21, v11, s3, v34
	ds_write_b128 v154, v[18:21] offset:16
	v_lshl_add_u64 v[14:15], s[6:7], 0, v[24:25]
	v_lshl_add_u64 v[22:23], s[6:7], 0, v[38:39]
	v_lshl_add_u64 v[18:19], s[6:7], 0, v[26:27]
	v_lshl_add_u64 v[20:21], s[6:7], 0, v[36:37]
	global_load_dword v24, v[14:15], off
	global_load_dword v26, v[20:21], off
	global_load_dword v27, v[22:23], off
	global_load_dword v25, v[18:19], off
	v_lshrrev_b32_e32 v11, 2, v41
	v_lshrrev_b32_e32 v15, 2, v42
	v_lshrrev_b32_e32 v18, 2, v43
	v_lshrrev_b32_e32 v20, 2, v44
	v_and_b32_e32 v11, 60, v11
	v_and_b32_e32 v14, 15, v41
	v_and_b32_e32 v15, 60, v15
	v_and_b32_e32 v17, 15, v42
	v_and_b32_e32 v18, 60, v18
	v_and_b32_e32 v19, 15, v43
	v_and_b32_e32 v20, 60, v20
	v_and_b32_e32 v21, 15, v44
	v_add_u32_e32 v11, v16, v11
	v_lshl_add_u32 v14, v14, 2, v16
	v_add_u32_e32 v15, v16, v15
	v_lshl_add_u32 v17, v17, 2, v16
	v_add_u32_e32 v18, v16, v18
	v_lshl_add_u32 v19, v19, 2, v16
	v_add_u32_e32 v20, v16, v20
	v_lshl_add_u32 v21, v21, 2, v16
	ds_read_b32 v11, v11
	ds_read_b32 v14, v14 offset:64
	ds_read_b32 v15, v15
	ds_read_b32 v17, v17 offset:64
	ds_read_b32 v18, v18
	ds_read_b32 v19, v19 offset:64
	ds_read_b32 v20, v20
	ds_read_b32 v21, v21 offset:64
	s_waitcnt lgkmcnt(6)
	v_lshl_add_u32 v14, v11, 7, v14
	s_waitcnt lgkmcnt(4)
	v_lshl_add_u32 v22, v15, 7, v17
	s_waitcnt lgkmcnt(2)
	v_lshl_add_u32 v32, v18, 7, v19
	v_pk_mul_f32 v[18:19], v[28:29], v[10:11] op_sel_hi:[1,0]
	s_waitcnt lgkmcnt(0)
	v_lshl_add_u32 v34, v20, 7, v21
	v_pk_mul_f32 v[20:21], v[30:31], v[10:11] op_sel_hi:[1,0]
	v_ashrrev_i32_e32 v15, 31, v14
	v_ashrrev_i32_e32 v33, 31, v32
	v_ashrrev_i32_e32 v23, 31, v22
	v_lshlrev_b64 v[28:29], 2, v[32:33]
	v_lshl_add_u64 v[30:31], s[8:9], 0, v[28:29]
	v_ashrrev_i32_e32 v35, 31, v34
	s_waitcnt vmcnt(1)
	v_pk_mul_f32 v[20:21], v[20:21], v[26:27]
	s_waitcnt vmcnt(0)
	v_pk_mul_f32 v[18:19], v[18:19], v[24:25]
	v_lshlrev_b64 v[24:25], 2, v[14:15]
	ds_write_b128 v154, v[18:21] offset:80
	v_lshlrev_b64 v[26:27], 2, v[22:23]
	s_nop 0
	v_lshl_add_u64 v[18:19], s[8:9], 0, v[24:25]
	v_lshl_add_u64 v[20:21], s[8:9], 0, v[26:27]
	global_load_dword v11, v[18:19], off
	global_load_dword v15, v[20:21], off
	global_load_dword v17, v[30:31], off
	v_lshlrev_b64 v[30:31], 2, v[34:35]
	v_lshl_add_u64 v[18:19], s[8:9], 0, v[30:31]
	global_load_dword v21, v[18:19], off
	s_waitcnt vmcnt(3)
	v_lshrrev_b32_e32 v11, 9, v11
	v_and_or_b32 v18, v11, s3, v14
	s_waitcnt vmcnt(2)
; #define RT_PK(q_) (ex[q_] | (int)((__float_as_uint(usc[ex[q_]]) >> 23) << 14))
;     __device__ __forceinline__ void fused(f32x4 (&acc)[2][2][4][2], const Unit& u, int wr, int wc, int fr, int fq, PG8_LAS unsigned char* lds, int wid, int lane) const {
;     ...
;             for (int q = 0; q < 16; ++q) { const unsigned cid = __float_as_uint(best[q]) & 255u; ex[q] = idxl[cid >> 4] * 128 + idxl[16 + (cid & 15u)]; }
;             const size_t o = ((size_t)u.pn * 16384 + (size_t)(u.pm * BM + row)) * 16;
;             typedef int i32x4 __attribute__((ext_vector_type(4)));
; #pragma unroll
;             for (int i = 0; i < 4; ++i) {
;     ...
;                 *(i32x4*)(eidx + o + 4 * i) = (i32x4){RT_PK(4 * i), RT_PK(4 * i + 1), RT_PK(4 * i + 2), RT_PK(4 * i + 3)};
;                 *(f32x4*)(egate + o + 4 * i) = (f32x4){sc[4 * i] * rs * vsc[ex[4 * i]], sc[4 * i + 1] * rs * vsc[ex[4 * i + 1]], sc[4 * i + 2] * rs * vsc[ex[4 * i + 2]], sc[4 * i + 3] * rs * vsc[ex[4 * i + 3]]};
;             }
	v_lshrrev_b32_e32 v11, 9, v15
	v_and_or_b32 v19, v11, s3, v22
	s_waitcnt vmcnt(1)
	v_lshrrev_b32_e32 v11, 9, v17
	v_and_or_b32 v20, v11, s3, v32
	s_waitcnt vmcnt(0)
	v_lshrrev_b32_e32 v11, 9, v21
	v_and_or_b32 v21, v11, s3, v34
	ds_write_b128 v154, v[18:21] offset:32
	v_lshl_add_u64 v[14:15], s[6:7], 0, v[24:25]
	v_lshl_add_u64 v[22:23], s[6:7], 0, v[30:31]
	v_lshl_add_u64 v[18:19], s[6:7], 0, v[26:27]
	v_lshl_add_u64 v[20:21], s[6:7], 0, v[28:29]
	global_load_dword v24, v[14:15], off
	global_load_dword v26, v[20:21], off
	global_load_dword v27, v[22:23], off
	global_load_dword v25, v[18:19], off
	v_lshrrev_b32_e32 v11, 2, v45
	v_lshrrev_b32_e32 v15, 2, v46
	v_lshrrev_b32_e32 v18, 2, v47
	v_lshrrev_b32_e32 v20, 2, v48
	v_and_b32_e32 v11, 60, v11
	v_and_b32_e32 v14, 15, v45
	v_and_b32_e32 v15, 60, v15
	v_and_b32_e32 v17, 15, v46
	v_and_b32_e32 v18, 60, v18
	v_and_b32_e32 v19, 15, v47
	v_and_b32_e32 v20, 60, v20
	v_add_u32_e32 v11, v16, v11
	v_lshl_add_u32 v14, v14, 2, v16
	v_add_u32_e32 v15, v16, v15
	v_lshl_add_u32 v17, v17, 2, v16
	v_add_u32_e32 v18, v16, v18
	v_lshl_add_u32 v19, v19, 2, v16
	v_add_u32_e32 v20, v16, v20
	v_and_b32_e32 v21, 15, v48
	v_lshl_add_u32 v16, v21, 2, v16
	ds_read_b32 v11, v11
	ds_read_b32 v14, v14 offset:64
	ds_read_b32 v15, v15
	ds_read_b32 v17, v17 offset:64
	ds_read_b32 v18, v18
	ds_read_b32 v19, v19 offset:64
	ds_read_b32 v20, v20
	ds_read_b32 v21, v16 offset:64
	s_waitcnt lgkmcnt(6)
	v_lshl_add_u32 v14, v11, 7, v14
	s_waitcnt lgkmcnt(4)
	v_lshl_add_u32 v16, v15, 7, v17
	s_waitcnt lgkmcnt(2)
	v_lshl_add_u32 v18, v18, 7, v19
	v_pk_mul_f32 v[6:7], v[6:7], v[10:11] op_sel_hi:[1,0]
	v_pk_mul_f32 v[8:9], v[8:9], v[10:11] op_sel_hi:[1,0]
	v_ashrrev_i32_e32 v15, 31, v14
	v_ashrrev_i32_e32 v19, 31, v18
	s_waitcnt lgkmcnt(0)
	v_lshl_add_u32 v20, v20, 7, v21
	v_lshlrev_b64 v[22:23], 2, v[14:15]
	v_ashrrev_i32_e32 v17, 31, v16
	v_ashrrev_i32_e32 v21, 31, v20
	s_waitcnt vmcnt(1)
	v_pk_mul_f32 v[8:9], v[8:9], v[26:27]
	s_waitcnt vmcnt(0)
	v_pk_mul_f32 v[6:7], v[6:7], v[24:25]
	v_lshlrev_b64 v[26:27], 2, v[18:19]
	ds_write_b128 v154, v[6:9] offset:96
	v_lshlrev_b64 v[24:25], 2, v[16:17]
	v_lshl_add_u64 v[28:29], s[8:9], 0, v[26:27]
	v_lshl_add_u64 v[6:7], s[8:9], 0, v[22:23]
	v_lshl_add_u64 v[8:9], s[8:9], 0, v[24:25]
	global_load_dword v11, v[6:7], off
	global_load_dword v15, v[8:9], off
	global_load_dword v17, v[28:29], off
	v_lshlrev_b64 v[28:29], 2, v[20:21]
	v_lshl_add_u64 v[6:7], s[8:9], 0, v[28:29]
	global_load_dword v9, v[6:7], off
	s_waitcnt vmcnt(3)
	v_lshrrev_b32_e32 v6, 9, v11
	s_waitcnt vmcnt(2)
	v_lshrrev_b32_e32 v7, 9, v15
	s_waitcnt vmcnt(1)
	v_lshrrev_b32_e32 v8, 9, v17
	v_and_or_b32 v6, v6, s3, v14
	v_and_or_b32 v7, v7, s3, v16
	s_waitcnt vmcnt(0)
	v_lshrrev_b32_e32 v9, 9, v9
	v_and_or_b32 v8, v8, s3, v18
	v_and_or_b32 v9, v9, s3, v20
	ds_write_b128 v154, v[6:9] offset:48
	v_lshl_add_u64 v[0:1], s[6:7], 0, v[22:23]
	v_lshl_add_u64 v[14:15], s[6:7], 0, v[28:29]
	v_lshl_add_u64 v[6:7], s[6:7], 0, v[24:25]
	v_lshl_add_u64 v[8:9], s[6:7], 0, v[26:27]
	global_load_dword v16, v[0:1], off
	global_load_dword v18, v[8:9], off
	global_load_dword v19, v[14:15], off
	global_load_dword v17, v[6:7], off
	v_pk_mul_f32 v[0:1], v[2:3], v[10:11] op_sel_hi:[1,0]
	v_pk_mul_f32 v[2:3], v[4:5], v[10:11] op_sel_hi:[1,0]
	s_waitcnt vmcnt(0)
	v_pk_mul_f32 v[0:1], v[0:1], v[16:17]
	v_pk_mul_f32 v[2:3], v[2:3], v[18:19]
	ds_write_b128 v154, v[0:3] offset:112
	s_waitcnt lgkmcnt(0)
	ds_read_b128 v[156:159], v154
	ds_read_b128 v[160:163], v154 offset:16
	ds_read_b128 v[164:167], v154 offset:32
	ds_read_b128 v[168:171], v154 offset:48
	ds_read_b128 v[172:175], v154 offset:64
	ds_read_b128 v[176:179], v154 offset:80
	ds_read_b128 v[180:183], v154 offset:96
	ds_read_b128 v[184:187], v154 offset:112
	s_waitcnt lgkmcnt(0)
	global_store_dwordx4 v[152:153], v[156:159], off
	global_store_dwordx4 v[152:153], v[160:163], off offset:16
	global_store_dwordx4 v[152:153], v[164:167], off offset:32
	global_store_dwordx4 v[152:153], v[168:171], off offset:48
	global_store_dwordx4 v[12:13], v[172:175], off
	global_store_dwordx4 v[12:13], v[176:179], off offset:16
	global_store_dwordx4 v[12:13], v[180:183], off offset:32
	global_store_dwordx4 v[12:13], v[184:187], off offset:48

;     __device__ __forceinline__ void fused(f32x4 (&acc)[2][2][4][2], const Unit& u, int wr, int wc, int fr, int fq, PG8_LAS unsigned char* lds, int wid, int lane) const {
;     ...
;             for (int m = 0; m < 4; ++m) { const int r = ai * HALF + wr * 64 + m * 16 + fr; const size_t off = (size_t)(u.pm * BM + r) * ldc + col0;
; #pragma unroll
;                 for (int bj = 0; bj < 2; ++bj)
; #pragma unroll
;                     for (int n = 0; n < 2; ++n) { const u32x2v bw = __builtin_nontemporal_load((const u32x2v*)(base + off + bj * HALF + n * 16));
;                         const f32x4 bs = (f32x4){__uint_as_float(bw.x << 16), __uint_as_float(bw.x & 0xffff0000u), __uint_as_float(bw.y << 16), __uint_as_float(bw.y & 0xffff0000u)}; acc[ai][bj][m][n] = bs * alpha + acc[ai][bj][m][n]; }
;                 asm volatile("" : "+v"(acc[ai][0][m][0]), "+v"(acc[ai][0][m][1]), "+v"(acc[ai][1][m][0]), "+v"(acc[ai][1][m][1]));
;                 if (m == 3) asm volatile("" ::: "memory"); }
.LBB0_1448:
	s_add_u32 s6, s10, 0x2000000
	s_addc_u32 s7, s11, 0
	v_bfe_u32 v167, v144, 4, 2
	s_lshl_b32 s29, s16, 8
	v_lshlrev_b32_e32 v128, 2, v167
	s_add_i32 s4, s29, s57
	s_lshl_b32 s28, s8, 8
	v_lshl_or_b32 v163, s17, 5, v128
	v_or_b32_e32 v130, s4, v145
	v_or_b32_e32 v128, s28, v163
	v_ashrrev_i32_e32 v131, 31, v130
	v_ashrrev_i32_e32 v129, 31, v128
	v_lshlrev_b64 v[132:133], 11, v[130:131]
	v_lshl_add_u64 v[134:135], s[6:7], 0, v[132:133]
	v_lshlrev_b64 v[132:133], 1, v[128:129]
	v_lshl_add_u64 v[134:135], v[134:135], 0, v[132:133]
	s_barrier
	global_load_dwordx2 v[170:171], v[134:135], off nt
	global_load_dwordx2 v[172:173], v[134:135], off offset:32 nt
	global_load_dwordx2 v[174:175], v[134:135], off offset:256 nt
	global_load_dwordx2 v[176:177], v[134:135], off offset:288 nt
	v_add_u32_e32 v234, 0x10, v130
	v_mov_b32_e32 v235, 0
	v_lshlrev_b64 v[234:235], 11, v[234:235]
	v_lshl_add_u64 v[234:235], s[6:7], 0, v[234:235]
	v_lshl_add_u64 v[234:235], v[234:235], 0, v[132:133]
	s_nop 1
	global_load_dwordx2 v[178:179], v[234:235], off nt
	global_load_dwordx2 v[180:181], v[234:235], off offset:32 nt
	global_load_dwordx2 v[182:183], v[234:235], off offset:256 nt
	global_load_dwordx2 v[184:185], v[234:235], off offset:288 nt
	v_add_u32_e32 v234, 0x20, v130
	v_mov_b32_e32 v235, 0
	v_lshlrev_b64 v[234:235], 11, v[234:235]
	v_lshl_add_u64 v[234:235], s[6:7], 0, v[234:235]
	v_lshl_add_u64 v[234:235], v[234:235], 0, v[132:133]
	s_nop 1
	global_load_dwordx2 v[186:187], v[234:235], off nt
	global_load_dwordx2 v[188:189], v[234:235], off offset:32 nt
	global_load_dwordx2 v[190:191], v[234:235], off offset:256 nt
	global_load_dwordx2 v[192:193], v[234:235], off offset:288 nt
	v_add_u32_e32 v234, 0x30, v130
	v_mov_b32_e32 v235, 0
	v_lshlrev_b64 v[234:235], 11, v[234:235]
	v_lshl_add_u64 v[234:235], s[6:7], 0, v[234:235]
	v_lshl_add_u64 v[234:235], v[234:235], 0, v[132:133]
	s_nop 1
	global_load_dwordx2 v[194:195], v[234:235], off nt
	global_load_dwordx2 v[196:197], v[234:235], off offset:32 nt
	global_load_dwordx2 v[198:199], v[234:235], off offset:256 nt
	global_load_dwordx2 v[200:201], v[234:235], off offset:288 nt
	v_add_u32_e32 v234, 0x80, v130
	v_mov_b32_e32 v235, 0
	v_lshlrev_b64 v[234:235], 11, v[234:235]
	v_lshl_add_u64 v[234:235], s[6:7], 0, v[234:235]
	v_lshl_add_u64 v[234:235], v[234:235], 0, v[132:133]
	s_nop 1
	global_load_dwordx2 v[202:203], v[234:235], off nt
	global_load_dwordx2 v[204:205], v[234:235], off offset:32 nt
	global_load_dwordx2 v[206:207], v[234:235], off offset:256 nt
	global_load_dwordx2 v[208:209], v[234:235], off offset:288 nt
	v_add_u32_e32 v234, 0x90, v130
	v_mov_b32_e32 v235, 0
	v_lshlrev_b64 v[234:235], 11, v[234:235]
	v_lshl_add_u64 v[234:235], s[6:7], 0, v[234:235]
	v_lshl_add_u64 v[234:235], v[234:235], 0, v[132:133]
	s_nop 1
	global_load_dwordx2 v[210:211], v[234:235], off nt
	global_load_dwordx2 v[212:213], v[234:235], off offset:32 nt
	global_load_dwordx2 v[214:215], v[234:235], off offset:256 nt
	global_load_dwordx2 v[216:217], v[234:235], off offset:288 nt
	v_add_u32_e32 v234, 0xa0, v130
	v_mov_b32_e32 v235, 0
	v_lshlrev_b64 v[234:235], 11, v[234:235]
	v_lshl_add_u64 v[234:235], s[6:7], 0, v[234:235]
	v_lshl_add_u64 v[234:235], v[234:235], 0, v[132:133]
	s_nop 1
	global_load_dwordx2 v[218:219], v[234:235], off nt
	global_load_dwordx2 v[220:221], v[234:235], off offset:32 nt
	global_load_dwordx2 v[222:223], v[234:235], off offset:256 nt
	global_load_dwordx2 v[224:225], v[234:235], off offset:288 nt
	v_add_u32_e32 v234, 0xb0, v130
	v_mov_b32_e32 v235, 0
	v_lshlrev_b64 v[234:235], 11, v[234:235]
	v_lshl_add_u64 v[234:235], s[6:7], 0, v[234:235]
	v_lshl_add_u64 v[234:235], v[234:235], 0, v[132:133]
	s_nop 1
	global_load_dwordx2 v[226:227], v[234:235], off nt
	global_load_dwordx2 v[228:229], v[234:235], off offset:32 nt
	global_load_dwordx2 v[230:231], v[234:235], off offset:256 nt
	global_load_dwordx2 v[232:233], v[234:235], off offset:288 nt
	s_nop 0
	v_or_b32_e32 v142, 16, v130
	v_ashrrev_i32_e32 v143, 31, v142
	v_lshlrev_b64 v[142:143], 11, v[142:143]
	s_mov_b32 s4, 0x3fb504f3
	v_lshl_add_u64 v[142:143], s[6:7], 0, v[142:143]
	v_lshl_add_u64 v[142:143], v[142:143], 0, v[132:133]
	v_xor_b32_e32 v131, 16, v165
	v_and_b32_e32 v168, 63, v144
	s_waitcnt vmcnt(28)
	v_mov_b32_e32 v136, v170
	v_mov_b32_e32 v137, v171
	v_mov_b32_e32 v138, v172
	v_mov_b32_e32 v139, v173
	v_mov_b32_e32 v140, v174
	v_mov_b32_e32 v141, v175
	v_mov_b32_e32 v134, v176
	v_mov_b32_e32 v135, v177
	v_lshlrev_b32_e32 v146, 16, v136
	v_and_b32_e32 v147, 0xffff0000, v136
	v_lshlrev_b32_e32 v136, 16, v137
	v_and_b32_e32 v137, 0xffff0000, v137
	v_lshlrev_b32_e32 v148, 16, v138
	v_and_b32_e32 v149, 0xffff0000, v138
	v_lshlrev_b32_e32 v138, 16, v139
	v_and_b32_e32 v139, 0xffff0000, v139
	v_lshlrev_b32_e32 v150, 16, v140
	v_and_b32_e32 v151, 0xffff0000, v140
	v_lshlrev_b32_e32 v140, 16, v141
	v_and_b32_e32 v141, 0xffff0000, v141
	v_lshlrev_b32_e32 v154, 16, v134
	v_and_b32_e32 v155, 0xffff0000, v134
	v_lshlrev_b32_e32 v134, 16, v135
	v_and_b32_e32 v135, 0xffff0000, v135
	v_pk_fma_f32 v[126:127], v[136:137], s[4:5], v[126:127] op_sel_hi:[1,0,1]
	v_pk_fma_f32 v[124:125], v[146:147], s[4:5], v[124:125] op_sel_hi:[1,0,1]
	v_pk_fma_f32 v[122:123], v[138:139], s[4:5], v[122:123] op_sel_hi:[1,0,1]
	v_pk_fma_f32 v[120:121], v[148:149], s[4:5], v[120:121] op_sel_hi:[1,0,1]
	v_pk_fma_f32 v[114:115], v[140:141], s[4:5], v[114:115] op_sel_hi:[1,0,1]
	v_pk_fma_f32 v[112:113], v[150:151], s[4:5], v[112:113] op_sel_hi:[1,0,1]
	v_pk_fma_f32 v[102:103], v[134:135], s[4:5], v[102:103] op_sel_hi:[1,0,1]
	v_pk_fma_f32 v[100:101], v[154:155], s[4:5], v[100:101] op_sel_hi:[1,0,1]
	s_nop 0
	v_or_b32_e32 v142, 32, v130
	v_ashrrev_i32_e32 v143, 31, v142
	v_lshlrev_b64 v[142:143], 11, v[142:143]
	v_lshl_add_u64 v[142:143], s[6:7], 0, v[142:143]
	v_lshl_add_u64 v[142:143], v[142:143], 0, v[132:133]
	s_waitcnt vmcnt(24)
;     __device__ __forceinline__ void fused(f32x4 (&acc)[2][2][4][2], const Unit& u, int wr, int wc, int fr, int fq, PG8_LAS unsigned char* lds, int wid, int lane) const {
;     ...
;             for (int m = 0; m < 4; ++m) { const int r = ai * HALF + wr * 64 + m * 16 + fr; const size_t off = (size_t)(u.pm * BM + r) * ldc + col0;
; #pragma unroll
;                 for (int bj = 0; bj < 2; ++bj)
; #pragma unroll
;                     for (int n = 0; n < 2; ++n) { const u32x2v bw = __builtin_nontemporal_load((const u32x2v*)(base + off + bj * HALF + n * 16));
;                         const f32x4 bs = (f32x4){__uint_as_float(bw.x << 16), __uint_as_float(bw.x & 0xffff0000u), __uint_as_float(bw.y << 16), __uint_as_float(bw.y & 0xffff0000u)}; acc[ai][bj][m][n] = bs * alpha + acc[ai][bj][m][n]; }
;                 asm volatile("" : "+v"(acc[ai][0][m][0]), "+v"(acc[ai][0][m][1]), "+v"(acc[ai][1][m][0]), "+v"(acc[ai][1][m][1]));
;                 if (m == 3) asm volatile("" ::: "memory"); }
	v_mov_b32_e32 v134, v178
	v_mov_b32_e32 v135, v179
	v_mov_b32_e32 v136, v180
	v_mov_b32_e32 v137, v181
	v_mov_b32_e32 v138, v182
	v_mov_b32_e32 v139, v183
	v_mov_b32_e32 v140, v184
	v_mov_b32_e32 v141, v185
	v_lshlrev_b32_e32 v146, 16, v134
	v_and_b32_e32 v147, 0xffff0000, v134
	v_lshlrev_b32_e32 v134, 16, v135
	v_and_b32_e32 v135, 0xffff0000, v135
	v_lshlrev_b32_e32 v148, 16, v136
	v_and_b32_e32 v149, 0xffff0000, v136
	v_lshlrev_b32_e32 v136, 16, v137
	v_and_b32_e32 v137, 0xffff0000, v137
	v_lshlrev_b32_e32 v150, 16, v138
	v_and_b32_e32 v151, 0xffff0000, v138
	v_lshlrev_b32_e32 v138, 16, v139
	v_and_b32_e32 v139, 0xffff0000, v139
	v_lshlrev_b32_e32 v154, 16, v140
	v_and_b32_e32 v155, 0xffff0000, v140
	v_lshlrev_b32_e32 v140, 16, v141
	v_and_b32_e32 v141, 0xffff0000, v141
	v_pk_fma_f32 v[118:119], v[134:135], s[4:5], v[118:119] op_sel_hi:[1,0,1]
	v_pk_fma_f32 v[116:117], v[146:147], s[4:5], v[116:117] op_sel_hi:[1,0,1]
	v_pk_fma_f32 v[106:107], v[136:137], s[4:5], v[106:107] op_sel_hi:[1,0,1]
	v_pk_fma_f32 v[104:105], v[148:149], s[4:5], v[104:105] op_sel_hi:[1,0,1]
	v_pk_fma_f32 v[90:91], v[138:139], s[4:5], v[90:91] op_sel_hi:[1,0,1]
	v_pk_fma_f32 v[88:89], v[150:151], s[4:5], v[88:89] op_sel_hi:[1,0,1]
	v_pk_fma_f32 v[78:79], v[140:141], s[4:5], v[78:79] op_sel_hi:[1,0,1]
	v_pk_fma_f32 v[76:77], v[154:155], s[4:5], v[76:77] op_sel_hi:[1,0,1]
	s_nop 0
	v_or_b32_e32 v142, 48, v130
	v_ashrrev_i32_e32 v143, 31, v142
	v_lshlrev_b64 v[142:143], 11, v[142:143]
	v_lshl_add_u64 v[142:143], s[6:7], 0, v[142:143]
	v_lshl_add_u64 v[142:143], v[142:143], 0, v[132:133]
	s_waitcnt vmcnt(20)
	v_mov_b32_e32 v134, v186
	v_mov_b32_e32 v135, v187
	v_mov_b32_e32 v136, v188
	v_mov_b32_e32 v137, v189
	v_mov_b32_e32 v138, v190
	v_mov_b32_e32 v139, v191
	v_mov_b32_e32 v140, v192
	v_mov_b32_e32 v141, v193
	v_lshlrev_b32_e32 v146, 16, v134
	v_and_b32_e32 v147, 0xffff0000, v134
	v_lshlrev_b32_e32 v134, 16, v135
	v_and_b32_e32 v135, 0xffff0000, v135
	v_lshlrev_b32_e32 v148, 16, v136
	v_and_b32_e32 v149, 0xffff0000, v136
	v_lshlrev_b32_e32 v136, 16, v137
	v_and_b32_e32 v137, 0xffff0000, v137
	v_lshlrev_b32_e32 v150, 16, v138
	v_and_b32_e32 v151, 0xffff0000, v138
	v_lshlrev_b32_e32 v138, 16, v139
	v_and_b32_e32 v139, 0xffff0000, v139
	v_lshlrev_b32_e32 v154, 16, v140
	v_and_b32_e32 v155, 0xffff0000, v140
	v_lshlrev_b32_e32 v140, 16, v141
	v_and_b32_e32 v141, 0xffff0000, v141
	v_pk_fma_f32 v[110:111], v[134:135], s[4:5], v[110:111] op_sel_hi:[1,0,1]
	v_pk_fma_f32 v[108:109], v[146:147], s[4:5], v[108:109] op_sel_hi:[1,0,1]
	v_pk_fma_f32 v[94:95], v[136:137], s[4:5], v[94:95] op_sel_hi:[1,0,1]
	v_pk_fma_f32 v[92:93], v[148:149], s[4:5], v[92:93] op_sel_hi:[1,0,1]
	v_pk_fma_f32 v[82:83], v[138:139], s[4:5], v[82:83] op_sel_hi:[1,0,1]
	v_pk_fma_f32 v[80:81], v[150:151], s[4:5], v[80:81] op_sel_hi:[1,0,1]
	v_pk_fma_f32 v[70:71], v[140:141], s[4:5], v[70:71] op_sel_hi:[1,0,1]
	v_pk_fma_f32 v[68:69], v[154:155], s[4:5], v[68:69] op_sel_hi:[1,0,1]
	s_nop 0
	v_add_u32_e32 v142, 0x80, v130
	v_ashrrev_i32_e32 v143, 31, v142
	v_lshlrev_b64 v[142:143], 11, v[142:143]
	v_lshl_add_u64 v[142:143], s[6:7], 0, v[142:143]
	v_lshl_add_u64 v[142:143], v[142:143], 0, v[132:133]
	s_waitcnt vmcnt(16)
	v_mov_b32_e32 v134, v194
	v_mov_b32_e32 v135, v195
	v_mov_b32_e32 v136, v196
	v_mov_b32_e32 v137, v197
	v_mov_b32_e32 v138, v198
	v_mov_b32_e32 v139, v199
	v_mov_b32_e32 v140, v200
	v_mov_b32_e32 v141, v201
	v_lshlrev_b32_e32 v146, 16, v134
	v_and_b32_e32 v147, 0xffff0000, v134
	v_lshlrev_b32_e32 v134, 16, v135
	v_and_b32_e32 v135, 0xffff0000, v135
	v_lshlrev_b32_e32 v148, 16, v136
	v_and_b32_e32 v149, 0xffff0000, v136
	v_lshlrev_b32_e32 v136, 16, v137
	v_and_b32_e32 v137, 0xffff0000, v137
	v_lshlrev_b32_e32 v150, 16, v138
	v_and_b32_e32 v151, 0xffff0000, v138
	v_lshlrev_b32_e32 v138, 16, v139
	v_and_b32_e32 v139, 0xffff0000, v139
	v_lshlrev_b32_e32 v154, 16, v140
	v_and_b32_e32 v155, 0xffff0000, v140
	v_lshlrev_b32_e32 v140, 16, v141
	v_and_b32_e32 v141, 0xffff0000, v141
	v_pk_fma_f32 v[98:99], v[134:135], s[4:5], v[98:99] op_sel_hi:[1,0,1]
	v_pk_fma_f32 v[96:97], v[146:147], s[4:5], v[96:97] op_sel_hi:[1,0,1]
	v_pk_fma_f32 v[86:87], v[136:137], s[4:5], v[86:87] op_sel_hi:[1,0,1]
	v_pk_fma_f32 v[84:85], v[148:149], s[4:5], v[84:85] op_sel_hi:[1,0,1]
	v_pk_fma_f32 v[74:75], v[138:139], s[4:5], v[74:75] op_sel_hi:[1,0,1]
	v_pk_fma_f32 v[72:73], v[150:151], s[4:5], v[72:73] op_sel_hi:[1,0,1]
	v_pk_fma_f32 v[66:67], v[140:141], s[4:5], v[66:67] op_sel_hi:[1,0,1]
	v_pk_fma_f32 v[64:65], v[154:155], s[4:5], v[64:65] op_sel_hi:[1,0,1]
	s_nop 0
	v_add_u32_e32 v142, 0x90, v130
	v_ashrrev_i32_e32 v143, 31, v142
	v_lshlrev_b64 v[142:143], 11, v[142:143]
	v_lshl_add_u64 v[142:143], s[6:7], 0, v[142:143]
	v_lshl_add_u64 v[142:143], v[142:143], 0, v[132:133]
	s_waitcnt vmcnt(12)
	v_mov_b32_e32 v134, v202
	v_mov_b32_e32 v135, v203
	v_mov_b32_e32 v136, v204
	v_mov_b32_e32 v137, v205
	v_mov_b32_e32 v138, v206
	v_mov_b32_e32 v139, v207
	v_mov_b32_e32 v140, v208
	v_mov_b32_e32 v141, v209
	v_lshlrev_b32_e32 v146, 16, v134
	v_and_b32_e32 v147, 0xffff0000, v134
	v_lshlrev_b32_e32 v134, 16, v135
	v_and_b32_e32 v135, 0xffff0000, v135
	v_lshlrev_b32_e32 v148, 16, v136
	v_and_b32_e32 v149, 0xffff0000, v136
	v_lshlrev_b32_e32 v136, 16, v137
	v_and_b32_e32 v137, 0xffff0000, v137
	v_lshlrev_b32_e32 v150, 16, v138
	v_and_b32_e32 v151, 0xffff0000, v138
	v_lshlrev_b32_e32 v138, 16, v139
	v_and_b32_e32 v139, 0xffff0000, v139
	v_lshlrev_b32_e32 v154, 16, v140
	v_and_b32_e32 v155, 0xffff0000, v140
	v_lshlrev_b32_e32 v140, 16, v141
	v_and_b32_e32 v141, 0xffff0000, v141
	v_pk_fma_f32 v[62:63], v[134:135], s[4:5], v[62:63] op_sel_hi:[1,0,1]
	v_pk_fma_f32 v[60:61], v[146:147], s[4:5], v[60:61] op_sel_hi:[1,0,1]
	v_pk_fma_f32 v[54:55], v[136:137], s[4:5], v[54:55] op_sel_hi:[1,0,1]
	v_pk_fma_f32 v[52:53], v[148:149], s[4:5], v[52:53] op_sel_hi:[1,0,1]
	v_pk_fma_f32 v[46:47], v[138:139], s[4:5], v[46:47] op_sel_hi:[1,0,1]
	v_pk_fma_f32 v[44:45], v[150:151], s[4:5], v[44:45] op_sel_hi:[1,0,1]
	v_pk_fma_f32 v[38:39], v[140:141], s[4:5], v[38:39] op_sel_hi:[1,0,1]
	v_pk_fma_f32 v[36:37], v[154:155], s[4:5], v[36:37] op_sel_hi:[1,0,1]
	s_nop 0
	v_add_u32_e32 v142, 0xa0, v130
	v_ashrrev_i32_e32 v143, 31, v142
	v_lshlrev_b64 v[142:143], 11, v[142:143]
	v_lshl_add_u64 v[142:143], s[6:7], 0, v[142:143]
	v_lshl_add_u64 v[142:143], v[142:143], 0, v[132:133]
	s_waitcnt vmcnt(8)
;     __device__ __forceinline__ bool run(const f32x4 (&v)[2][2][4][2], const Unit& u, int wr, int wc, int fr, int fq, PG8_LAS unsigned char* lds, int wid, int lane) const {
;     ...
;                 float s = 0.f;
; #pragma unroll
;                 for (int bj = 0; bj < 2; ++bj)
; #pragma unroll
;                     for (int n = 0; n < 2; ++n) { const f32x4 x = v[ai][bj][m][n]; s += (x[0] + x[1]) + (x[2] + x[3]); }
;                 s += __shfl_xor(s, 16); s += __shfl_xor(s, 32);
;     __device__ __forceinline__ void fused(f32x4 (&acc)[2][2][4][2], const Unit& u, int wr, int wc, int fr, int fq, PG8_LAS unsigned char* lds, int wid, int lane) const {
;     ...
;             for (int m = 0; m < 4; ++m) { const int r = ai * HALF + wr * 64 + m * 16 + fr; const size_t off = (size_t)(u.pm * BM + r) * ldc + col0;
; #pragma unroll
;                 for (int bj = 0; bj < 2; ++bj)
; #pragma unroll
;                     for (int n = 0; n < 2; ++n) { const u32x2v bw = __builtin_nontemporal_load((const u32x2v*)(base + off + bj * HALF + n * 16));
;                         const f32x4 bs = (f32x4){__uint_as_float(bw.x << 16), __uint_as_float(bw.x & 0xffff0000u), __uint_as_float(bw.y << 16), __uint_as_float(bw.y & 0xffff0000u)}; acc[ai][bj][m][n] = bs * alpha + acc[ai][bj][m][n]; }
;                 asm volatile("" : "+v"(acc[ai][0][m][0]), "+v"(acc[ai][0][m][1]), "+v"(acc[ai][1][m][0]), "+v"(acc[ai][1][m][1]));
;                 if (m == 3) asm volatile("" ::: "memory"); }
	v_mov_b32_e32 v134, v210
	v_mov_b32_e32 v135, v211
	v_mov_b32_e32 v136, v212
	v_mov_b32_e32 v137, v213
	v_mov_b32_e32 v138, v214
	v_mov_b32_e32 v139, v215
	v_mov_b32_e32 v140, v216
	v_mov_b32_e32 v141, v217
	v_lshlrev_b32_e32 v146, 16, v134
	v_and_b32_e32 v147, 0xffff0000, v134
	v_lshlrev_b32_e32 v134, 16, v135
	v_and_b32_e32 v135, 0xffff0000, v135
	v_lshlrev_b32_e32 v148, 16, v136
	v_and_b32_e32 v149, 0xffff0000, v136
	v_lshlrev_b32_e32 v136, 16, v137
	v_and_b32_e32 v137, 0xffff0000, v137
	v_lshlrev_b32_e32 v150, 16, v138
	v_and_b32_e32 v151, 0xffff0000, v138
	v_lshlrev_b32_e32 v138, 16, v139
	v_and_b32_e32 v139, 0xffff0000, v139
	v_lshlrev_b32_e32 v154, 16, v140
	v_and_b32_e32 v155, 0xffff0000, v140
	v_lshlrev_b32_e32 v140, 16, v141
	v_and_b32_e32 v141, 0xffff0000, v141
	v_pk_fma_f32 v[58:59], v[134:135], s[4:5], v[58:59] op_sel_hi:[1,0,1]
	v_pk_fma_f32 v[56:57], v[146:147], s[4:5], v[56:57] op_sel_hi:[1,0,1]
	v_pk_fma_f32 v[50:51], v[136:137], s[4:5], v[50:51] op_sel_hi:[1,0,1]
	v_pk_fma_f32 v[48:49], v[148:149], s[4:5], v[48:49] op_sel_hi:[1,0,1]
	v_pk_fma_f32 v[42:43], v[138:139], s[4:5], v[42:43] op_sel_hi:[1,0,1]
	v_pk_fma_f32 v[40:41], v[150:151], s[4:5], v[40:41] op_sel_hi:[1,0,1]
	v_pk_fma_f32 v[34:35], v[140:141], s[4:5], v[34:35] op_sel_hi:[1,0,1]
	v_pk_fma_f32 v[32:33], v[154:155], s[4:5], v[32:33] op_sel_hi:[1,0,1]
	v_mov_b32_e32 v146, v124
	v_and_b32_e32 v142, 64, v165
	v_add_u32_e32 v153, 64, v142
	v_add_u32_e32 v142, 0xb0, v130
	v_ashrrev_i32_e32 v143, 31, v142
	v_lshlrev_b64 v[142:143], 11, v[142:143]
	v_lshl_add_u64 v[142:143], s[6:7], 0, v[142:143]
	v_lshl_add_u64 v[132:133], v[142:143], 0, v[132:133]
	v_mov_b32_e32 v142, v125
	v_mov_b32_e32 v143, v126
	v_mov_b32_e32 v147, v127
	v_pk_add_f32 v[142:143], v[142:143], v[146:147]
	v_mov_b32_e32 v148, v121
	v_mov_b32_e32 v149, v122
	v_add_f32_e32 v130, v142, v143
	v_cmp_lt_i32_e32 vcc, v131, v153
	s_waitcnt vmcnt(4)
	v_mov_b32_e32 v134, v218
	v_mov_b32_e32 v135, v219
	v_mov_b32_e32 v136, v220
	v_mov_b32_e32 v137, v221
	v_mov_b32_e32 v138, v222
	v_mov_b32_e32 v139, v223
	v_mov_b32_e32 v140, v224
	v_mov_b32_e32 v141, v225
	v_lshlrev_b32_e32 v150, 16, v134
	v_and_b32_e32 v151, 0xffff0000, v134
	v_lshlrev_b32_e32 v134, 16, v135
	v_and_b32_e32 v135, 0xffff0000, v135
	v_lshlrev_b32_e32 v154, 16, v136
	v_and_b32_e32 v155, 0xffff0000, v136
	v_lshlrev_b32_e32 v136, 16, v137
	v_and_b32_e32 v137, 0xffff0000, v137
	v_lshlrev_b32_e32 v156, 16, v138
	v_and_b32_e32 v157, 0xffff0000, v138
	v_lshlrev_b32_e32 v138, 16, v139
	v_and_b32_e32 v139, 0xffff0000, v139
	v_lshlrev_b32_e32 v158, 16, v140
	v_and_b32_e32 v159, 0xffff0000, v140
	v_lshlrev_b32_e32 v140, 16, v141
	v_and_b32_e32 v141, 0xffff0000, v141
	v_pk_fma_f32 v[30:31], v[134:135], s[4:5], v[30:31] op_sel_hi:[1,0,1]
	v_pk_fma_f32 v[28:29], v[150:151], s[4:5], v[28:29] op_sel_hi:[1,0,1]
	v_pk_fma_f32 v[26:27], v[136:137], s[4:5], v[26:27] op_sel_hi:[1,0,1]
	v_pk_fma_f32 v[24:25], v[154:155], s[4:5], v[24:25] op_sel_hi:[1,0,1]
	v_pk_fma_f32 v[22:23], v[138:139], s[4:5], v[22:23] op_sel_hi:[1,0,1]
	v_pk_fma_f32 v[20:21], v[156:157], s[4:5], v[20:21] op_sel_hi:[1,0,1]
	v_pk_fma_f32 v[18:19], v[140:141], s[4:5], v[18:19] op_sel_hi:[1,0,1]
	v_pk_fma_f32 v[16:17], v[158:159], s[4:5], v[16:17] op_sel_hi:[1,0,1]
	v_mov_b32_e32 v134, v120
	v_mov_b32_e32 v135, v123
	v_pk_add_f32 v[132:133], v[148:149], v[134:135]
	v_add_f32_e32 v141, v112, v113
	v_pk_add_f32 v[132:133], v[132:133], v[132:133] op_sel_hi:[0,1]
	v_add_f32_e32 v151, v114, v115
	v_mov_b32_e32 v140, v100
	v_mov_b32_e32 v150, v101
	v_mov_b32_e32 v156, v103
	v_add_f32_e32 v157, 0, v130
	v_mov_b32_e32 v132, v102
	v_pk_add_f32 v[134:135], v[140:141], v[150:151]
	v_pk_add_f32 v[132:133], v[132:133], v[156:157]
	v_cndmask_b32_e32 v131, v165, v131, vcc
	v_pk_add_f32 v[132:133], v[134:135], v[132:133]
	v_lshlrev_b32_e32 v131, 2, v131
	v_add_f32_e32 v132, v132, v133
	ds_bpermute_b32 v133, v131, v132
	v_xor_b32_e32 v130, 32, v165
	v_cmp_lt_i32_e32 vcc, v130, v153
	s_waitcnt lgkmcnt(0)
;     __device__ __forceinline__ bool run(const f32x4 (&v)[2][2][4][2], const Unit& u, int wr, int wc, int fr, int fq, PG8_LAS unsigned char* lds, int wid, int lane) const {
;     ...
;                 s += __shfl_xor(s, 16); s += __shfl_xor(s, 32);
;                 const float mw = s * (1.0f / 64.0f); float q = 0.f;
; #pragma unroll
;                 for (int bj = 0; bj < 2; ++bj)
; #pragma unroll
;                     for (int n = 0; n < 2; ++n) { const f32x4 d = v[ai][bj][m][n] - mw; q += (d[0] * d[0] + d[1] * d[1]) + (d[2] * d[2] + d[3] * d[3]); }
;                 q += __shfl_xor(q, 16); q += __shfl_xor(q, 32);
;                 if (fq == 0) P[(ai * HALF + wr * 64 + m * 16 + fr) * 4 + wc] = (f32x2v){mw, q};
;     __device__ __forceinline__ void fused(f32x4 (&acc)[2][2][4][2], const Unit& u, int wr, int wc, int fr, int fq, PG8_LAS unsigned char* lds, int wid, int lane) const {
;     ...
;             for (int m = 0; m < 4; ++m) { const int r = ai * HALF + wr * 64 + m * 16 + fr; const size_t off = (size_t)(u.pm * BM + r) * ldc + col0;
; #pragma unroll
;                 for (int bj = 0; bj < 2; ++bj)
; #pragma unroll
;                     for (int n = 0; n < 2; ++n) { const u32x2v bw = __builtin_nontemporal_load((const u32x2v*)(base + off + bj * HALF + n * 16));
;                         const f32x4 bs = (f32x4){__uint_as_float(bw.x << 16), __uint_as_float(bw.x & 0xffff0000u), __uint_as_float(bw.y << 16), __uint_as_float(bw.y & 0xffff0000u)}; acc[ai][bj][m][n] = bs * alpha + acc[ai][bj][m][n]; }
;                 asm volatile("" : "+v"(acc[ai][0][m][0]), "+v"(acc[ai][0][m][1]), "+v"(acc[ai][1][m][0]), "+v"(acc[ai][1][m][1]));
;                 if (m == 3) asm volatile("" ::: "memory"); }
	v_add_f32_e32 v132, v132, v133
	v_cndmask_b32_e32 v130, v165, v130, vcc
	v_lshlrev_b32_e32 v130, 2, v130
	ds_bpermute_b32 v133, v130, v132
	v_cmp_gt_u32_e32 vcc, 16, v168
	s_waitcnt lgkmcnt(0)
	v_add_f32_e32 v132, v132, v133
	v_fmamk_f32 v134, v132, 0xbc800000, v127
	v_fmamk_f32 v140, v132, 0xbc800000, v125
	v_fmamk_f32 v142, v132, 0xbc800000, v123
	v_fmamk_f32 v148, v132, 0xbc800000, v121
	v_fmamk_f32 v133, v132, 0xbc800000, v126
	v_fmamk_f32 v135, v132, 0xbc800000, v124
	v_fmamk_f32 v141, v132, 0xbc800000, v122
	v_fmamk_f32 v143, v132, 0xbc800000, v120
	v_fmamk_f32 v150, v132, 0xbc800000, v115
	v_fmamk_f32 v153, v132, 0xbc800000, v113
	v_mul_f32_e32 v140, v140, v140
	v_mul_f32_e32 v134, v134, v134
	v_mul_f32_e32 v148, v148, v148
	v_mul_f32_e32 v142, v142, v142
	v_fmamk_f32 v149, v132, 0xbc800000, v114
	v_fmamk_f32 v151, v132, 0xbc800000, v112
	v_fmamk_f32 v157, v132, 0xbc800000, v103
	v_fmamk_f32 v159, v132, 0xbc800000, v101
	v_mul_f32_e32 v153, v153, v153
	v_mul_f32_e32 v150, v150, v150
	v_fmac_f32_e32 v140, v135, v135
	v_fmac_f32_e32 v134, v133, v133
	v_fmac_f32_e32 v148, v143, v143
	v_fmac_f32_e32 v142, v141, v141
	v_fmamk_f32 v156, v132, 0xbc800000, v102
	v_fmamk_f32 v158, v132, 0xbc800000, v100
	v_mul_f32_e32 v159, v159, v159
	v_mul_f32_e32 v157, v157, v157
	v_fmac_f32_e32 v153, v151, v151
	v_fmac_f32_e32 v150, v149, v149
	v_add_f32_e32 v133, v140, v134
	v_add_f32_e32 v134, v148, v142
	v_fmac_f32_e32 v159, v158, v158
	v_fmac_f32_e32 v157, v156, v156
	v_add_f32_e32 v135, v153, v150
	v_add_f32_e32 v133, v133, v134
	v_add_f32_e32 v140, v159, v157
	v_add_f32_e32 v133, v135, v133
	v_add_f32_e32 v133, v140, v133
	ds_bpermute_b32 v134, v131, v133
	s_waitcnt lgkmcnt(0)
	v_add_f32_e32 v133, v133, v134
	ds_bpermute_b32 v134, v130, v133
	s_waitcnt vmcnt(0)
	v_mov_b32_e32 v136, v226
	v_mov_b32_e32 v137, v227
	v_mov_b32_e32 v138, v228
	v_mov_b32_e32 v139, v229
	v_mov_b32_e32 v154, v230
	v_mov_b32_e32 v155, v231
	v_mov_b32_e32 v146, v232
	v_mov_b32_e32 v147, v233
	v_lshlrev_b32_e32 v140, 16, v136
	v_and_b32_e32 v141, 0xffff0000, v136
	v_lshlrev_b32_e32 v136, 16, v137
	v_and_b32_e32 v137, 0xffff0000, v137
	v_lshlrev_b32_e32 v142, 16, v138
	v_and_b32_e32 v143, 0xffff0000, v138
	v_lshlrev_b32_e32 v138, 16, v139
	v_and_b32_e32 v139, 0xffff0000, v139
	v_lshlrev_b32_e32 v148, 16, v154
	v_and_b32_e32 v149, 0xffff0000, v154
	v_lshlrev_b32_e32 v150, 16, v155
	v_and_b32_e32 v151, 0xffff0000, v155
	v_lshlrev_b32_e32 v154, 16, v146
	v_and_b32_e32 v155, 0xffff0000, v146
	v_lshlrev_b32_e32 v146, 16, v147
	v_and_b32_e32 v147, 0xffff0000, v147
	v_pk_fma_f32 v[14:15], v[136:137], s[4:5], v[14:15] op_sel_hi:[1,0,1]
	v_pk_fma_f32 v[12:13], v[140:141], s[4:5], v[12:13] op_sel_hi:[1,0,1]
	v_pk_fma_f32 v[10:11], v[138:139], s[4:5], v[10:11] op_sel_hi:[1,0,1]
	v_pk_fma_f32 v[8:9], v[142:143], s[4:5], v[8:9] op_sel_hi:[1,0,1]
	v_pk_fma_f32 v[6:7], v[150:151], s[4:5], v[6:7] op_sel_hi:[1,0,1]
	v_pk_fma_f32 v[4:5], v[148:149], s[4:5], v[4:5] op_sel_hi:[1,0,1]
	v_pk_fma_f32 v[2:3], v[146:147], s[4:5], v[2:3] op_sel_hi:[1,0,1]
	v_pk_fma_f32 v[0:1], v[154:155], s[4:5], v[0:1] op_sel_hi:[1,0,1]
	s_lshl_b32 s4, s17, 3
	s_add_i32 s6, s4, 0
	s_and_saveexec_b64 s[4:5], vcc
	s_cbranch_execz .LBB0_1450
	s_lshl_b32 s7, s9, 11
	s_add_i32 s7, s6, s7
	v_mul_f32_e32 v132, 0x3c800000, v132
	s_waitcnt lgkmcnt(0)
	v_add_f32_e32 v133, v133, v134
	v_lshl_add_u32 v134, v145, 5, s7
	ds_write_b64 v134, v[132:133]
